# tail conversion v4 + static s_setprio for waves 4-7 in attention phases + GEMM K-loop LDS-DMA rebalanced 4/4/4/4 per SP
# speedup vs baseline: 1.0321x; 1.0052x over previous
.LBB0_189:
	s_ashr_i32 s11, s10, 31
	s_lshl_b64 s[14:15], s[10:11], 18
	s_add_u32 s14, s35, s14
	s_addc_u32 s15, s36, s15
	s_and_b64 s[18:19], s[16:17], exec
	ds_read_b128 v[0:3], v130
	ds_read_b128 v[4:7], v130 offset:1024
	ds_read_b128 v[8:11], v130 offset:2048
	ds_read_b128 v[12:15], v130 offset:3072
	ds_read_b128 v[16:19], v131
	ds_read_b128 v[20:23], v131 offset:1024
	ds_read_b128 v[24:27], v131 offset:2048
	ds_read_b128 v[28:31], v131 offset:3072
	s_cselect_b32 s5, s15, s25
	s_cselect_b32 s11, s14, s24
	s_ashr_i32 s13, s12, 31
	s_lshl_b64 s[18:19], s[12:13], 18
	s_add_u32 s18, s33, s18
	s_addc_u32 s19, s34, s19
	s_and_b64 s[26:27], s[16:17], exec
	s_cselect_b32 s13, s19, s23
	s_cselect_b32 s57, s18, s22
	s_add_u32 s26, s24, 0x100
	s_addc_u32 s27, s25, 0
	s_add_u32 s28, s24, 0x180
	s_addc_u32 s29, s25, 0
	s_add_u32 s30, s22, 0x100
	s_addc_u32 s31, s23, 0
	ds_read_b128 v[32:35], v132
	ds_read_b128 v[36:39], v132 offset:1024
	ds_read_b128 v[40:43], v132 offset:2048
	ds_read_b128 v[44:47], v132 offset:3072
	ds_read_b128 v[48:51], v132 offset:4096
	ds_read_b128 v[52:55], v132 offset:5120
	ds_read_b128 v[56:59], v132 offset:6144
	ds_read_b128 v[60:63], v132 offset:7168
	s_add_u32 s58, s24, 0x20080
	s_addc_u32 s59, s25, 0
	s_mov_b32 s60, m0
	s_mov_b32 m0, s53
	s_nop 0
	global_load_lds_dwordx4 v129, s[58:59]
	s_mov_b32 m0, s60
	s_add_u32 s58, s24, 0x30080
	s_addc_u32 s59, s25, 0
	s_mov_b32 s60, m0
	s_mov_b32 m0, s54
	s_nop 0
	global_load_lds_dwordx4 v129, s[58:59]
	s_mov_b32 m0, s60
	s_waitcnt vmcnt(8)
	s_waitcnt lgkmcnt(0)
	s_barrier
	s_setprio 1
	s_waitcnt lgkmcnt(6)
	v_mfma_scale_f32_16x16x128_f8f6f4 v[64:67], v[0:7], v[32:39], 0, v133, v133 op_sel_hi:[0,0,0]
	v_mfma_scale_f32_16x16x128_f8f6f4 v[68:71], v[8:15], v[32:39], 0, v133, v133 op_sel_hi:[0,0,0]
	s_waitcnt lgkmcnt(4)
	v_mfma_scale_f32_16x16x128_f8f6f4 v[72:75], v[0:7], v[40:47], 0, v133, v133 op_sel_hi:[0,0,0]
	v_mfma_scale_f32_16x16x128_f8f6f4 v[76:79], v[8:15], v[40:47], 0, v133, v133 op_sel_hi:[0,0,0]
	s_waitcnt lgkmcnt(2)
	v_mfma_scale_f32_16x16x128_f8f6f4 v[80:83], v[0:7], v[48:55], 0, v133, v133 op_sel_hi:[0,0,0]
	v_mfma_scale_f32_16x16x128_f8f6f4 v[84:87], v[8:15], v[48:55], 0, v133, v133 op_sel_hi:[0,0,0]
	s_waitcnt lgkmcnt(0)
	v_mfma_scale_f32_16x16x128_f8f6f4 v[88:91], v[0:7], v[56:63], 0, v133, v133 op_sel_hi:[0,0,0]
	v_mfma_scale_f32_16x16x128_f8f6f4 v[92:95], v[8:15], v[56:63], 0, v133, v133 op_sel_hi:[0,0,0]
	s_setprio 0
	s_setprio 1
	v_mfma_scale_f32_16x16x128_f8f6f4 v[104:107], v[16:23], v[32:39], 0, v133, v133 op_sel_hi:[0,0,0]
	v_mfma_scale_f32_16x16x128_f8f6f4 v[108:111], v[24:31], v[32:39], 0, v133, v133 op_sel_hi:[0,0,0]
	v_mfma_scale_f32_16x16x128_f8f6f4 v[154:157], v[16:23], v[40:47], 0, v133, v133 op_sel_hi:[0,0,0]
	v_mfma_scale_f32_16x16x128_f8f6f4 v[158:161], v[24:31], v[40:47], 0, v133, v133 op_sel_hi:[0,0,0]
	v_mfma_scale_f32_16x16x128_f8f6f4 v[162:165], v[16:23], v[48:55], 0, v133, v133 op_sel_hi:[0,0,0]
	v_mfma_scale_f32_16x16x128_f8f6f4 v[166:169], v[24:31], v[48:55], 0, v133, v133 op_sel_hi:[0,0,0]
	v_mfma_scale_f32_16x16x128_f8f6f4 v[170:173], v[16:23], v[56:63], 0, v133, v133 op_sel_hi:[0,0,0]
	v_mfma_scale_f32_16x16x128_f8f6f4 v[174:177], v[24:31], v[56:63], 0, v133, v133 op_sel_hi:[0,0,0]
	s_setprio 0
	s_barrier
	ds_read_b128 v[32:35], v132 offset:16384
	ds_read_b128 v[36:39], v132 offset:17408
	ds_read_b128 v[40:43], v132 offset:18432
	ds_read_b128 v[44:47], v132 offset:19456
	ds_read_b128 v[48:51], v132 offset:20480
	ds_read_b128 v[52:55], v132 offset:21504
	ds_read_b128 v[56:59], v132 offset:22528
	ds_read_b128 v[60:63], v132 offset:23552
	s_mov_b32 s58, m0
	s_mov_b32 m0, s21
	s_nop 0
	global_load_lds_dwordx4 v129, s[30:31]
	s_mov_b32 m0, s58
	s_add_u32 s30, s22, 0x10100
	s_addc_u32 s31, s23, 0
	s_mov_b32 s58, m0
	s_mov_b32 m0, s38
	s_nop 0
	global_load_lds_dwordx4 v129, s[30:31]
	s_mov_b32 m0, s58
	s_add_u32 s30, s22, 0x20100
	s_addc_u32 s31, s23, 0
	s_mov_b32 s58, m0
	s_mov_b32 m0, s39
	s_nop 0
	global_load_lds_dwordx4 v129, s[30:31]
	s_mov_b32 m0, s58
	s_add_u32 s30, s22, 0x30100
	s_addc_u32 s31, s23, 0
	s_mov_b32 s58, m0
	s_mov_b32 m0, s40
	s_nop 0
	global_load_lds_dwordx4 v129, s[30:31]
	s_mov_b32 m0, s58
	s_waitcnt vmcnt(6)
	s_waitcnt lgkmcnt(0)
	s_barrier
	s_setprio 1
	s_waitcnt lgkmcnt(6)
	v_mfma_scale_f32_16x16x128_f8f6f4 v[186:189], v[0:7], v[32:39], 0, v133, v133 op_sel_hi:[0,0,0]
	v_mfma_scale_f32_16x16x128_f8f6f4 v[190:193], v[8:15], v[32:39], 0, v133, v133 op_sel_hi:[0,0,0]
	s_waitcnt lgkmcnt(4)
	v_mfma_scale_f32_16x16x128_f8f6f4 v[194:197], v[0:7], v[40:47], 0, v133, v133 op_sel_hi:[0,0,0]
	v_mfma_scale_f32_16x16x128_f8f6f4 v[198:201], v[8:15], v[40:47], 0, v133, v133 op_sel_hi:[0,0,0]
	s_waitcnt lgkmcnt(2)
	v_mfma_scale_f32_16x16x128_f8f6f4 v[202:205], v[0:7], v[48:55], 0, v133, v133 op_sel_hi:[0,0,0]
	v_mfma_scale_f32_16x16x128_f8f6f4 v[206:209], v[8:15], v[48:55], 0, v133, v133 op_sel_hi:[0,0,0]
	s_waitcnt lgkmcnt(0)
	v_mfma_scale_f32_16x16x128_f8f6f4 v[210:213], v[0:7], v[56:63], 0, v133, v133 op_sel_hi:[0,0,0]
	v_mfma_scale_f32_16x16x128_f8f6f4 v[214:217], v[8:15], v[56:63], 0, v133, v133 op_sel_hi:[0,0,0]
	s_setprio 0
	s_setprio 1
	v_mfma_scale_f32_16x16x128_f8f6f4 v[218:221], v[16:23], v[32:39], 0, v133, v133 op_sel_hi:[0,0,0]
	v_mfma_scale_f32_16x16x128_f8f6f4 v[222:225], v[24:31], v[32:39], 0, v133, v133 op_sel_hi:[0,0,0]
	v_mfma_scale_f32_16x16x128_f8f6f4 v[226:229], v[16:23], v[40:47], 0, v133, v133 op_sel_hi:[0,0,0]
	v_mfma_scale_f32_16x16x128_f8f6f4 v[230:233], v[24:31], v[40:47], 0, v133, v133 op_sel_hi:[0,0,0]
	v_mfma_scale_f32_16x16x128_f8f6f4 v[234:237], v[16:23], v[48:55], 0, v133, v133 op_sel_hi:[0,0,0]
	v_mfma_scale_f32_16x16x128_f8f6f4 v[238:241], v[24:31], v[48:55], 0, v133, v133 op_sel_hi:[0,0,0]
	v_mfma_scale_f32_16x16x128_f8f6f4 v[242:245], v[16:23], v[56:63], 0, v133, v133 op_sel_hi:[0,0,0]
	v_mfma_scale_f32_16x16x128_f8f6f4 v[246:249], v[24:31], v[56:63], 0, v133, v133 op_sel_hi:[0,0,0]
	s_setprio 0
	s_barrier
	ds_read_b128 v[0:3], v134
	ds_read_b128 v[4:7], v134 offset:1024
	ds_read_b128 v[12:15], v134 offset:2048
	ds_read_b128 v[16:19], v134 offset:3072
	ds_read_b128 v[138:141], v135
	ds_read_b128 v[142:145], v135 offset:1024
	ds_read_b128 v[146:149], v135 offset:2048
	ds_read_b128 v[150:153], v135 offset:3072
	ds_read_b128 v[20:23], v132 offset:32768
	ds_read_b128 v[24:27], v132 offset:33792
	ds_read_b128 v[28:31], v132 offset:34816
	ds_read_b128 v[32:35], v132 offset:35840
	ds_read_b128 v[36:39], v132 offset:36864
	ds_read_b128 v[40:43], v132 offset:37888
	ds_read_b128 v[44:47], v132 offset:38912
	ds_read_b128 v[48:51], v132 offset:39936
	s_mov_b32 s30, m0
	s_mov_b32 m0, s37
	s_nop 0
	global_load_lds_dwordx4 v129, s[26:27]
	s_mov_b32 m0, s30
	s_add_u32 s30, s24, 0x10100
	s_addc_u32 s31, s25, 0
	s_mov_b32 s58, m0
	s_mov_b32 m0, s41
	s_nop 0
	global_load_lds_dwordx4 v129, s[30:31]
	s_mov_b32 m0, s58
	s_add_u32 s30, s24, 0x20100
	s_addc_u32 s31, s25, 0
	s_mov_b32 s58, m0
	s_mov_b32 m0, s42
	s_nop 0
	global_load_lds_dwordx4 v129, s[30:31]
	s_mov_b32 m0, s58
	s_add_u32 s30, s24, 0x30100
	s_addc_u32 s31, s25, 0
	s_mov_b32 s58, m0
	s_mov_b32 m0, s43
	s_nop 0
	global_load_lds_dwordx4 v129, s[30:31]
	s_mov_b32 m0, s58
	s_waitcnt vmcnt(8)
	s_waitcnt lgkmcnt(0)
	s_barrier
	s_setprio 1
	s_waitcnt lgkmcnt(6)
	v_mfma_scale_f32_16x16x128_f8f6f4 v[112:115], v[0:7], v[20:27], v[64:67], v133, v133 op_sel_hi:[0,0,0]
	v_mfma_scale_f32_16x16x128_f8f6f4 v[116:119], v[12:19], v[20:27], v[68:71], v133, v133 op_sel_hi:[0,0,0]
	s_waitcnt lgkmcnt(4)
	v_mfma_scale_f32_16x16x128_f8f6f4 v[96:99], v[0:7], v[28:35], v[72:75], v133, v133 op_sel_hi:[0,0,0]
	v_mfma_scale_f32_16x16x128_f8f6f4 v[100:103], v[12:19], v[28:35], v[76:79], v133, v133 op_sel_hi:[0,0,0]
	s_waitcnt lgkmcnt(2)
	v_mfma_scale_f32_16x16x128_f8f6f4 v[80:83], v[0:7], v[36:43], v[80:83], v133, v133 op_sel_hi:[0,0,0]
	v_mfma_scale_f32_16x16x128_f8f6f4 v[84:87], v[12:19], v[36:43], v[84:87], v133, v133 op_sel_hi:[0,0,0]
	s_waitcnt lgkmcnt(0)
	v_mfma_scale_f32_16x16x128_f8f6f4 v[64:67], v[0:7], v[44:51], v[88:91], v133, v133 op_sel_hi:[0,0,0]
	v_mfma_scale_f32_16x16x128_f8f6f4 v[72:75], v[12:19], v[44:51], v[92:95], v133, v133 op_sel_hi:[0,0,0]
	s_setprio 0
	s_setprio 1
	v_mfma_scale_f32_16x16x128_f8f6f4 v[120:123], v[138:145], v[20:27], v[104:107], v133, v133 op_sel_hi:[0,0,0]
	v_mfma_scale_f32_16x16x128_f8f6f4 v[124:127], v[146:153], v[20:27], v[108:111], v133, v133 op_sel_hi:[0,0,0]
	v_mfma_scale_f32_16x16x128_f8f6f4 v[104:107], v[138:145], v[28:35], v[154:157], v133, v133 op_sel_hi:[0,0,0]
	v_mfma_scale_f32_16x16x128_f8f6f4 v[108:111], v[146:153], v[28:35], v[158:161], v133, v133 op_sel_hi:[0,0,0]
	v_mfma_scale_f32_16x16x128_f8f6f4 v[88:91], v[138:145], v[36:43], v[162:165], v133, v133 op_sel_hi:[0,0,0]
	v_mfma_scale_f32_16x16x128_f8f6f4 v[92:95], v[146:153], v[36:43], v[166:169], v133, v133 op_sel_hi:[0,0,0]
	v_mfma_scale_f32_16x16x128_f8f6f4 v[68:71], v[138:145], v[44:51], v[170:173], v133, v133 op_sel_hi:[0,0,0]
	v_mfma_scale_f32_16x16x128_f8f6f4 v[76:79], v[146:153], v[44:51], v[174:177], v133, v133 op_sel_hi:[0,0,0]
	s_setprio 0
	s_barrier
	s_add_u32 s30, s22, 0x180
	s_addc_u32 s31, s23, 0
	ds_read_b128 v[154:157], v132 offset:49152
	ds_read_b128 v[158:161], v132 offset:50176
	ds_read_b128 v[162:165], v132 offset:51200
	ds_read_b128 v[166:169], v132 offset:52224
	ds_read_b128 v[170:173], v132 offset:53248
	ds_read_b128 v[174:177], v132 offset:54272
	ds_read_b128 v[178:181], v132 offset:55296
	ds_read_b128 v[182:185], v132 offset:56320
	s_mov_b32 s58, m0
	s_mov_b32 m0, s47
	s_nop 0
	global_load_lds_dwordx4 v129, s[30:31]
	s_mov_b32 m0, s58
	s_add_u32 s30, s22, 0x10180
	s_addc_u32 s31, s23, 0
	s_mov_b32 s58, m0
	s_mov_b32 m0, s48
	s_nop 0
	global_load_lds_dwordx4 v129, s[30:31]
	s_mov_b32 m0, s58
	s_add_u32 s30, s22, 0x20180
	s_addc_u32 s31, s23, 0
	s_mov_b32 s58, m0
	s_mov_b32 m0, s51
	s_nop 0
	global_load_lds_dwordx4 v129, s[30:31]
	s_mov_b32 m0, s58
	s_add_u32 s30, s22, 0x30180
	s_addc_u32 s31, s23, 0
	s_mov_b32 s58, m0
	s_mov_b32 m0, s52
	s_nop 0
	global_load_lds_dwordx4 v129, s[30:31]
	s_mov_b32 m0, s58
	s_mov_b32 s30, m0
	s_mov_b32 m0, s49
	s_nop 0
	global_load_lds_dwordx4 v129, s[28:29]
	s_mov_b32 m0, s30
	s_add_u32 s24, s24, 0x10180
	s_addc_u32 s25, s25, 0
	s_mov_b32 s28, m0
	s_mov_b32 m0, s50
	s_nop 0
	global_load_lds_dwordx4 v129, s[24:25]
	s_mov_b32 m0, s28
	s_waitcnt vmcnt(8)
	s_waitcnt lgkmcnt(0)
	s_barrier
	s_setprio 1
	s_waitcnt lgkmcnt(6)
	v_mfma_scale_f32_16x16x128_f8f6f4 v[48:51], v[0:7], v[154:161], v[186:189], v133, v133 op_sel_hi:[0,0,0]
	v_mfma_scale_f32_16x16x128_f8f6f4 v[52:55], v[12:19], v[154:161], v[190:193], v133, v133 op_sel_hi:[0,0,0]
	s_waitcnt lgkmcnt(4)
	v_mfma_scale_f32_16x16x128_f8f6f4 v[32:35], v[0:7], v[162:169], v[194:197], v133, v133 op_sel_hi:[0,0,0]
	v_mfma_scale_f32_16x16x128_f8f6f4 v[40:43], v[12:19], v[162:169], v[198:201], v133, v133 op_sel_hi:[0,0,0]
	s_waitcnt lgkmcnt(2)
	v_mfma_scale_f32_16x16x128_f8f6f4 v[24:27], v[0:7], v[170:177], v[202:205], v133, v133 op_sel_hi:[0,0,0]
	v_mfma_scale_f32_16x16x128_f8f6f4 v[28:31], v[12:19], v[170:177], v[206:209], v133, v133 op_sel_hi:[0,0,0]
	s_waitcnt lgkmcnt(0)
	v_mfma_scale_f32_16x16x128_f8f6f4 v[8:11], v[0:7], v[178:185], v[210:213], v133, v133 op_sel_hi:[0,0,0]
	v_mfma_scale_f32_16x16x128_f8f6f4 v[12:15], v[12:19], v[178:185], v[214:217], v133, v133 op_sel_hi:[0,0,0]
	s_setprio 0
	s_setprio 1
	v_mfma_scale_f32_16x16x128_f8f6f4 v[56:59], v[138:145], v[154:161], v[218:221], v133, v133 op_sel_hi:[0,0,0]
	v_mfma_scale_f32_16x16x128_f8f6f4 v[60:63], v[146:153], v[154:161], v[222:225], v133, v133 op_sel_hi:[0,0,0]
	v_mfma_scale_f32_16x16x128_f8f6f4 v[36:39], v[138:145], v[162:169], v[226:229], v133, v133 op_sel_hi:[0,0,0]
	v_mfma_scale_f32_16x16x128_f8f6f4 v[44:47], v[146:153], v[162:169], v[230:233], v133, v133 op_sel_hi:[0,0,0]
	v_mfma_scale_f32_16x16x128_f8f6f4 v[16:19], v[138:145], v[170:177], v[234:237], v133, v133 op_sel_hi:[0,0,0]
	v_mfma_scale_f32_16x16x128_f8f6f4 v[20:23], v[146:153], v[170:177], v[238:241], v133, v133 op_sel_hi:[0,0,0]
	v_mfma_scale_f32_16x16x128_f8f6f4 v[0:3], v[138:145], v[178:185], v[242:245], v133, v133 op_sel_hi:[0,0,0]
	v_mfma_scale_f32_16x16x128_f8f6f4 v[4:7], v[146:153], v[178:185], v[246:249], v133, v133 op_sel_hi:[0,0,0]
	s_setprio 0
	s_barrier
	s_add_u32 s58, s22, 0x200
	s_addc_u32 s59, s23, 0
	s_mov_b32 s60, 0
.LBB0_190:
	ds_read_b128 v[138:141], v130
	ds_read_b128 v[142:145], v130 offset:1024
	ds_read_b128 v[146:149], v130 offset:2048
	ds_read_b128 v[150:153], v130 offset:3072
	ds_read_b128 v[154:157], v131
	ds_read_b128 v[158:161], v131 offset:1024
	ds_read_b128 v[162:165], v131 offset:2048
	ds_read_b128 v[166:169], v131 offset:3072
	s_add_u32 s22, s26, 0x100
	s_addc_u32 s23, s27, 0
	s_cmp_eq_u32 s60, 4
	s_cselect_b32 s24, s11, s22
	s_cselect_b32 s25, s5, s23
	s_cselect_b32 s30, s57, s58
	s_cselect_b32 s31, s13, s59
	s_add_u32 s28, s24, 0x80
	s_addc_u32 s29, s25, 0
	ds_read_b128 v[170:173], v132
	ds_read_b128 v[174:177], v132 offset:1024
	ds_read_b128 v[178:181], v132 offset:2048
	ds_read_b128 v[182:185], v132 offset:3072
	ds_read_b128 v[186:189], v132 offset:4096
	ds_read_b128 v[190:193], v132 offset:5120
	ds_read_b128 v[194:197], v132 offset:6144
	ds_read_b128 v[198:201], v132 offset:7168
	s_add_u32 s62, s26, 0x20080
	s_addc_u32 s63, s27, 0
	s_mov_b32 s61, m0
	s_mov_b32 m0, s53
	s_nop 0
	global_load_lds_dwordx4 v129, s[62:63]
	s_mov_b32 m0, s61
	s_add_u32 s26, s26, 0x30080
	s_addc_u32 s27, s27, 0
	s_mov_b32 s61, m0
	s_mov_b32 m0, s54
	s_nop 0
	global_load_lds_dwordx4 v129, s[26:27]
	s_mov_b32 m0, s61
	s_waitcnt vmcnt(8)
	s_waitcnt lgkmcnt(0)
	s_barrier
	s_setprio 1
	s_waitcnt lgkmcnt(6)
	v_mfma_scale_f32_16x16x128_f8f6f4 v[112:115], v[138:145], v[170:177], v[112:115], v133, v133 op_sel_hi:[0,0,0]
	v_mfma_scale_f32_16x16x128_f8f6f4 v[116:119], v[146:153], v[170:177], v[116:119], v133, v133 op_sel_hi:[0,0,0]
	s_waitcnt lgkmcnt(4)
	v_mfma_scale_f32_16x16x128_f8f6f4 v[96:99], v[138:145], v[178:185], v[96:99], v133, v133 op_sel_hi:[0,0,0]
	v_mfma_scale_f32_16x16x128_f8f6f4 v[100:103], v[146:153], v[178:185], v[100:103], v133, v133 op_sel_hi:[0,0,0]
	s_waitcnt lgkmcnt(2)
	v_mfma_scale_f32_16x16x128_f8f6f4 v[202:205], v[138:145], v[186:193], v[80:83], v133, v133 op_sel_hi:[0,0,0]
	v_mfma_scale_f32_16x16x128_f8f6f4 v[206:209], v[146:153], v[186:193], v[84:87], v133, v133 op_sel_hi:[0,0,0]
	s_waitcnt lgkmcnt(0)
	v_mfma_scale_f32_16x16x128_f8f6f4 v[210:213], v[138:145], v[194:201], v[64:67], v133, v133 op_sel_hi:[0,0,0]
	v_mfma_scale_f32_16x16x128_f8f6f4 v[214:217], v[146:153], v[194:201], v[72:75], v133, v133 op_sel_hi:[0,0,0]
	s_setprio 0
	s_setprio 1
	v_mfma_scale_f32_16x16x128_f8f6f4 v[120:123], v[154:161], v[170:177], v[120:123], v133, v133 op_sel_hi:[0,0,0]
	v_mfma_scale_f32_16x16x128_f8f6f4 v[124:127], v[162:169], v[170:177], v[124:127], v133, v133 op_sel_hi:[0,0,0]
	v_mfma_scale_f32_16x16x128_f8f6f4 v[104:107], v[154:161], v[178:185], v[104:107], v133, v133 op_sel_hi:[0,0,0]
	v_mfma_scale_f32_16x16x128_f8f6f4 v[108:111], v[162:169], v[178:185], v[108:111], v133, v133 op_sel_hi:[0,0,0]
	v_mfma_scale_f32_16x16x128_f8f6f4 v[170:173], v[154:161], v[186:193], v[88:91], v133, v133 op_sel_hi:[0,0,0]
	v_mfma_scale_f32_16x16x128_f8f6f4 v[174:177], v[162:169], v[186:193], v[92:95], v133, v133 op_sel_hi:[0,0,0]
	v_mfma_scale_f32_16x16x128_f8f6f4 v[178:181], v[154:161], v[194:201], v[68:71], v133, v133 op_sel_hi:[0,0,0]
	v_mfma_scale_f32_16x16x128_f8f6f4 v[182:185], v[162:169], v[194:201], v[76:79], v133, v133 op_sel_hi:[0,0,0]
	s_setprio 0
	s_barrier
	ds_read_b128 v[64:67], v132 offset:16384
	s_nop 2
	ds_read_b128 v[68:71], v132 offset:17408
	ds_read_b128 v[72:75], v132 offset:18432
	ds_read_b128 v[76:79], v132 offset:19456
	ds_read_b128 v[80:83], v132 offset:20480
	ds_read_b128 v[84:87], v132 offset:21504
	ds_read_b128 v[88:91], v132 offset:22528
	ds_read_b128 v[92:95], v132 offset:23552
	s_mov_b32 s26, m0
	s_mov_b32 m0, s21
	s_nop 0
	global_load_lds_dwordx4 v129, s[30:31]
	s_mov_b32 m0, s26
	s_add_u32 s26, s30, 0x10000
	s_addc_u32 s27, s31, 0
	s_mov_b32 s61, m0
	s_mov_b32 m0, s38
	s_nop 0
	global_load_lds_dwordx4 v129, s[26:27]
	s_mov_b32 m0, s61
	s_add_u32 s26, s30, 0x20000
	s_addc_u32 s27, s31, 0
	s_mov_b32 s61, m0
	s_mov_b32 m0, s39
	s_nop 0
	global_load_lds_dwordx4 v129, s[26:27]
	s_mov_b32 m0, s61
	s_add_u32 s26, s30, 0x30000
	s_addc_u32 s27, s31, 0
	s_mov_b32 s61, m0
	s_mov_b32 m0, s40
	s_nop 0
	global_load_lds_dwordx4 v129, s[26:27]
	s_mov_b32 m0, s61
	s_waitcnt vmcnt(6)
	s_waitcnt lgkmcnt(0)
	s_barrier
	s_setprio 1
	s_waitcnt lgkmcnt(6)
	v_mfma_scale_f32_16x16x128_f8f6f4 v[52:55], v[146:153], v[64:71], v[52:55], v133, v133 op_sel_hi:[0,0,0]
	s_waitcnt lgkmcnt(0)
	v_mfma_scale_f32_16x16x128_f8f6f4 v[8:11], v[138:145], v[88:95], v[8:11], v133, v133 op_sel_hi:[0,0,0]
	v_mfma_scale_f32_16x16x128_f8f6f4 v[186:189], v[138:145], v[64:71], v[48:51], v133, v133 op_sel_hi:[0,0,0]
	v_mfma_scale_f32_16x16x128_f8f6f4 v[190:193], v[138:145], v[72:79], v[32:35], v133, v133 op_sel_hi:[0,0,0]
	v_mfma_scale_f32_16x16x128_f8f6f4 v[194:197], v[146:153], v[72:79], v[40:43], v133, v133 op_sel_hi:[0,0,0]
	v_mfma_scale_f32_16x16x128_f8f6f4 v[198:201], v[138:145], v[80:87], v[24:27], v133, v133 op_sel_hi:[0,0,0]
	v_mfma_scale_f32_16x16x128_f8f6f4 v[218:221], v[146:153], v[80:87], v[28:31], v133, v133 op_sel_hi:[0,0,0]
	v_mfma_scale_f32_16x16x128_f8f6f4 v[222:225], v[146:153], v[88:95], v[12:15], v133, v133 op_sel_hi:[0,0,0]
	s_setprio 0
	s_setprio 1
	v_mfma_scale_f32_16x16x128_f8f6f4 v[56:59], v[154:161], v[64:71], v[56:59], v133, v133 op_sel_hi:[0,0,0]
	v_mfma_scale_f32_16x16x128_f8f6f4 v[60:63], v[162:169], v[64:71], v[60:63], v133, v133 op_sel_hi:[0,0,0]
	v_mfma_scale_f32_16x16x128_f8f6f4 v[226:229], v[154:161], v[72:79], v[36:39], v133, v133 op_sel_hi:[0,0,0]
	v_mfma_scale_f32_16x16x128_f8f6f4 v[230:233], v[162:169], v[72:79], v[44:47], v133, v133 op_sel_hi:[0,0,0]
	v_mfma_scale_f32_16x16x128_f8f6f4 v[234:237], v[154:161], v[80:87], v[16:19], v133, v133 op_sel_hi:[0,0,0]
	v_mfma_scale_f32_16x16x128_f8f6f4 v[238:241], v[162:169], v[80:87], v[20:23], v133, v133 op_sel_hi:[0,0,0]
	v_mfma_scale_f32_16x16x128_f8f6f4 v[242:245], v[154:161], v[88:95], v[0:3], v133, v133 op_sel_hi:[0,0,0]
	v_mfma_scale_f32_16x16x128_f8f6f4 v[246:249], v[162:169], v[88:95], v[4:7], v133, v133 op_sel_hi:[0,0,0]
	s_setprio 0
	s_barrier
	s_nop 3
	ds_read_b128 v[0:3], v134
	ds_read_b128 v[4:7], v134 offset:1024
	ds_read_b128 v[12:15], v134 offset:2048
	ds_read_b128 v[16:19], v134 offset:3072
	ds_read_b128 v[138:141], v135
	ds_read_b128 v[142:145], v135 offset:1024
	ds_read_b128 v[146:149], v135 offset:2048
	ds_read_b128 v[150:153], v135 offset:3072
	ds_read_b128 v[20:23], v132 offset:32768
	ds_read_b128 v[24:27], v132 offset:33792
	ds_read_b128 v[28:31], v132 offset:34816
	ds_read_b128 v[32:35], v132 offset:35840
	ds_read_b128 v[36:39], v132 offset:36864
	ds_read_b128 v[40:43], v132 offset:37888
	ds_read_b128 v[44:47], v132 offset:38912
	ds_read_b128 v[48:51], v132 offset:39936
	s_mov_b32 s26, m0
	s_mov_b32 m0, s37
	s_nop 0
	global_load_lds_dwordx4 v129, s[24:25]
	s_mov_b32 m0, s26
	s_add_u32 s26, s24, 0x10000
	s_addc_u32 s27, s25, 0
	s_mov_b32 s61, m0
	s_mov_b32 m0, s41
	s_nop 0
	global_load_lds_dwordx4 v129, s[26:27]
	s_mov_b32 m0, s61
	s_add_u32 s26, s24, 0x20000
	s_addc_u32 s27, s25, 0
	s_mov_b32 s61, m0
	s_mov_b32 m0, s42
	s_nop 0
	global_load_lds_dwordx4 v129, s[26:27]
	s_mov_b32 m0, s61
	s_add_u32 s26, s24, 0x30000
	s_addc_u32 s27, s25, 0
	s_mov_b32 s61, m0
	s_mov_b32 m0, s43
	s_nop 0
	global_load_lds_dwordx4 v129, s[26:27]
	s_mov_b32 m0, s61
	s_waitcnt vmcnt(8)
	s_waitcnt lgkmcnt(0)
	s_barrier
	s_setprio 1
	s_waitcnt lgkmcnt(6)
	v_mfma_scale_f32_16x16x128_f8f6f4 v[112:115], v[0:7], v[20:27], v[112:115], v133, v133 op_sel_hi:[0,0,0]
	v_mfma_scale_f32_16x16x128_f8f6f4 v[116:119], v[12:19], v[20:27], v[116:119], v133, v133 op_sel_hi:[0,0,0]
	s_waitcnt lgkmcnt(4)
	v_mfma_scale_f32_16x16x128_f8f6f4 v[96:99], v[0:7], v[28:35], v[96:99], v133, v133 op_sel_hi:[0,0,0]
	v_mfma_scale_f32_16x16x128_f8f6f4 v[100:103], v[12:19], v[28:35], v[100:103], v133, v133 op_sel_hi:[0,0,0]
	s_waitcnt lgkmcnt(2)
	v_mfma_scale_f32_16x16x128_f8f6f4 v[80:83], v[0:7], v[36:43], v[202:205], v133, v133 op_sel_hi:[0,0,0]
	v_mfma_scale_f32_16x16x128_f8f6f4 v[84:87], v[12:19], v[36:43], v[206:209], v133, v133 op_sel_hi:[0,0,0]
	s_waitcnt lgkmcnt(0)
	v_mfma_scale_f32_16x16x128_f8f6f4 v[64:67], v[0:7], v[44:51], v[210:213], v133, v133 op_sel_hi:[0,0,0]
	v_mfma_scale_f32_16x16x128_f8f6f4 v[72:75], v[12:19], v[44:51], v[214:217], v133, v133 op_sel_hi:[0,0,0]
	s_setprio 0
	s_setprio 1
	v_mfma_scale_f32_16x16x128_f8f6f4 v[120:123], v[138:145], v[20:27], v[120:123], v133, v133 op_sel_hi:[0,0,0]
	v_mfma_scale_f32_16x16x128_f8f6f4 v[124:127], v[146:153], v[20:27], v[124:127], v133, v133 op_sel_hi:[0,0,0]
	v_mfma_scale_f32_16x16x128_f8f6f4 v[104:107], v[138:145], v[28:35], v[104:107], v133, v133 op_sel_hi:[0,0,0]
	v_mfma_scale_f32_16x16x128_f8f6f4 v[108:111], v[146:153], v[28:35], v[108:111], v133, v133 op_sel_hi:[0,0,0]
	v_mfma_scale_f32_16x16x128_f8f6f4 v[88:91], v[138:145], v[36:43], v[170:173], v133, v133 op_sel_hi:[0,0,0]
	v_mfma_scale_f32_16x16x128_f8f6f4 v[92:95], v[146:153], v[36:43], v[174:177], v133, v133 op_sel_hi:[0,0,0]
	v_mfma_scale_f32_16x16x128_f8f6f4 v[68:71], v[138:145], v[44:51], v[178:181], v133, v133 op_sel_hi:[0,0,0]
	v_mfma_scale_f32_16x16x128_f8f6f4 v[76:79], v[146:153], v[44:51], v[182:185], v133, v133 op_sel_hi:[0,0,0]
	s_setprio 0
	s_barrier
	s_add_u32 s26, s30, 0x80
	s_addc_u32 s27, s31, 0
	ds_read_b128 v[154:157], v132 offset:49152
	ds_read_b128 v[158:161], v132 offset:50176
	ds_read_b128 v[162:165], v132 offset:51200
	ds_read_b128 v[166:169], v132 offset:52224
	ds_read_b128 v[170:173], v132 offset:53248
	ds_read_b128 v[174:177], v132 offset:54272
	ds_read_b128 v[178:181], v132 offset:55296
	ds_read_b128 v[182:185], v132 offset:56320
	s_mov_b32 s61, m0
	s_mov_b32 m0, s47
	s_nop 0
	global_load_lds_dwordx4 v129, s[26:27]
	s_mov_b32 m0, s61
	s_add_u32 s26, s30, 0x10080
	s_addc_u32 s27, s31, 0
	s_mov_b32 s61, m0
	s_mov_b32 m0, s48
	s_nop 0
	global_load_lds_dwordx4 v129, s[26:27]
	s_mov_b32 m0, s61
	s_add_u32 s26, s30, 0x20080
	s_addc_u32 s27, s31, 0
	s_mov_b32 s61, m0
	s_mov_b32 m0, s51
	s_nop 0
	global_load_lds_dwordx4 v129, s[26:27]
	s_mov_b32 m0, s61
	s_add_u32 s26, s30, 0x30080
	s_addc_u32 s27, s31, 0
	s_mov_b32 s30, m0
	s_mov_b32 m0, s52
	s_nop 0
	global_load_lds_dwordx4 v129, s[26:27]
	s_mov_b32 m0, s30
	s_mov_b32 s26, m0
	s_mov_b32 m0, s49
	s_nop 0
	global_load_lds_dwordx4 v129, s[28:29]
	s_mov_b32 m0, s26
	s_add_u32 s24, s24, 0x10080
	s_addc_u32 s25, s25, 0
	s_mov_b32 s26, m0
	s_mov_b32 m0, s50
	s_nop 0
	global_load_lds_dwordx4 v129, s[24:25]
	s_mov_b32 m0, s26
	s_waitcnt vmcnt(8)
	s_waitcnt lgkmcnt(0)
	s_barrier
	s_setprio 1
	s_waitcnt lgkmcnt(6)
	v_mfma_scale_f32_16x16x128_f8f6f4 v[48:51], v[0:7], v[154:161], v[186:189], v133, v133 op_sel_hi:[0,0,0]
	v_mfma_scale_f32_16x16x128_f8f6f4 v[52:55], v[12:19], v[154:161], v[52:55], v133, v133 op_sel_hi:[0,0,0]
	s_waitcnt lgkmcnt(4)
	v_mfma_scale_f32_16x16x128_f8f6f4 v[32:35], v[0:7], v[162:169], v[190:193], v133, v133 op_sel_hi:[0,0,0]
	v_mfma_scale_f32_16x16x128_f8f6f4 v[40:43], v[12:19], v[162:169], v[194:197], v133, v133 op_sel_hi:[0,0,0]
	s_waitcnt lgkmcnt(2)
	v_mfma_scale_f32_16x16x128_f8f6f4 v[24:27], v[0:7], v[170:177], v[198:201], v133, v133 op_sel_hi:[0,0,0]
	v_mfma_scale_f32_16x16x128_f8f6f4 v[28:31], v[12:19], v[170:177], v[218:221], v133, v133 op_sel_hi:[0,0,0]
	s_waitcnt lgkmcnt(0)
	v_mfma_scale_f32_16x16x128_f8f6f4 v[8:11], v[0:7], v[178:185], v[8:11], v133, v133 op_sel_hi:[0,0,0]
	v_mfma_scale_f32_16x16x128_f8f6f4 v[12:15], v[12:19], v[178:185], v[222:225], v133, v133 op_sel_hi:[0,0,0]
	s_setprio 0
	s_setprio 1
	v_mfma_scale_f32_16x16x128_f8f6f4 v[56:59], v[138:145], v[154:161], v[56:59], v133, v133 op_sel_hi:[0,0,0]
	v_mfma_scale_f32_16x16x128_f8f6f4 v[60:63], v[146:153], v[154:161], v[60:63], v133, v133 op_sel_hi:[0,0,0]
	v_mfma_scale_f32_16x16x128_f8f6f4 v[36:39], v[138:145], v[162:169], v[226:229], v133, v133 op_sel_hi:[0,0,0]
	v_mfma_scale_f32_16x16x128_f8f6f4 v[44:47], v[146:153], v[162:169], v[230:233], v133, v133 op_sel_hi:[0,0,0]
	v_mfma_scale_f32_16x16x128_f8f6f4 v[16:19], v[138:145], v[170:177], v[234:237], v133, v133 op_sel_hi:[0,0,0]
	v_mfma_scale_f32_16x16x128_f8f6f4 v[20:23], v[146:153], v[170:177], v[238:241], v133, v133 op_sel_hi:[0,0,0]
	v_mfma_scale_f32_16x16x128_f8f6f4 v[0:3], v[138:145], v[178:185], v[242:245], v133, v133 op_sel_hi:[0,0,0]
	v_mfma_scale_f32_16x16x128_f8f6f4 v[4:7], v[146:153], v[178:185], v[246:249], v133, v133 op_sel_hi:[0,0,0]
	s_setprio 0
	s_barrier
	s_add_i32 s60, s60, 2
	s_add_u32 s58, s58, 0x100
	s_addc_u32 s59, s59, 0
	s_cmp_gt_u32 s60, 5
	s_mov_b64 s[26:27], s[22:23]
	s_cbranch_scc0 .LBB0_190
	s_and_b64 vcc, exec, s[8:9]
	s_cbranch_vccz .LBB0_193
	s_barrier

.LBB0_284:
	s_setprio 0
	s_cmp_lt_u32 s96, 64
	s_cbranch_scc1 .Ltc_skip_2
	v_writelane_b32 v200, s0, 0
	s_nop 1
	v_writelane_b32 v200, s1, 1
	s_nop 1
	v_writelane_b32 v200, s2, 2
	s_nop 1
	v_writelane_b32 v200, s3, 3
	s_nop 1
	v_writelane_b32 v200, s4, 4
	s_nop 1
	v_writelane_b32 v200, s5, 5
	s_nop 1
	v_writelane_b32 v200, s6, 6
	s_nop 1
	v_writelane_b32 v200, s7, 7
	s_nop 1
	v_writelane_b32 v200, s10, 8
	s_nop 1
	v_writelane_b32 v200, s11, 9
	s_nop 1
	v_writelane_b32 v200, s12, 10
	s_nop 1
	v_writelane_b32 v200, s13, 11
	s_nop 1
	v_writelane_b32 v200, s14, 12
	s_nop 1
	v_writelane_b32 v200, s15, 13
	s_nop 1
	v_writelane_b32 v200, s16, 14
	s_nop 1
	v_writelane_b32 v200, s17, 15
	s_nop 1
	v_writelane_b32 v200, s18, 16
	s_nop 1
	v_writelane_b32 v200, s19, 17
	s_nop 1
	v_writelane_b32 v200, s20, 18
	s_nop 1
	v_writelane_b32 v200, s21, 19
	s_nop 1
	v_writelane_b32 v200, s22, 20
	s_nop 1
	v_writelane_b32 v200, s23, 21
	s_nop 1
	v_writelane_b32 v200, s24, 22
	s_nop 1
	v_writelane_b32 v200, s25, 23
	s_nop 1
	v_writelane_b32 v200, s36, 24
	s_nop 1
	v_writelane_b32 v200, s37, 25
	s_nop 1
	v_writelane_b32 v200, s38, 26
	s_nop 1
	v_writelane_b32 v200, s39, 27
	s_nop 1
	v_writelane_b32 v200, s40, 28
	s_nop 1
	v_writelane_b32 v200, s41, 29
	s_nop 1
	v_writelane_b32 v200, s42, 30
	s_nop 1
	v_writelane_b32 v200, s43, 31
	s_nop 1
	v_writelane_b32 v200, s44, 32
	s_nop 1
	v_writelane_b32 v200, s45, 33
	s_nop 1
	v_writelane_b32 v200, s46, 34
	s_nop 1
	v_writelane_b32 v200, s47, 35
	s_nop 1
	v_writelane_b32 v200, s48, 36
	s_nop 1
	v_writelane_b32 v200, s49, 37
	s_nop 1
	v_writelane_b32 v200, s50, 38
	s_nop 1
	v_writelane_b32 v200, s51, 39
	s_nop 1
	s_mov_b32 s99, 2
	s_mov_b32 s98, 1
	s_mov_b32 s101, 192
	s_add_i32 s100, s96, 384
	s_branch .Ltc_next

.LBB0_350:
	ds_read_b128 v[112:115], v203
	ds_read_b128 v[116:119], v203 offset:1024
	ds_read_b128 v[144:147], v203 offset:2048
	ds_read_b128 v[148:151], v203 offset:3072
	ds_read_b128 v[152:155], v204
	ds_read_b128 v[156:159], v204 offset:1024
	ds_read_b128 v[160:163], v204 offset:2048
	ds_read_b128 v[164:167], v204 offset:3072
	s_add_u32 s20, s24, 0x100
	s_addc_u32 s21, s25, 0
	s_cmp_eq_u32 s56, 4
	s_cselect_b32 s22, s52, s20
	s_cselect_b32 s23, s7, s21
	s_cselect_b32 s28, s53, s54
	s_cselect_b32 s29, s9, s55
	s_add_u32 s26, s22, 0x80
	s_addc_u32 s27, s23, 0
	ds_read_b128 v[168:171], v205
	ds_read_b128 v[172:175], v205 offset:1024
	ds_read_b128 v[176:179], v205 offset:2048
	ds_read_b128 v[180:183], v205 offset:3072
	ds_read_b128 v[184:187], v205 offset:4096
	ds_read_b128 v[188:191], v205 offset:5120
	ds_read_b128 v[192:195], v205 offset:6144
	ds_read_b128 v[196:199], v205 offset:7168
	s_add_u32 s58, s24, 0x20080
	s_addc_u32 s59, s25, 0
	s_mov_b32 s57, m0
	s_mov_b32 m0, s50
	s_nop 0
	global_load_lds_dwordx4 v202, s[58:59]
	s_mov_b32 m0, s57
	s_add_u32 s24, s24, 0x30080
	s_addc_u32 s25, s25, 0
	s_mov_b32 s57, m0
	s_mov_b32 m0, s51
	s_nop 0
	global_load_lds_dwordx4 v202, s[24:25]
	s_mov_b32 m0, s57
	s_waitcnt vmcnt(8)
	s_waitcnt lgkmcnt(0)
	s_barrier
	s_setprio 1
	s_waitcnt lgkmcnt(6)
	v_mfma_scale_f32_16x16x128_f8f6f4 v[124:127], v[144:151], v[168:175], v[124:127], v206, v206 op_sel_hi:[0,0,0]
	s_waitcnt lgkmcnt(4)
	v_mfma_scale_f32_16x16x128_f8f6f4 v[104:107], v[112:119], v[176:183], v[104:107], v206, v206 op_sel_hi:[0,0,0]
	s_waitcnt lgkmcnt(0)
	v_mfma_scale_f32_16x16x128_f8f6f4 v[68:71], v[112:119], v[192:199], v[68:71], v206, v206 op_sel_hi:[0,0,0]
	v_mfma_scale_f32_16x16x128_f8f6f4 v[56:59], v[144:151], v[192:199], v[56:59], v206, v206 op_sel_hi:[0,0,0]
	v_mfma_scale_f32_16x16x128_f8f6f4 v[120:123], v[112:119], v[168:175], v[128:131], v206, v206 op_sel_hi:[0,0,0]
	v_mfma_scale_f32_16x16x128_f8f6f4 v[136:139], v[144:151], v[176:183], v[96:99], v206, v206 op_sel_hi:[0,0,0]
	v_mfma_scale_f32_16x16x128_f8f6f4 v[210:213], v[112:119], v[184:191], v[92:95], v206, v206 op_sel_hi:[0,0,0]
	v_mfma_scale_f32_16x16x128_f8f6f4 v[214:217], v[144:151], v[184:191], v[84:87], v206, v206 op_sel_hi:[0,0,0]
	s_setprio 0
	s_setprio 1
	v_mfma_scale_f32_16x16x128_f8f6f4 v[140:143], v[152:159], v[168:175], v[140:143], v206, v206 op_sel_hi:[0,0,0]
	v_mfma_scale_f32_16x16x128_f8f6f4 v[132:135], v[160:167], v[168:175], v[132:135], v206, v206 op_sel_hi:[0,0,0]
	v_mfma_scale_f32_16x16x128_f8f6f4 v[108:111], v[152:159], v[176:183], v[108:111], v206, v206 op_sel_hi:[0,0,0]
	v_mfma_scale_f32_16x16x128_f8f6f4 v[168:171], v[160:167], v[176:183], v[100:103], v206, v206 op_sel_hi:[0,0,0]
	v_mfma_scale_f32_16x16x128_f8f6f4 v[172:175], v[152:159], v[184:191], v[88:91], v206, v206 op_sel_hi:[0,0,0]
	v_mfma_scale_f32_16x16x128_f8f6f4 v[176:179], v[160:167], v[184:191], v[80:83], v206, v206 op_sel_hi:[0,0,0]
	v_mfma_scale_f32_16x16x128_f8f6f4 v[180:183], v[152:159], v[192:199], v[52:55], v206, v206 op_sel_hi:[0,0,0]
	v_mfma_scale_f32_16x16x128_f8f6f4 v[184:187], v[160:167], v[192:199], v[48:51], v206, v206 op_sel_hi:[0,0,0]
	s_setprio 0
	s_barrier
	s_nop 4
	ds_read_b128 v[48:51], v205 offset:16384
	ds_read_b128 v[52:55], v205 offset:17408
	ds_read_b128 v[80:83], v205 offset:18432
	ds_read_b128 v[84:87], v205 offset:19456
	ds_read_b128 v[88:91], v205 offset:20480
	ds_read_b128 v[92:95], v205 offset:21504
	ds_read_b128 v[96:99], v205 offset:22528
	ds_read_b128 v[100:103], v205 offset:23552
	s_mov_b32 s24, m0
	s_mov_b32 m0, s17
	s_nop 0
	global_load_lds_dwordx4 v201, s[28:29]
	s_mov_b32 m0, s24
	s_add_u32 s24, s28, 0x10000
	s_addc_u32 s25, s29, 0
	s_mov_b32 s57, m0
	s_mov_b32 m0, s19
	s_nop 0
	global_load_lds_dwordx4 v201, s[24:25]
	s_mov_b32 m0, s57
	s_add_u32 s24, s28, 0x20000
	s_addc_u32 s25, s29, 0
	s_mov_b32 s57, m0
	s_mov_b32 m0, s34
	s_nop 0
	global_load_lds_dwordx4 v201, s[24:25]
	s_mov_b32 m0, s57
	s_add_u32 s24, s28, 0x30000
	s_addc_u32 s25, s29, 0
	s_mov_b32 s57, m0
	s_mov_b32 m0, s35
	s_nop 0
	global_load_lds_dwordx4 v201, s[24:25]
	s_mov_b32 m0, s57
	s_waitcnt vmcnt(6)
	s_waitcnt lgkmcnt(0)
	s_barrier
	s_setprio 1
	s_waitcnt lgkmcnt(6)
	v_mfma_scale_f32_16x16x128_f8f6f4 v[76:79], v[112:119], v[48:55], v[76:79], v206, v206 op_sel_hi:[0,0,0]
	v_mfma_scale_f32_16x16x128_f8f6f4 v[64:67], v[144:151], v[48:55], v[64:67], v206, v206 op_sel_hi:[0,0,0]
	s_waitcnt lgkmcnt(4)
	v_mfma_scale_f32_16x16x128_f8f6f4 v[188:191], v[112:119], v[80:87], v[44:47], v206, v206 op_sel_hi:[0,0,0]
	v_mfma_scale_f32_16x16x128_f8f6f4 v[192:195], v[144:151], v[80:87], v[40:43], v206, v206 op_sel_hi:[0,0,0]
	s_waitcnt lgkmcnt(2)
	v_mfma_scale_f32_16x16x128_f8f6f4 v[196:199], v[112:119], v[88:95], v[28:31], v206, v206 op_sel_hi:[0,0,0]
	v_mfma_scale_f32_16x16x128_f8f6f4 v[218:221], v[144:151], v[88:95], v[24:27], v206, v206 op_sel_hi:[0,0,0]
	s_waitcnt lgkmcnt(0)
	v_mfma_scale_f32_16x16x128_f8f6f4 v[222:225], v[112:119], v[96:103], v[12:15], v206, v206 op_sel_hi:[0,0,0]
	v_mfma_scale_f32_16x16x128_f8f6f4 v[226:229], v[144:151], v[96:103], v[8:11], v206, v206 op_sel_hi:[0,0,0]
	s_setprio 0
	s_setprio 1
	v_mfma_scale_f32_16x16x128_f8f6f4 v[72:75], v[152:159], v[48:55], v[72:75], v206, v206 op_sel_hi:[0,0,0]
	v_mfma_scale_f32_16x16x128_f8f6f4 v[60:63], v[160:167], v[48:55], v[60:63], v206, v206 op_sel_hi:[0,0,0]
	v_mfma_scale_f32_16x16x128_f8f6f4 v[230:233], v[152:159], v[80:87], v[36:39], v206, v206 op_sel_hi:[0,0,0]
	v_mfma_scale_f32_16x16x128_f8f6f4 v[234:237], v[160:167], v[80:87], v[32:35], v206, v206 op_sel_hi:[0,0,0]
	v_mfma_scale_f32_16x16x128_f8f6f4 v[238:241], v[152:159], v[88:95], v[20:23], v206, v206 op_sel_hi:[0,0,0]
	v_mfma_scale_f32_16x16x128_f8f6f4 v[242:245], v[160:167], v[88:95], v[16:19], v206, v206 op_sel_hi:[0,0,0]
	v_mfma_scale_f32_16x16x128_f8f6f4 v[246:249], v[152:159], v[96:103], v[4:7], v206, v206 op_sel_hi:[0,0,0]
	v_mfma_scale_f32_16x16x128_f8f6f4 v[250:253], v[160:167], v[96:103], v[0:3], v206, v206 op_sel_hi:[0,0,0]
	s_setprio 0
	s_barrier
	s_nop 4
	ds_read_b128 v[0:3], v207
	ds_read_b128 v[4:7], v207 offset:1024
	ds_read_b128 v[16:19], v207 offset:2048
	ds_read_b128 v[20:23], v207 offset:3072
	ds_read_b128 v[112:115], v208
	ds_read_b128 v[116:119], v208 offset:1024
	ds_read_b128 v[144:147], v208 offset:2048
	ds_read_b128 v[148:151], v208 offset:3072
	ds_read_b128 v[8:11], v205 offset:32768
	ds_read_b128 v[12:15], v205 offset:33792
	ds_read_b128 v[24:27], v205 offset:34816
	ds_read_b128 v[28:31], v205 offset:35840
	ds_read_b128 v[32:35], v205 offset:36864
	ds_read_b128 v[36:39], v205 offset:37888
	ds_read_b128 v[40:43], v205 offset:38912
	ds_read_b128 v[44:47], v205 offset:39936
	s_mov_b32 s24, m0
	s_mov_b32 m0, s33
	s_nop 0
	global_load_lds_dwordx4 v202, s[22:23]
	s_mov_b32 m0, s24
	s_add_u32 s24, s22, 0x10000
	s_addc_u32 s25, s23, 0
	s_mov_b32 s57, m0
	s_mov_b32 m0, s36
	s_nop 0
	global_load_lds_dwordx4 v202, s[24:25]
	s_mov_b32 m0, s57
	s_add_u32 s24, s22, 0x20000
	s_addc_u32 s25, s23, 0
	s_mov_b32 s57, m0
	s_mov_b32 m0, s37
	s_nop 0
	global_load_lds_dwordx4 v202, s[24:25]
	s_mov_b32 m0, s57
	s_add_u32 s24, s22, 0x30000
	s_addc_u32 s25, s23, 0
	s_mov_b32 s57, m0
	s_mov_b32 m0, s38
	s_nop 0
	global_load_lds_dwordx4 v202, s[24:25]
	s_mov_b32 m0, s57
	s_waitcnt vmcnt(8)
	s_waitcnt lgkmcnt(0)
	s_barrier
	s_setprio 1
	s_waitcnt lgkmcnt(6)
	v_mfma_scale_f32_16x16x128_f8f6f4 v[128:131], v[0:7], v[8:15], v[120:123], v206, v206 op_sel_hi:[0,0,0]
	v_mfma_scale_f32_16x16x128_f8f6f4 v[124:127], v[16:23], v[8:15], v[124:127], v206, v206 op_sel_hi:[0,0,0]
	s_waitcnt lgkmcnt(4)
	v_mfma_scale_f32_16x16x128_f8f6f4 v[104:107], v[0:7], v[24:31], v[104:107], v206, v206 op_sel_hi:[0,0,0]
	v_mfma_scale_f32_16x16x128_f8f6f4 v[96:99], v[16:23], v[24:31], v[136:139], v206, v206 op_sel_hi:[0,0,0]
	s_waitcnt lgkmcnt(2)
	v_mfma_scale_f32_16x16x128_f8f6f4 v[92:95], v[0:7], v[32:39], v[210:213], v206, v206 op_sel_hi:[0,0,0]
	v_mfma_scale_f32_16x16x128_f8f6f4 v[84:87], v[16:23], v[32:39], v[214:217], v206, v206 op_sel_hi:[0,0,0]
	s_waitcnt lgkmcnt(0)
	v_mfma_scale_f32_16x16x128_f8f6f4 v[68:71], v[0:7], v[40:47], v[68:71], v206, v206 op_sel_hi:[0,0,0]
	v_mfma_scale_f32_16x16x128_f8f6f4 v[56:59], v[16:23], v[40:47], v[56:59], v206, v206 op_sel_hi:[0,0,0]
	s_setprio 0
	s_setprio 1
	v_mfma_scale_f32_16x16x128_f8f6f4 v[140:143], v[112:119], v[8:15], v[140:143], v206, v206 op_sel_hi:[0,0,0]
	v_mfma_scale_f32_16x16x128_f8f6f4 v[132:135], v[144:151], v[8:15], v[132:135], v206, v206 op_sel_hi:[0,0,0]
	v_mfma_scale_f32_16x16x128_f8f6f4 v[108:111], v[112:119], v[24:31], v[108:111], v206, v206 op_sel_hi:[0,0,0]
	v_mfma_scale_f32_16x16x128_f8f6f4 v[100:103], v[144:151], v[24:31], v[168:171], v206, v206 op_sel_hi:[0,0,0]
	v_mfma_scale_f32_16x16x128_f8f6f4 v[88:91], v[112:119], v[32:39], v[172:175], v206, v206 op_sel_hi:[0,0,0]
	v_mfma_scale_f32_16x16x128_f8f6f4 v[80:83], v[144:151], v[32:39], v[176:179], v206, v206 op_sel_hi:[0,0,0]
	v_mfma_scale_f32_16x16x128_f8f6f4 v[52:55], v[112:119], v[40:47], v[180:183], v206, v206 op_sel_hi:[0,0,0]
	v_mfma_scale_f32_16x16x128_f8f6f4 v[48:51], v[144:151], v[40:47], v[184:187], v206, v206 op_sel_hi:[0,0,0]
	s_setprio 0
	s_barrier
	s_add_u32 s24, s28, 0x80
	s_addc_u32 s25, s29, 0
	ds_read_b128 v[32:35], v205 offset:49152
	ds_read_b128 v[36:39], v205 offset:50176
	ds_read_b128 v[152:155], v205 offset:51200
	ds_read_b128 v[156:159], v205 offset:52224
	ds_read_b128 v[160:163], v205 offset:53248
	ds_read_b128 v[164:167], v205 offset:54272
	ds_read_b128 v[168:171], v205 offset:55296
	ds_read_b128 v[172:175], v205 offset:56320
	s_mov_b32 s57, m0
	s_mov_b32 m0, s44
	s_nop 0
	global_load_lds_dwordx4 v201, s[24:25]
	s_mov_b32 m0, s57
	s_add_u32 s24, s28, 0x10080
	s_addc_u32 s25, s29, 0
	s_mov_b32 s57, m0
	s_mov_b32 m0, s45
	s_nop 0
	global_load_lds_dwordx4 v201, s[24:25]
	s_mov_b32 m0, s57
	s_add_u32 s24, s28, 0x20080
	s_addc_u32 s25, s29, 0
	s_mov_b32 s57, m0
	s_mov_b32 m0, s48
	s_nop 0
	global_load_lds_dwordx4 v201, s[24:25]
	s_mov_b32 m0, s57
	s_add_u32 s24, s28, 0x30080
	s_addc_u32 s25, s29, 0
	s_mov_b32 s28, m0
	s_mov_b32 m0, s49
	s_nop 0
	global_load_lds_dwordx4 v201, s[24:25]
	s_mov_b32 m0, s28
	s_mov_b32 s24, m0
	s_mov_b32 m0, s46
	s_nop 0
	global_load_lds_dwordx4 v202, s[26:27]
	s_mov_b32 m0, s24
	s_add_u32 s22, s22, 0x10080
	s_addc_u32 s23, s23, 0
	s_mov_b32 s24, m0
	s_mov_b32 m0, s47
	s_nop 0
	global_load_lds_dwordx4 v202, s[22:23]
	s_mov_b32 m0, s24
	s_waitcnt vmcnt(8)
	s_waitcnt lgkmcnt(0)
	s_barrier
	s_setprio 1
	s_waitcnt lgkmcnt(6)
	v_mfma_scale_f32_16x16x128_f8f6f4 v[76:79], v[0:7], v[32:39], v[76:79], v206, v206 op_sel_hi:[0,0,0]
	v_mfma_scale_f32_16x16x128_f8f6f4 v[64:67], v[16:23], v[32:39], v[64:67], v206, v206 op_sel_hi:[0,0,0]
	s_waitcnt lgkmcnt(4)
	v_mfma_scale_f32_16x16x128_f8f6f4 v[44:47], v[0:7], v[152:159], v[188:191], v206, v206 op_sel_hi:[0,0,0]
	v_mfma_scale_f32_16x16x128_f8f6f4 v[40:43], v[16:23], v[152:159], v[192:195], v206, v206 op_sel_hi:[0,0,0]
	s_waitcnt lgkmcnt(2)
	v_mfma_scale_f32_16x16x128_f8f6f4 v[28:31], v[0:7], v[160:167], v[196:199], v206, v206 op_sel_hi:[0,0,0]
	v_mfma_scale_f32_16x16x128_f8f6f4 v[24:27], v[16:23], v[160:167], v[218:221], v206, v206 op_sel_hi:[0,0,0]
	s_waitcnt lgkmcnt(0)
	v_mfma_scale_f32_16x16x128_f8f6f4 v[12:15], v[0:7], v[168:175], v[222:225], v206, v206 op_sel_hi:[0,0,0]
	v_mfma_scale_f32_16x16x128_f8f6f4 v[8:11], v[16:23], v[168:175], v[226:229], v206, v206 op_sel_hi:[0,0,0]
	s_setprio 0
	s_setprio 1
	v_mfma_scale_f32_16x16x128_f8f6f4 v[72:75], v[112:119], v[32:39], v[72:75], v206, v206 op_sel_hi:[0,0,0]
	v_mfma_scale_f32_16x16x128_f8f6f4 v[60:63], v[144:151], v[32:39], v[60:63], v206, v206 op_sel_hi:[0,0,0]
	v_mfma_scale_f32_16x16x128_f8f6f4 v[36:39], v[112:119], v[152:159], v[230:233], v206, v206 op_sel_hi:[0,0,0]
	v_mfma_scale_f32_16x16x128_f8f6f4 v[32:35], v[144:151], v[152:159], v[234:237], v206, v206 op_sel_hi:[0,0,0]
	v_mfma_scale_f32_16x16x128_f8f6f4 v[20:23], v[112:119], v[160:167], v[238:241], v206, v206 op_sel_hi:[0,0,0]
	v_mfma_scale_f32_16x16x128_f8f6f4 v[16:19], v[144:151], v[160:167], v[242:245], v206, v206 op_sel_hi:[0,0,0]
	v_mfma_scale_f32_16x16x128_f8f6f4 v[4:7], v[112:119], v[168:175], v[246:249], v206, v206 op_sel_hi:[0,0,0]
	v_mfma_scale_f32_16x16x128_f8f6f4 v[0:3], v[144:151], v[168:175], v[250:253], v206, v206 op_sel_hi:[0,0,0]
	s_setprio 0
	s_barrier
	s_add_i32 s56, s56, 2
	s_add_u32 s54, s54, 0x100
	s_addc_u32 s55, s55, 0
	s_cmp_gt_u32 s56, 5
	s_mov_b64 s[24:25], s[20:21]
	s_cbranch_scc0 .LBB0_350
	s_and_b64 vcc, exec, s[4:5]
	s_cbranch_vccz .LBB0_353
	s_barrier

.LBB0_530:
	s_add_u32 s34, s34, 0x100
	s_addc_u32 s35, s35, 0
	s_and_b64 s[36:37], s[38:39], exec
	s_cselect_b32 s42, s16, s34
	s_cselect_b32 s43, s17, s35
	s_add_u32 s36, s42, 0x80
	s_addc_u32 s37, s43, 0
	s_waitcnt vmcnt(8)
	s_and_b64 s[38:39], s[38:39], exec
	s_waitcnt lgkmcnt(0)
	s_cselect_b32 s38, s26, s15
	s_cselect_b32 s39, s27, s23
	s_add_u32 s40, s38, 0x80
	s_addc_u32 s41, s39, 0
	s_barrier
	s_setprio 1
	s_waitcnt lgkmcnt(6)
	v_mfma_scale_f32_16x16x128_f8f6f4 v[188:191], v[16:23], v[56:63], v[188:191], v205, v205 op_sel_hi:[0,0,0]
	v_mfma_scale_f32_16x16x128_f8f6f4 v[180:183], v[24:31], v[56:63], v[180:183], v205, v205 op_sel_hi:[0,0,0]
	s_waitcnt lgkmcnt(4)
	v_mfma_scale_f32_16x16x128_f8f6f4 v[172:175], v[16:23], v[48:55], v[172:175], v205, v205 op_sel_hi:[0,0,0]
	v_mfma_scale_f32_16x16x128_f8f6f4 v[164:167], v[24:31], v[48:55], v[164:167], v205, v205 op_sel_hi:[0,0,0]
	s_waitcnt lgkmcnt(2)
	v_mfma_scale_f32_16x16x128_f8f6f4 v[156:159], v[16:23], v[40:47], v[156:159], v205, v205 op_sel_hi:[0,0,0]
	v_mfma_scale_f32_16x16x128_f8f6f4 v[148:151], v[24:31], v[40:47], v[148:151], v205, v205 op_sel_hi:[0,0,0]
	s_waitcnt lgkmcnt(0)
	v_mfma_scale_f32_16x16x128_f8f6f4 v[140:143], v[16:23], v[32:39], v[140:143], v205, v205 op_sel_hi:[0,0,0]
	v_mfma_scale_f32_16x16x128_f8f6f4 v[132:135], v[24:31], v[32:39], v[132:135], v205, v205 op_sel_hi:[0,0,0]
	s_setprio 0
	s_setprio 1
	v_mfma_scale_f32_16x16x128_f8f6f4 v[184:187], v[0:7], v[56:63], v[184:187], v205, v205 op_sel_hi:[0,0,0]
	v_mfma_scale_f32_16x16x128_f8f6f4 v[176:179], v[8:15], v[56:63], v[176:179], v205, v205 op_sel_hi:[0,0,0]
	v_mfma_scale_f32_16x16x128_f8f6f4 v[168:171], v[0:7], v[48:55], v[168:171], v205, v205 op_sel_hi:[0,0,0]
	v_mfma_scale_f32_16x16x128_f8f6f4 v[160:163], v[8:15], v[48:55], v[160:163], v205, v205 op_sel_hi:[0,0,0]
	v_mfma_scale_f32_16x16x128_f8f6f4 v[152:155], v[0:7], v[40:47], v[152:155], v205, v205 op_sel_hi:[0,0,0]
	v_mfma_scale_f32_16x16x128_f8f6f4 v[144:147], v[8:15], v[40:47], v[144:147], v205, v205 op_sel_hi:[0,0,0]
	v_mfma_scale_f32_16x16x128_f8f6f4 v[136:139], v[0:7], v[32:39], v[136:139], v205, v205 op_sel_hi:[0,0,0]
	v_mfma_scale_f32_16x16x128_f8f6f4 v[128:131], v[8:15], v[32:39], v[128:131], v205, v205 op_sel_hi:[0,0,0]
	s_setprio 0
	s_barrier
	s_add_u32 s70, s38, 0x10000
	ds_read_b128 v[32:35], v210 offset:16384
	ds_read_b128 v[36:39], v210 offset:17408
	ds_read_b128 v[40:43], v210 offset:18432
	ds_read_b128 v[44:47], v210 offset:19456
	ds_read_b128 v[48:51], v210 offset:20480
	ds_read_b128 v[52:55], v210 offset:21504
	ds_read_b128 v[56:59], v210 offset:22528
	ds_read_b128 v[60:63], v210 offset:23552
	s_mov_b32 s69, m0
	s_mov_b32 m0, s29
	s_nop 0
	global_load_lds_dwordx4 v199, s[38:39]
	s_mov_b32 m0, s69
	s_addc_u32 s71, s39, 0
	s_mov_b32 s69, m0
	s_mov_b32 m0, s47
	s_nop 0
	global_load_lds_dwordx4 v199, s[70:71]
	s_mov_b32 m0, s69
	s_add_u32 s70, s38, 0x20000
	s_addc_u32 s71, s39, 0
	s_mov_b32 s69, m0
	s_mov_b32 m0, s48
	s_nop 0
	global_load_lds_dwordx4 v199, s[70:71]
	s_mov_b32 m0, s69
	s_add_u32 s70, s38, 0x30000
	s_addc_u32 s71, s39, 0
	s_mov_b32 s69, m0
	s_mov_b32 m0, s49
	s_nop 0
	global_load_lds_dwordx4 v199, s[70:71]
	s_mov_b32 m0, s69
	s_nop 0
	s_waitcnt vmcnt(6)
	s_waitcnt lgkmcnt(0)
	s_barrier
	s_setprio 1
	s_waitcnt lgkmcnt(6)
	v_mfma_scale_f32_16x16x128_f8f6f4 v[124:127], v[16:23], v[32:39], v[124:127], v205, v205 op_sel_hi:[0,0,0]
	v_mfma_scale_f32_16x16x128_f8f6f4 v[116:119], v[24:31], v[32:39], v[116:119], v205, v205 op_sel_hi:[0,0,0]
	s_waitcnt lgkmcnt(4)
	v_mfma_scale_f32_16x16x128_f8f6f4 v[108:111], v[16:23], v[40:47], v[108:111], v205, v205 op_sel_hi:[0,0,0]
	v_mfma_scale_f32_16x16x128_f8f6f4 v[100:103], v[24:31], v[40:47], v[100:103], v205, v205 op_sel_hi:[0,0,0]
	s_waitcnt lgkmcnt(2)
	v_mfma_scale_f32_16x16x128_f8f6f4 v[92:95], v[16:23], v[48:55], v[92:95], v205, v205 op_sel_hi:[0,0,0]
	v_mfma_scale_f32_16x16x128_f8f6f4 v[84:87], v[24:31], v[48:55], v[84:87], v205, v205 op_sel_hi:[0,0,0]
	s_waitcnt lgkmcnt(0)
	v_mfma_scale_f32_16x16x128_f8f6f4 v[72:75], v[16:23], v[56:63], v[72:75], v205, v205 op_sel_hi:[0,0,0]
	v_mfma_scale_f32_16x16x128_f8f6f4 v[64:67], v[24:31], v[56:63], v[64:67], v205, v205 op_sel_hi:[0,0,0]
	s_setprio 0
	s_setprio 1
	v_mfma_scale_f32_16x16x128_f8f6f4 v[120:123], v[0:7], v[32:39], v[120:123], v205, v205 op_sel_hi:[0,0,0]
	v_mfma_scale_f32_16x16x128_f8f6f4 v[112:115], v[8:15], v[32:39], v[112:115], v205, v205 op_sel_hi:[0,0,0]
	v_mfma_scale_f32_16x16x128_f8f6f4 v[104:107], v[0:7], v[40:47], v[104:107], v205, v205 op_sel_hi:[0,0,0]
	v_mfma_scale_f32_16x16x128_f8f6f4 v[96:99], v[8:15], v[40:47], v[96:99], v205, v205 op_sel_hi:[0,0,0]
	v_mfma_scale_f32_16x16x128_f8f6f4 v[88:91], v[0:7], v[48:55], v[88:91], v205, v205 op_sel_hi:[0,0,0]
	v_mfma_scale_f32_16x16x128_f8f6f4 v[80:83], v[8:15], v[48:55], v[80:83], v205, v205 op_sel_hi:[0,0,0]
	v_mfma_scale_f32_16x16x128_f8f6f4 v[76:79], v[0:7], v[56:63], v[76:79], v205, v205 op_sel_hi:[0,0,0]
	v_mfma_scale_f32_16x16x128_f8f6f4 v[68:71], v[8:15], v[56:63], v[68:71], v205, v205 op_sel_hi:[0,0,0]
	s_setprio 0
	s_barrier
	v_add_u32_e32 v12, 0x18000, v209
	v_add_u32_e32 v28, 0x1c000, v209
	ds_read_b128 v[0:3], v12
	ds_read_b128 v[4:7], v12 offset:1024
	ds_read_b128 v[8:11], v12 offset:2048
	ds_read_b128 v[12:15], v12 offset:3072
	ds_read_b128 v[16:19], v28
	ds_read_b128 v[20:23], v28 offset:1024
	ds_read_b128 v[24:27], v28 offset:2048
	ds_read_b128 v[28:31], v28 offset:3072
	ds_read_b128 v[32:35], v210 offset:32768
	ds_read_b128 v[36:39], v210 offset:33792
	ds_read_b128 v[40:43], v210 offset:34816
	ds_read_b128 v[44:47], v210 offset:35840
	ds_read_b128 v[48:51], v210 offset:36864
	ds_read_b128 v[52:55], v210 offset:37888
	ds_read_b128 v[56:59], v210 offset:38912
	ds_read_b128 v[60:63], v210 offset:39936
	s_mov_b32 s69, m0
	s_mov_b32 m0, s46
	s_nop 0
	global_load_lds_dwordx4 v200, s[42:43]
	s_mov_b32 m0, s69
	s_nop 0
	s_mov_b32 s69, m0
	s_mov_b32 m0, s50
	s_nop 0
	global_load_lds_dwordx4 v201, s[42:43]
	s_mov_b32 m0, s69
	s_mov_b32 s69, m0
	s_mov_b32 m0, s51
	s_nop 0
	global_load_lds_dwordx4 v202, s[42:43]
	s_mov_b32 m0, s69
	s_nop 0
	s_mov_b32 s69, m0
	s_mov_b32 m0, s52
	s_nop 0
	global_load_lds_dwordx4 v203, s[42:43]
	s_mov_b32 m0, s69
	s_waitcnt vmcnt(8)
	s_waitcnt lgkmcnt(0)
	s_barrier
	s_setprio 1
	s_waitcnt lgkmcnt(6)
	v_mfma_scale_f32_16x16x128_f8f6f4 v[188:191], v[0:7], v[32:39], v[188:191], v205, v205 op_sel_hi:[0,0,0]
	v_mfma_scale_f32_16x16x128_f8f6f4 v[180:183], v[8:15], v[32:39], v[180:183], v205, v205 op_sel_hi:[0,0,0]
	s_waitcnt lgkmcnt(4)
	v_mfma_scale_f32_16x16x128_f8f6f4 v[172:175], v[0:7], v[40:47], v[172:175], v205, v205 op_sel_hi:[0,0,0]
	v_mfma_scale_f32_16x16x128_f8f6f4 v[164:167], v[8:15], v[40:47], v[164:167], v205, v205 op_sel_hi:[0,0,0]
	s_waitcnt lgkmcnt(2)
	v_mfma_scale_f32_16x16x128_f8f6f4 v[156:159], v[0:7], v[48:55], v[156:159], v205, v205 op_sel_hi:[0,0,0]
	v_mfma_scale_f32_16x16x128_f8f6f4 v[148:151], v[8:15], v[48:55], v[148:151], v205, v205 op_sel_hi:[0,0,0]
	s_waitcnt lgkmcnt(0)
	v_mfma_scale_f32_16x16x128_f8f6f4 v[140:143], v[0:7], v[56:63], v[140:143], v205, v205 op_sel_hi:[0,0,0]
	v_mfma_scale_f32_16x16x128_f8f6f4 v[132:135], v[8:15], v[56:63], v[132:135], v205, v205 op_sel_hi:[0,0,0]
	s_setprio 0
	s_setprio 1
	v_mfma_scale_f32_16x16x128_f8f6f4 v[184:187], v[16:23], v[32:39], v[184:187], v205, v205 op_sel_hi:[0,0,0]
	v_mfma_scale_f32_16x16x128_f8f6f4 v[176:179], v[24:31], v[32:39], v[176:179], v205, v205 op_sel_hi:[0,0,0]
	v_mfma_scale_f32_16x16x128_f8f6f4 v[168:171], v[16:23], v[40:47], v[168:171], v205, v205 op_sel_hi:[0,0,0]
	v_mfma_scale_f32_16x16x128_f8f6f4 v[160:163], v[24:31], v[40:47], v[160:163], v205, v205 op_sel_hi:[0,0,0]
	v_mfma_scale_f32_16x16x128_f8f6f4 v[152:155], v[16:23], v[48:55], v[152:155], v205, v205 op_sel_hi:[0,0,0]
	v_mfma_scale_f32_16x16x128_f8f6f4 v[144:147], v[24:31], v[48:55], v[144:147], v205, v205 op_sel_hi:[0,0,0]
	v_mfma_scale_f32_16x16x128_f8f6f4 v[136:139], v[16:23], v[56:63], v[136:139], v205, v205 op_sel_hi:[0,0,0]
	v_mfma_scale_f32_16x16x128_f8f6f4 v[128:131], v[24:31], v[56:63], v[128:131], v205, v205 op_sel_hi:[0,0,0]
	s_setprio 0
	s_barrier
	ds_read_b128 v[32:35], v210 offset:49152
	ds_read_b128 v[36:39], v210 offset:50176
	ds_read_b128 v[40:43], v210 offset:51200
	ds_read_b128 v[44:47], v210 offset:52224
	ds_read_b128 v[48:51], v210 offset:53248
	ds_read_b128 v[52:55], v210 offset:54272
	ds_read_b128 v[56:59], v210 offset:55296
	ds_read_b128 v[60:63], v210 offset:56320
	s_mov_b32 s42, m0
	s_mov_b32 m0, s55
	s_nop 0
	global_load_lds_dwordx4 v199, s[40:41]
	s_mov_b32 m0, s42
	s_add_u32 s40, s38, 0x10080
	s_addc_u32 s41, s39, 0
	s_mov_b32 s42, m0
	s_mov_b32 m0, s56
	s_nop 0
	global_load_lds_dwordx4 v199, s[40:41]
	s_mov_b32 m0, s42
	s_add_u32 s40, s38, 0x20080
	s_addc_u32 s41, s39, 0
	s_mov_b32 s42, m0
	s_mov_b32 m0, s59
	s_nop 0
	global_load_lds_dwordx4 v199, s[40:41]
	s_mov_b32 m0, s42
	s_add_u32 s38, s38, 0x30080
	s_addc_u32 s39, s39, 0
	s_mov_b32 s40, m0
	s_mov_b32 m0, s60
	s_nop 0
	global_load_lds_dwordx4 v199, s[38:39]
	s_mov_b32 m0, s40
	s_mov_b32 s38, m0
	s_mov_b32 m0, s57
	s_nop 0
	global_load_lds_dwordx4 v200, s[36:37]
	s_mov_b32 m0, s38
	s_nop 0
	s_mov_b32 s38, m0
	s_mov_b32 m0, s58
	s_nop 0
	global_load_lds_dwordx4 v201, s[36:37]
	s_mov_b32 m0, s38
	s_waitcnt vmcnt(8)
	s_waitcnt lgkmcnt(0)
	s_barrier
	s_setprio 1
	s_waitcnt lgkmcnt(6)
	v_mfma_scale_f32_16x16x128_f8f6f4 v[124:127], v[0:7], v[32:39], v[124:127], v205, v205 op_sel_hi:[0,0,0]
	v_mfma_scale_f32_16x16x128_f8f6f4 v[116:119], v[8:15], v[32:39], v[116:119], v205, v205 op_sel_hi:[0,0,0]
	s_waitcnt lgkmcnt(4)
	v_mfma_scale_f32_16x16x128_f8f6f4 v[108:111], v[0:7], v[40:47], v[108:111], v205, v205 op_sel_hi:[0,0,0]
	v_mfma_scale_f32_16x16x128_f8f6f4 v[100:103], v[8:15], v[40:47], v[100:103], v205, v205 op_sel_hi:[0,0,0]
	s_waitcnt lgkmcnt(2)
	v_mfma_scale_f32_16x16x128_f8f6f4 v[92:95], v[0:7], v[48:55], v[92:95], v205, v205 op_sel_hi:[0,0,0]
	v_mfma_scale_f32_16x16x128_f8f6f4 v[84:87], v[8:15], v[48:55], v[84:87], v205, v205 op_sel_hi:[0,0,0]
	s_waitcnt lgkmcnt(0)
	v_mfma_scale_f32_16x16x128_f8f6f4 v[72:75], v[0:7], v[56:63], v[72:75], v205, v205 op_sel_hi:[0,0,0]
	v_mfma_scale_f32_16x16x128_f8f6f4 v[64:67], v[8:15], v[56:63], v[64:67], v205, v205 op_sel_hi:[0,0,0]
	s_setprio 0
	s_setprio 1
	v_mfma_scale_f32_16x16x128_f8f6f4 v[120:123], v[16:23], v[32:39], v[120:123], v205, v205 op_sel_hi:[0,0,0]
	v_mfma_scale_f32_16x16x128_f8f6f4 v[112:115], v[24:31], v[32:39], v[112:115], v205, v205 op_sel_hi:[0,0,0]
	v_mfma_scale_f32_16x16x128_f8f6f4 v[104:107], v[16:23], v[40:47], v[104:107], v205, v205 op_sel_hi:[0,0,0]
	v_mfma_scale_f32_16x16x128_f8f6f4 v[96:99], v[24:31], v[40:47], v[96:99], v205, v205 op_sel_hi:[0,0,0]
	v_mfma_scale_f32_16x16x128_f8f6f4 v[88:91], v[16:23], v[48:55], v[88:91], v205, v205 op_sel_hi:[0,0,0]
	v_mfma_scale_f32_16x16x128_f8f6f4 v[80:83], v[24:31], v[48:55], v[80:83], v205, v205 op_sel_hi:[0,0,0]
	v_mfma_scale_f32_16x16x128_f8f6f4 v[76:79], v[16:23], v[56:63], v[76:79], v205, v205 op_sel_hi:[0,0,0]
	v_mfma_scale_f32_16x16x128_f8f6f4 v[68:71], v[24:31], v[56:63], v[68:71], v205, v205 op_sel_hi:[0,0,0]
	s_setprio 0
	s_barrier
	s_add_i32 s25, s25, 2
	s_add_u32 s15, s15, 0x100
	s_addc_u32 s23, s23, 0
	s_cmp_gt_u32 s25, 5
	s_cbranch_scc1 .LBB0_533

.LBB0_645:
	ds_read_b128 v[146:149], v139
	ds_read_b128 v[150:153], v139 offset:1024
	ds_read_b128 v[154:157], v139 offset:2048
	ds_read_b128 v[158:161], v139 offset:3072
	ds_read_b128 v[162:165], v140
	ds_read_b128 v[166:169], v140 offset:1024
	ds_read_b128 v[170:173], v140 offset:2048
	ds_read_b128 v[174:177], v140 offset:3072
	s_add_u32 s24, s22, 0x100
	s_addc_u32 s25, s23, 0
	s_cmp_eq_u32 s13, 4
	s_cselect_b32 s26, s16, s24
	s_cselect_b32 s27, s17, s25
	s_cselect_b32 s30, s18, s1
	s_cselect_b32 s31, s19, s11
	s_add_u32 s28, s26, 0x80
	s_addc_u32 s29, s27, 0
	ds_read_b128 v[178:181], v141
	ds_read_b128 v[182:185], v141 offset:1024
	ds_read_b128 v[186:189], v141 offset:2048
	ds_read_b128 v[190:193], v141 offset:3072
	ds_read_b128 v[194:197], v141 offset:4096
	ds_read_b128 v[198:201], v141 offset:5120
	ds_read_b128 v[202:205], v141 offset:6144
	ds_read_b128 v[206:209], v141 offset:7168
	s_add_u32 s60, s22, 0x20080
	s_addc_u32 s61, s23, 0
	s_mov_b32 s15, m0
	s_mov_b32 m0, s53
	s_nop 0
	global_load_lds_dwordx4 v137, s[60:61]
	s_mov_b32 m0, s15
	s_add_u32 s22, s22, 0x30080
	s_addc_u32 s23, s23, 0
	s_mov_b32 s15, m0
	s_mov_b32 m0, s54
	s_nop 0
	global_load_lds_dwordx4 v137, s[22:23]
	s_mov_b32 m0, s15
	s_waitcnt vmcnt(8)
	s_waitcnt lgkmcnt(0)
	s_barrier
	s_setprio 1
	s_waitcnt lgkmcnt(6)
	v_mfma_scale_f32_16x16x128_f8f6f4 v[124:127], v[146:153], v[178:185], v[124:127], v142, v142 op_sel_hi:[0,0,0]
	v_mfma_scale_f32_16x16x128_f8f6f4 v[120:123], v[154:161], v[178:185], v[120:123], v142, v142 op_sel_hi:[0,0,0]
	s_waitcnt lgkmcnt(4)
	v_mfma_scale_f32_16x16x128_f8f6f4 v[116:119], v[146:153], v[186:193], v[116:119], v142, v142 op_sel_hi:[0,0,0]
	v_mfma_scale_f32_16x16x128_f8f6f4 v[112:115], v[154:161], v[186:193], v[112:115], v142, v142 op_sel_hi:[0,0,0]
	s_waitcnt lgkmcnt(2)
	v_mfma_scale_f32_16x16x128_f8f6f4 v[128:131], v[146:153], v[194:201], v[92:95], v142, v142 op_sel_hi:[0,0,0]
	v_mfma_scale_f32_16x16x128_f8f6f4 v[210:213], v[154:161], v[194:201], v[88:91], v142, v142 op_sel_hi:[0,0,0]
	s_waitcnt lgkmcnt(0)
	v_mfma_scale_f32_16x16x128_f8f6f4 v[214:217], v[146:153], v[202:209], v[84:87], v142, v142 op_sel_hi:[0,0,0]
	v_mfma_scale_f32_16x16x128_f8f6f4 v[218:221], v[154:161], v[202:209], v[80:83], v142, v142 op_sel_hi:[0,0,0]
	s_setprio 0
	s_setprio 1
	v_mfma_scale_f32_16x16x128_f8f6f4 v[108:111], v[162:169], v[178:185], v[108:111], v142, v142 op_sel_hi:[0,0,0]
	v_mfma_scale_f32_16x16x128_f8f6f4 v[104:107], v[170:177], v[178:185], v[104:107], v142, v142 op_sel_hi:[0,0,0]
	v_mfma_scale_f32_16x16x128_f8f6f4 v[100:103], v[162:169], v[186:193], v[100:103], v142, v142 op_sel_hi:[0,0,0]
	v_mfma_scale_f32_16x16x128_f8f6f4 v[96:99], v[170:177], v[186:193], v[96:99], v142, v142 op_sel_hi:[0,0,0]
	v_mfma_scale_f32_16x16x128_f8f6f4 v[178:181], v[162:169], v[194:201], v[76:79], v142, v142 op_sel_hi:[0,0,0]
	v_mfma_scale_f32_16x16x128_f8f6f4 v[182:185], v[170:177], v[194:201], v[72:75], v142, v142 op_sel_hi:[0,0,0]
	v_mfma_scale_f32_16x16x128_f8f6f4 v[186:189], v[162:169], v[202:209], v[68:71], v142, v142 op_sel_hi:[0,0,0]
	v_mfma_scale_f32_16x16x128_f8f6f4 v[190:193], v[170:177], v[202:209], v[64:67], v142, v142 op_sel_hi:[0,0,0]
	s_setprio 0
	s_barrier
	s_add_u32 s22, s30, 0x10000
	s_nop 3
	ds_read_b128 v[64:67], v141 offset:16384
	ds_read_b128 v[68:71], v141 offset:17408
	ds_read_b128 v[72:75], v141 offset:18432
	ds_read_b128 v[76:79], v141 offset:19456
	ds_read_b128 v[80:83], v141 offset:20480
	ds_read_b128 v[84:87], v141 offset:21504
	ds_read_b128 v[88:91], v141 offset:22528
	ds_read_b128 v[92:95], v141 offset:23552
	s_mov_b32 s15, m0
	s_mov_b32 m0, s36
	s_nop 0
	global_load_lds_dwordx4 v136, s[30:31]
	s_mov_b32 m0, s15
	s_addc_u32 s23, s31, 0
	s_mov_b32 s15, m0
	s_mov_b32 m0, s37
	s_nop 0
	global_load_lds_dwordx4 v136, s[22:23]
	s_mov_b32 m0, s15
	s_add_u32 s22, s30, 0x20000
	s_addc_u32 s23, s31, 0
	s_mov_b32 s15, m0
	s_mov_b32 m0, s38
	s_nop 0
	global_load_lds_dwordx4 v136, s[22:23]
	s_mov_b32 m0, s15
	s_add_u32 s22, s30, 0x30000
	s_addc_u32 s23, s31, 0
	s_mov_b32 s15, m0
	s_mov_b32 m0, s39
	s_nop 0
	global_load_lds_dwordx4 v136, s[22:23]
	s_mov_b32 m0, s15
	s_waitcnt vmcnt(6)
	s_waitcnt lgkmcnt(0)
	s_barrier
	s_setprio 1
	s_waitcnt lgkmcnt(6)
	v_mfma_scale_f32_16x16x128_f8f6f4 v[60:63], v[146:153], v[64:71], v[60:63], v142, v142 op_sel_hi:[0,0,0]
	v_mfma_scale_f32_16x16x128_f8f6f4 v[56:59], v[154:161], v[64:71], v[56:59], v142, v142 op_sel_hi:[0,0,0]
	s_waitcnt lgkmcnt(4)
	v_mfma_scale_f32_16x16x128_f8f6f4 v[52:55], v[146:153], v[72:79], v[52:55], v142, v142 op_sel_hi:[0,0,0]
	v_mfma_scale_f32_16x16x128_f8f6f4 v[48:51], v[154:161], v[72:79], v[48:51], v142, v142 op_sel_hi:[0,0,0]
	s_waitcnt lgkmcnt(2)
	v_mfma_scale_f32_16x16x128_f8f6f4 v[194:197], v[146:153], v[80:87], v[28:31], v142, v142 op_sel_hi:[0,0,0]
	v_mfma_scale_f32_16x16x128_f8f6f4 v[198:201], v[154:161], v[80:87], v[24:27], v142, v142 op_sel_hi:[0,0,0]
	s_waitcnt lgkmcnt(0)
	v_mfma_scale_f32_16x16x128_f8f6f4 v[202:205], v[146:153], v[88:95], v[12:15], v142, v142 op_sel_hi:[0,0,0]
	v_mfma_scale_f32_16x16x128_f8f6f4 v[206:209], v[154:161], v[88:95], v[8:11], v142, v142 op_sel_hi:[0,0,0]
	s_setprio 0
	s_setprio 1
	v_mfma_scale_f32_16x16x128_f8f6f4 v[222:225], v[162:169], v[64:71], v[44:47], v142, v142 op_sel_hi:[0,0,0]
	v_mfma_scale_f32_16x16x128_f8f6f4 v[226:229], v[170:177], v[64:71], v[40:43], v142, v142 op_sel_hi:[0,0,0]
	v_mfma_scale_f32_16x16x128_f8f6f4 v[230:233], v[162:169], v[72:79], v[36:39], v142, v142 op_sel_hi:[0,0,0]
	v_mfma_scale_f32_16x16x128_f8f6f4 v[234:237], v[170:177], v[72:79], v[32:35], v142, v142 op_sel_hi:[0,0,0]
	v_mfma_scale_f32_16x16x128_f8f6f4 v[238:241], v[162:169], v[80:87], v[20:23], v142, v142 op_sel_hi:[0,0,0]
	v_mfma_scale_f32_16x16x128_f8f6f4 v[242:245], v[170:177], v[80:87], v[16:19], v142, v142 op_sel_hi:[0,0,0]
	v_mfma_scale_f32_16x16x128_f8f6f4 v[246:249], v[162:169], v[88:95], v[4:7], v142, v142 op_sel_hi:[0,0,0]
	v_mfma_scale_f32_16x16x128_f8f6f4 v[250:253], v[170:177], v[88:95], v[0:3], v142, v142 op_sel_hi:[0,0,0]
	s_setprio 0
	s_barrier
	s_nop 4
	ds_read_b128 v[0:3], v143
	ds_read_b128 v[4:7], v143 offset:1024
	ds_read_b128 v[16:19], v143 offset:2048
	ds_read_b128 v[20:23], v143 offset:3072
	ds_read_b128 v[146:149], v144
	ds_read_b128 v[150:153], v144 offset:1024
	ds_read_b128 v[154:157], v144 offset:2048
	ds_read_b128 v[158:161], v144 offset:3072
	ds_read_b128 v[8:11], v141 offset:32768
	ds_read_b128 v[12:15], v141 offset:33792
	ds_read_b128 v[24:27], v141 offset:34816
	ds_read_b128 v[28:31], v141 offset:35840
	ds_read_b128 v[32:35], v141 offset:36864
	ds_read_b128 v[36:39], v141 offset:37888
	ds_read_b128 v[40:43], v141 offset:38912
	ds_read_b128 v[44:47], v141 offset:39936
	s_add_u32 s22, s26, 0x10000
	s_mov_b32 s15, m0
	s_mov_b32 m0, s35
	s_nop 0
	global_load_lds_dwordx4 v137, s[26:27]
	s_mov_b32 m0, s15
	s_addc_u32 s23, s27, 0
	s_mov_b32 s15, m0
	s_mov_b32 m0, s40
	s_nop 0
	global_load_lds_dwordx4 v137, s[22:23]
	s_mov_b32 m0, s15
	s_add_u32 s22, s26, 0x20000
	s_addc_u32 s23, s27, 0
	s_mov_b32 s15, m0
	s_mov_b32 m0, s41
	s_nop 0
	global_load_lds_dwordx4 v137, s[22:23]
	s_mov_b32 m0, s15
	s_add_u32 s22, s26, 0x30000
	s_addc_u32 s23, s27, 0
	s_mov_b32 s15, m0
	s_mov_b32 m0, s42
	s_nop 0
	global_load_lds_dwordx4 v137, s[22:23]
	s_mov_b32 m0, s15
	s_waitcnt vmcnt(8)
	s_waitcnt lgkmcnt(0)
	s_barrier
	s_setprio 1
	s_waitcnt lgkmcnt(6)
	v_mfma_scale_f32_16x16x128_f8f6f4 v[124:127], v[0:7], v[8:15], v[124:127], v142, v142 op_sel_hi:[0,0,0]
	v_mfma_scale_f32_16x16x128_f8f6f4 v[120:123], v[16:23], v[8:15], v[120:123], v142, v142 op_sel_hi:[0,0,0]
	s_waitcnt lgkmcnt(4)
	v_mfma_scale_f32_16x16x128_f8f6f4 v[116:119], v[0:7], v[24:31], v[116:119], v142, v142 op_sel_hi:[0,0,0]
	v_mfma_scale_f32_16x16x128_f8f6f4 v[112:115], v[16:23], v[24:31], v[112:115], v142, v142 op_sel_hi:[0,0,0]
	s_waitcnt lgkmcnt(2)
	v_mfma_scale_f32_16x16x128_f8f6f4 v[92:95], v[0:7], v[32:39], v[128:131], v142, v142 op_sel_hi:[0,0,0]
	v_mfma_scale_f32_16x16x128_f8f6f4 v[88:91], v[16:23], v[32:39], v[210:213], v142, v142 op_sel_hi:[0,0,0]
	s_waitcnt lgkmcnt(0)
	v_mfma_scale_f32_16x16x128_f8f6f4 v[84:87], v[0:7], v[40:47], v[214:217], v142, v142 op_sel_hi:[0,0,0]
	v_mfma_scale_f32_16x16x128_f8f6f4 v[80:83], v[16:23], v[40:47], v[218:221], v142, v142 op_sel_hi:[0,0,0]
	s_setprio 0
	s_setprio 1
	v_mfma_scale_f32_16x16x128_f8f6f4 v[108:111], v[146:153], v[8:15], v[108:111], v142, v142 op_sel_hi:[0,0,0]
	v_mfma_scale_f32_16x16x128_f8f6f4 v[104:107], v[154:161], v[8:15], v[104:107], v142, v142 op_sel_hi:[0,0,0]
	v_mfma_scale_f32_16x16x128_f8f6f4 v[100:103], v[146:153], v[24:31], v[100:103], v142, v142 op_sel_hi:[0,0,0]
	v_mfma_scale_f32_16x16x128_f8f6f4 v[96:99], v[154:161], v[24:31], v[96:99], v142, v142 op_sel_hi:[0,0,0]
	v_mfma_scale_f32_16x16x128_f8f6f4 v[76:79], v[146:153], v[32:39], v[178:181], v142, v142 op_sel_hi:[0,0,0]
	v_mfma_scale_f32_16x16x128_f8f6f4 v[72:75], v[154:161], v[32:39], v[182:185], v142, v142 op_sel_hi:[0,0,0]
	v_mfma_scale_f32_16x16x128_f8f6f4 v[68:71], v[146:153], v[40:47], v[186:189], v142, v142 op_sel_hi:[0,0,0]
	v_mfma_scale_f32_16x16x128_f8f6f4 v[64:67], v[154:161], v[40:47], v[190:193], v142, v142 op_sel_hi:[0,0,0]
	s_setprio 0
	s_barrier
	s_add_u32 s22, s30, 0x80
	s_addc_u32 s23, s31, 0
	ds_read_b128 v[32:35], v141 offset:49152
	ds_read_b128 v[36:39], v141 offset:50176
	ds_read_b128 v[162:165], v141 offset:51200
	ds_read_b128 v[166:169], v141 offset:52224
	ds_read_b128 v[170:173], v141 offset:53248
	ds_read_b128 v[174:177], v141 offset:54272
	ds_read_b128 v[178:181], v141 offset:55296
	ds_read_b128 v[182:185], v141 offset:56320
	s_mov_b32 s15, m0
	s_mov_b32 m0, s45
	s_nop 0
	global_load_lds_dwordx4 v136, s[22:23]
	s_mov_b32 m0, s15
	s_add_u32 s22, s30, 0x10080
	s_addc_u32 s23, s31, 0
	s_mov_b32 s15, m0
	s_mov_b32 m0, s47
	s_nop 0
	global_load_lds_dwordx4 v136, s[22:23]
	s_mov_b32 m0, s15
	s_add_u32 s22, s30, 0x20080
	s_addc_u32 s23, s31, 0
	s_mov_b32 s15, m0
	s_mov_b32 m0, s50
	s_nop 0
	global_load_lds_dwordx4 v136, s[22:23]
	s_mov_b32 m0, s15
	s_add_u32 s22, s30, 0x30080
	s_addc_u32 s23, s31, 0
	s_mov_b32 s15, m0
	s_mov_b32 m0, s51
	s_nop 0
	global_load_lds_dwordx4 v136, s[22:23]
	s_mov_b32 m0, s15
	s_add_u32 s22, s26, 0x10080
	s_mov_b32 s15, m0
	s_mov_b32 m0, s48
	s_nop 0
	global_load_lds_dwordx4 v137, s[28:29]
	s_mov_b32 m0, s15
	s_addc_u32 s23, s27, 0
	s_mov_b32 s15, m0
	s_mov_b32 m0, s49
	s_nop 0
	global_load_lds_dwordx4 v137, s[22:23]
	s_mov_b32 m0, s15
	s_waitcnt vmcnt(8)
	s_waitcnt lgkmcnt(0)
	s_barrier
	s_setprio 1
	s_waitcnt lgkmcnt(6)
	v_mfma_scale_f32_16x16x128_f8f6f4 v[60:63], v[0:7], v[32:39], v[60:63], v142, v142 op_sel_hi:[0,0,0]
	v_mfma_scale_f32_16x16x128_f8f6f4 v[56:59], v[16:23], v[32:39], v[56:59], v142, v142 op_sel_hi:[0,0,0]
	s_waitcnt lgkmcnt(4)
	v_mfma_scale_f32_16x16x128_f8f6f4 v[52:55], v[0:7], v[162:169], v[52:55], v142, v142 op_sel_hi:[0,0,0]
	v_mfma_scale_f32_16x16x128_f8f6f4 v[48:51], v[16:23], v[162:169], v[48:51], v142, v142 op_sel_hi:[0,0,0]
	s_waitcnt lgkmcnt(2)
	v_mfma_scale_f32_16x16x128_f8f6f4 v[28:31], v[0:7], v[170:177], v[194:197], v142, v142 op_sel_hi:[0,0,0]
	v_mfma_scale_f32_16x16x128_f8f6f4 v[24:27], v[16:23], v[170:177], v[198:201], v142, v142 op_sel_hi:[0,0,0]
	s_waitcnt lgkmcnt(0)
	v_mfma_scale_f32_16x16x128_f8f6f4 v[12:15], v[0:7], v[178:185], v[202:205], v142, v142 op_sel_hi:[0,0,0]
	v_mfma_scale_f32_16x16x128_f8f6f4 v[8:11], v[16:23], v[178:185], v[206:209], v142, v142 op_sel_hi:[0,0,0]
	s_setprio 0
	s_setprio 1
	v_mfma_scale_f32_16x16x128_f8f6f4 v[44:47], v[146:153], v[32:39], v[222:225], v142, v142 op_sel_hi:[0,0,0]
	v_mfma_scale_f32_16x16x128_f8f6f4 v[40:43], v[154:161], v[32:39], v[226:229], v142, v142 op_sel_hi:[0,0,0]
	v_mfma_scale_f32_16x16x128_f8f6f4 v[36:39], v[146:153], v[162:169], v[230:233], v142, v142 op_sel_hi:[0,0,0]
	v_mfma_scale_f32_16x16x128_f8f6f4 v[32:35], v[154:161], v[162:169], v[234:237], v142, v142 op_sel_hi:[0,0,0]
	v_mfma_scale_f32_16x16x128_f8f6f4 v[20:23], v[146:153], v[170:177], v[238:241], v142, v142 op_sel_hi:[0,0,0]
	v_mfma_scale_f32_16x16x128_f8f6f4 v[16:19], v[154:161], v[170:177], v[242:245], v142, v142 op_sel_hi:[0,0,0]
	v_mfma_scale_f32_16x16x128_f8f6f4 v[4:7], v[146:153], v[178:185], v[246:249], v142, v142 op_sel_hi:[0,0,0]
	v_mfma_scale_f32_16x16x128_f8f6f4 v[0:3], v[154:161], v[178:185], v[250:253], v142, v142 op_sel_hi:[0,0,0]
	s_setprio 0
	s_barrier
	s_add_i32 s13, s13, 2
	s_add_u32 s1, s1, 0x100
	s_addc_u32 s11, s11, 0
	s_cmp_gt_u32 s13, 5
	s_mov_b64 s[22:23], s[24:25]
	s_cbranch_scc0 .LBB0_645
	s_and_b64 vcc, exec, s[8:9]
	s_cbranch_vccz .LBB0_648
	s_barrier

.LBB0_799:
	s_ashr_i32 s7, s6, 31
	s_lshl_b64 s[10:11], s[6:7], 18
	s_add_u32 s10, s33, s10
	s_addc_u32 s11, s34, s11
	s_and_b64 s[14:15], s[12:13], exec
	ds_read_b128 v[0:3], v135
	ds_read_b128 v[4:7], v135 offset:1024
	ds_read_b128 v[8:11], v135 offset:2048
	ds_read_b128 v[12:15], v135 offset:3072
	ds_read_b128 v[16:19], v136
	ds_read_b128 v[20:23], v136 offset:1024
	ds_read_b128 v[24:27], v136 offset:2048
	ds_read_b128 v[28:31], v136 offset:3072
	s_cselect_b32 s7, s11, s23
	s_cselect_b32 s53, s10, s22
	s_ashr_i32 s9, s8, 31
	s_lshl_b64 s[14:15], s[8:9], 18
	s_add_u32 s14, s30, s14
	s_addc_u32 s15, s31, s15
	s_and_b64 s[24:25], s[12:13], exec
	s_cselect_b32 s9, s15, s21
	s_cselect_b32 s54, s14, s20
	s_add_u32 s24, s22, 0x100
	s_addc_u32 s25, s23, 0
	s_add_u32 s26, s22, 0x180
	s_addc_u32 s27, s23, 0
	s_add_u32 s28, s20, 0x100
	s_addc_u32 s29, s21, 0
	ds_read_b128 v[32:35], v137
	ds_read_b128 v[36:39], v137 offset:1024
	ds_read_b128 v[40:43], v137 offset:2048
	ds_read_b128 v[44:47], v137 offset:3072
	ds_read_b128 v[48:51], v137 offset:4096
	ds_read_b128 v[52:55], v137 offset:5120
	ds_read_b128 v[56:59], v137 offset:6144
	ds_read_b128 v[60:63], v137 offset:7168
	s_add_u32 s56, s22, 0x20080
	s_addc_u32 s57, s23, 0
	s_mov_b32 s55, m0
	s_mov_b32 m0, s50
	s_nop 0
	global_load_lds_dwordx4 v134, s[56:57]
	s_mov_b32 m0, s55
	s_add_u32 s56, s22, 0x30080
	s_addc_u32 s57, s23, 0
	s_mov_b32 s55, m0
	s_mov_b32 m0, s51
	s_nop 0
	global_load_lds_dwordx4 v134, s[56:57]
	s_mov_b32 m0, s55
	s_waitcnt vmcnt(8)
	s_waitcnt lgkmcnt(0)
	s_barrier
	s_setprio 1
	s_waitcnt lgkmcnt(6)
	v_mfma_scale_f32_16x16x128_f8f6f4 v[64:67], v[0:7], v[32:39], 0, v138, v138 op_sel_hi:[0,0,0]
	v_mfma_scale_f32_16x16x128_f8f6f4 v[68:71], v[8:15], v[32:39], 0, v138, v138 op_sel_hi:[0,0,0]
	s_waitcnt lgkmcnt(4)
	v_mfma_scale_f32_16x16x128_f8f6f4 v[72:75], v[0:7], v[40:47], 0, v138, v138 op_sel_hi:[0,0,0]
	v_mfma_scale_f32_16x16x128_f8f6f4 v[76:79], v[8:15], v[40:47], 0, v138, v138 op_sel_hi:[0,0,0]
	s_waitcnt lgkmcnt(2)
	v_mfma_scale_f32_16x16x128_f8f6f4 v[80:83], v[0:7], v[48:55], 0, v138, v138 op_sel_hi:[0,0,0]
	v_mfma_scale_f32_16x16x128_f8f6f4 v[88:91], v[8:15], v[48:55], 0, v138, v138 op_sel_hi:[0,0,0]
	s_waitcnt lgkmcnt(0)
	v_mfma_scale_f32_16x16x128_f8f6f4 v[108:111], v[0:7], v[56:63], 0, v138, v138 op_sel_hi:[0,0,0]
	v_mfma_scale_f32_16x16x128_f8f6f4 v[116:119], v[8:15], v[56:63], 0, v138, v138 op_sel_hi:[0,0,0]
	s_setprio 0
	s_setprio 1
	v_mfma_scale_f32_16x16x128_f8f6f4 v[120:123], v[16:23], v[32:39], 0, v138, v138 op_sel_hi:[0,0,0]
	v_mfma_scale_f32_16x16x128_f8f6f4 v[124:127], v[24:31], v[32:39], 0, v138, v138 op_sel_hi:[0,0,0]
	v_mfma_scale_f32_16x16x128_f8f6f4 v[128:131], v[16:23], v[40:47], 0, v138, v138 op_sel_hi:[0,0,0]
	v_mfma_scale_f32_16x16x128_f8f6f4 v[158:161], v[24:31], v[40:47], 0, v138, v138 op_sel_hi:[0,0,0]
	v_mfma_scale_f32_16x16x128_f8f6f4 v[162:165], v[16:23], v[48:55], 0, v138, v138 op_sel_hi:[0,0,0]
	v_mfma_scale_f32_16x16x128_f8f6f4 v[166:169], v[24:31], v[48:55], 0, v138, v138 op_sel_hi:[0,0,0]
	v_mfma_scale_f32_16x16x128_f8f6f4 v[170:173], v[16:23], v[56:63], 0, v138, v138 op_sel_hi:[0,0,0]
	v_mfma_scale_f32_16x16x128_f8f6f4 v[174:177], v[24:31], v[56:63], 0, v138, v138 op_sel_hi:[0,0,0]
	s_setprio 0
	s_barrier
	ds_read_b128 v[32:35], v137 offset:16384
	ds_read_b128 v[36:39], v137 offset:17408
	ds_read_b128 v[40:43], v137 offset:18432
	ds_read_b128 v[44:47], v137 offset:19456
	ds_read_b128 v[48:51], v137 offset:20480
	ds_read_b128 v[52:55], v137 offset:21504
	ds_read_b128 v[56:59], v137 offset:22528
	ds_read_b128 v[60:63], v137 offset:23552
	s_mov_b32 s55, m0
	s_mov_b32 m0, s17
	s_nop 0
	global_load_lds_dwordx4 v133, s[28:29]
	s_mov_b32 m0, s55
	s_add_u32 s28, s20, 0x10100
	s_addc_u32 s29, s21, 0
	s_mov_b32 s55, m0
	s_mov_b32 m0, s19
	s_nop 0
	global_load_lds_dwordx4 v133, s[28:29]
	s_mov_b32 m0, s55
	s_add_u32 s28, s20, 0x20100
	s_addc_u32 s29, s21, 0
	s_mov_b32 s55, m0
	s_mov_b32 m0, s36
	s_nop 0
	global_load_lds_dwordx4 v133, s[28:29]
	s_mov_b32 m0, s55
	s_add_u32 s28, s20, 0x30100
	s_addc_u32 s29, s21, 0
	s_mov_b32 s55, m0
	s_mov_b32 m0, s37
	s_nop 0
	global_load_lds_dwordx4 v133, s[28:29]
	s_mov_b32 m0, s55
	s_waitcnt vmcnt(6)
	s_waitcnt lgkmcnt(0)
	s_barrier
	s_setprio 1
	s_waitcnt lgkmcnt(6)
	v_mfma_scale_f32_16x16x128_f8f6f4 v[190:193], v[0:7], v[32:39], 0, v138, v138 op_sel_hi:[0,0,0]
	v_mfma_scale_f32_16x16x128_f8f6f4 v[194:197], v[8:15], v[32:39], 0, v138, v138 op_sel_hi:[0,0,0]
	s_waitcnt lgkmcnt(4)
	v_mfma_scale_f32_16x16x128_f8f6f4 v[198:201], v[0:7], v[40:47], 0, v138, v138 op_sel_hi:[0,0,0]
	v_mfma_scale_f32_16x16x128_f8f6f4 v[202:205], v[8:15], v[40:47], 0, v138, v138 op_sel_hi:[0,0,0]
	s_waitcnt lgkmcnt(2)
	v_mfma_scale_f32_16x16x128_f8f6f4 v[206:209], v[0:7], v[48:55], 0, v138, v138 op_sel_hi:[0,0,0]
	v_mfma_scale_f32_16x16x128_f8f6f4 v[210:213], v[8:15], v[48:55], 0, v138, v138 op_sel_hi:[0,0,0]
	s_waitcnt lgkmcnt(0)
	v_mfma_scale_f32_16x16x128_f8f6f4 v[214:217], v[0:7], v[56:63], 0, v138, v138 op_sel_hi:[0,0,0]
	v_mfma_scale_f32_16x16x128_f8f6f4 v[218:221], v[8:15], v[56:63], 0, v138, v138 op_sel_hi:[0,0,0]
	s_setprio 0
	s_setprio 1
	v_mfma_scale_f32_16x16x128_f8f6f4 v[222:225], v[16:23], v[32:39], 0, v138, v138 op_sel_hi:[0,0,0]
	v_mfma_scale_f32_16x16x128_f8f6f4 v[226:229], v[24:31], v[32:39], 0, v138, v138 op_sel_hi:[0,0,0]
	v_mfma_scale_f32_16x16x128_f8f6f4 v[230:233], v[16:23], v[40:47], 0, v138, v138 op_sel_hi:[0,0,0]
	v_mfma_scale_f32_16x16x128_f8f6f4 v[234:237], v[24:31], v[40:47], 0, v138, v138 op_sel_hi:[0,0,0]
	v_mfma_scale_f32_16x16x128_f8f6f4 v[238:241], v[16:23], v[48:55], 0, v138, v138 op_sel_hi:[0,0,0]
	v_mfma_scale_f32_16x16x128_f8f6f4 v[242:245], v[24:31], v[48:55], 0, v138, v138 op_sel_hi:[0,0,0]
	v_mfma_scale_f32_16x16x128_f8f6f4 v[246:249], v[16:23], v[56:63], 0, v138, v138 op_sel_hi:[0,0,0]
	v_mfma_scale_f32_16x16x128_f8f6f4 v[250:253], v[24:31], v[56:63], 0, v138, v138 op_sel_hi:[0,0,0]
	s_setprio 0
	s_barrier
	ds_read_b128 v[0:3], v139
	ds_read_b128 v[4:7], v139 offset:1024
	ds_read_b128 v[96:99], v139 offset:2048
	ds_read_b128 v[100:103], v139 offset:3072
	ds_read_b128 v[142:145], v140
	ds_read_b128 v[146:149], v140 offset:1024
	ds_read_b128 v[150:153], v140 offset:2048
	ds_read_b128 v[154:157], v140 offset:3072
	ds_read_b128 v[8:11], v137 offset:32768
	ds_read_b128 v[12:15], v137 offset:33792
	ds_read_b128 v[16:19], v137 offset:34816
	ds_read_b128 v[20:23], v137 offset:35840
	ds_read_b128 v[28:31], v137 offset:36864
	ds_read_b128 v[32:35], v137 offset:37888
	ds_read_b128 v[56:59], v137 offset:38912
	ds_read_b128 v[60:63], v137 offset:39936
	s_mov_b32 s28, m0
	s_mov_b32 m0, s35
	s_nop 0
	global_load_lds_dwordx4 v134, s[24:25]
	s_mov_b32 m0, s28
	s_add_u32 s28, s22, 0x10100
	s_addc_u32 s29, s23, 0
	s_mov_b32 s55, m0
	s_mov_b32 m0, s38
	s_nop 0
	global_load_lds_dwordx4 v134, s[28:29]
	s_mov_b32 m0, s55
	s_add_u32 s28, s22, 0x20100
	s_addc_u32 s29, s23, 0
	s_mov_b32 s55, m0
	s_mov_b32 m0, s39
	s_nop 0
	global_load_lds_dwordx4 v134, s[28:29]
	s_mov_b32 m0, s55
	s_add_u32 s28, s22, 0x30100
	s_addc_u32 s29, s23, 0
	s_mov_b32 s55, m0
	s_mov_b32 m0, s40
	s_nop 0
	global_load_lds_dwordx4 v134, s[28:29]
	s_mov_b32 m0, s55
	s_waitcnt vmcnt(8)
	s_waitcnt lgkmcnt(0)
	s_barrier
	s_setprio 1
	s_waitcnt lgkmcnt(6)
	v_mfma_scale_f32_16x16x128_f8f6f4 v[104:107], v[0:7], v[8:15], v[64:67], v138, v138 op_sel_hi:[0,0,0]
	v_mfma_scale_f32_16x16x128_f8f6f4 v[112:115], v[96:103], v[8:15], v[68:71], v138, v138 op_sel_hi:[0,0,0]
	s_waitcnt lgkmcnt(4)
	v_mfma_scale_f32_16x16x128_f8f6f4 v[92:95], v[0:7], v[16:23], v[72:75], v138, v138 op_sel_hi:[0,0,0]
	v_mfma_scale_f32_16x16x128_f8f6f4 v[84:87], v[96:103], v[16:23], v[76:79], v138, v138 op_sel_hi:[0,0,0]
	s_waitcnt lgkmcnt(2)
	v_mfma_scale_f32_16x16x128_f8f6f4 v[64:67], v[0:7], v[28:35], v[80:83], v138, v138 op_sel_hi:[0,0,0]
	v_mfma_scale_f32_16x16x128_f8f6f4 v[52:55], v[96:103], v[28:35], v[88:91], v138, v138 op_sel_hi:[0,0,0]
	s_waitcnt lgkmcnt(0)
	v_mfma_scale_f32_16x16x128_f8f6f4 v[36:39], v[0:7], v[56:63], v[108:111], v138, v138 op_sel_hi:[0,0,0]
	v_mfma_scale_f32_16x16x128_f8f6f4 v[24:27], v[96:103], v[56:63], v[116:119], v138, v138 op_sel_hi:[0,0,0]
	s_setprio 0
	s_setprio 1
	v_mfma_scale_f32_16x16x128_f8f6f4 v[120:123], v[142:149], v[8:15], v[120:123], v138, v138 op_sel_hi:[0,0,0]
	v_mfma_scale_f32_16x16x128_f8f6f4 v[124:127], v[150:157], v[8:15], v[124:127], v138, v138 op_sel_hi:[0,0,0]
	v_mfma_scale_f32_16x16x128_f8f6f4 v[116:119], v[142:149], v[16:23], v[128:131], v138, v138 op_sel_hi:[0,0,0]
	v_mfma_scale_f32_16x16x128_f8f6f4 v[108:111], v[150:157], v[16:23], v[158:161], v138, v138 op_sel_hi:[0,0,0]
	v_mfma_scale_f32_16x16x128_f8f6f4 v[76:79], v[142:149], v[28:35], v[162:165], v138, v138 op_sel_hi:[0,0,0]
	v_mfma_scale_f32_16x16x128_f8f6f4 v[72:75], v[150:157], v[28:35], v[166:169], v138, v138 op_sel_hi:[0,0,0]
	v_mfma_scale_f32_16x16x128_f8f6f4 v[44:47], v[142:149], v[56:63], v[170:173], v138, v138 op_sel_hi:[0,0,0]
	v_mfma_scale_f32_16x16x128_f8f6f4 v[40:43], v[150:157], v[56:63], v[174:177], v138, v138 op_sel_hi:[0,0,0]
	s_setprio 0
	s_barrier
	s_add_u32 s28, s20, 0x180
	s_addc_u32 s29, s21, 0
	ds_read_b128 v[158:161], v137 offset:49152
	ds_read_b128 v[162:165], v137 offset:50176
	ds_read_b128 v[166:169], v137 offset:51200
	ds_read_b128 v[170:173], v137 offset:52224
	ds_read_b128 v[174:177], v137 offset:53248
	ds_read_b128 v[178:181], v137 offset:54272
	ds_read_b128 v[182:185], v137 offset:55296
	ds_read_b128 v[186:189], v137 offset:56320
	s_mov_b32 s55, m0
	s_mov_b32 m0, s44
	s_nop 0
	global_load_lds_dwordx4 v133, s[28:29]
	s_mov_b32 m0, s55
	s_add_u32 s28, s20, 0x10180
	s_addc_u32 s29, s21, 0
	s_mov_b32 s55, m0
	s_mov_b32 m0, s45
	s_nop 0
	global_load_lds_dwordx4 v133, s[28:29]
	s_mov_b32 m0, s55
	s_add_u32 s28, s20, 0x20180
	s_addc_u32 s29, s21, 0
	s_mov_b32 s55, m0
	s_mov_b32 m0, s48
	s_nop 0
	global_load_lds_dwordx4 v133, s[28:29]
	s_mov_b32 m0, s55
	s_add_u32 s28, s20, 0x30180
	s_addc_u32 s29, s21, 0
	s_mov_b32 s55, m0
	s_mov_b32 m0, s49
	s_nop 0
	global_load_lds_dwordx4 v133, s[28:29]
	s_mov_b32 m0, s55
	s_mov_b32 s28, m0
	s_mov_b32 m0, s46
	s_nop 0
	global_load_lds_dwordx4 v134, s[26:27]
	s_mov_b32 m0, s28
	s_add_u32 s22, s22, 0x10180
	s_addc_u32 s23, s23, 0
	s_mov_b32 s26, m0
	s_mov_b32 m0, s47
	s_nop 0
	global_load_lds_dwordx4 v134, s[22:23]
	s_mov_b32 m0, s26
	s_waitcnt vmcnt(8)
	s_waitcnt lgkmcnt(0)
	s_barrier
	s_setprio 1
	s_waitcnt lgkmcnt(6)
	v_mfma_scale_f32_16x16x128_f8f6f4 v[88:91], v[0:7], v[158:165], v[190:193], v138, v138 op_sel_hi:[0,0,0]
	v_mfma_scale_f32_16x16x128_f8f6f4 v[80:83], v[96:103], v[158:165], v[194:197], v138, v138 op_sel_hi:[0,0,0]
	s_waitcnt lgkmcnt(4)
	v_mfma_scale_f32_16x16x128_f8f6f4 v[56:59], v[0:7], v[166:173], v[198:201], v138, v138 op_sel_hi:[0,0,0]
	v_mfma_scale_f32_16x16x128_f8f6f4 v[48:51], v[96:103], v[166:173], v[202:205], v138, v138 op_sel_hi:[0,0,0]
	s_waitcnt lgkmcnt(2)
	v_mfma_scale_f32_16x16x128_f8f6f4 v[28:31], v[0:7], v[174:181], v[206:209], v138, v138 op_sel_hi:[0,0,0]
	v_mfma_scale_f32_16x16x128_f8f6f4 v[16:19], v[96:103], v[174:181], v[210:213], v138, v138 op_sel_hi:[0,0,0]
	s_waitcnt lgkmcnt(0)
	v_mfma_scale_f32_16x16x128_f8f6f4 v[12:15], v[0:7], v[182:189], v[214:217], v138, v138 op_sel_hi:[0,0,0]
	v_mfma_scale_f32_16x16x128_f8f6f4 v[8:11], v[96:103], v[182:189], v[218:221], v138, v138 op_sel_hi:[0,0,0]
	s_setprio 0
	s_setprio 1
	v_mfma_scale_f32_16x16x128_f8f6f4 v[100:103], v[142:149], v[158:165], v[222:225], v138, v138 op_sel_hi:[0,0,0]
	v_mfma_scale_f32_16x16x128_f8f6f4 v[96:99], v[150:157], v[158:165], v[226:229], v138, v138 op_sel_hi:[0,0,0]
	v_mfma_scale_f32_16x16x128_f8f6f4 v[68:71], v[142:149], v[166:173], v[230:233], v138, v138 op_sel_hi:[0,0,0]
	v_mfma_scale_f32_16x16x128_f8f6f4 v[60:63], v[150:157], v[166:173], v[234:237], v138, v138 op_sel_hi:[0,0,0]
	v_mfma_scale_f32_16x16x128_f8f6f4 v[32:35], v[142:149], v[174:181], v[238:241], v138, v138 op_sel_hi:[0,0,0]
	v_mfma_scale_f32_16x16x128_f8f6f4 v[20:23], v[150:157], v[174:181], v[242:245], v138, v138 op_sel_hi:[0,0,0]
	v_mfma_scale_f32_16x16x128_f8f6f4 v[4:7], v[142:149], v[182:189], v[246:249], v138, v138 op_sel_hi:[0,0,0]
	v_mfma_scale_f32_16x16x128_f8f6f4 v[0:3], v[150:157], v[182:189], v[250:253], v138, v138 op_sel_hi:[0,0,0]
	s_setprio 0
	s_barrier
	s_add_u32 s55, s20, 0x200
	s_addc_u32 s56, s21, 0
	s_mov_b32 s57, 0
.LBB0_800:
	ds_read_b128 v[142:145], v135
	ds_read_b128 v[146:149], v135 offset:1024
	ds_read_b128 v[150:153], v135 offset:2048
	ds_read_b128 v[154:157], v135 offset:3072
	ds_read_b128 v[158:161], v136
	ds_read_b128 v[162:165], v136 offset:1024
	ds_read_b128 v[166:169], v136 offset:2048
	ds_read_b128 v[170:173], v136 offset:3072
	s_add_u32 s20, s24, 0x100
	s_addc_u32 s21, s25, 0
	s_cmp_eq_u32 s57, 4
	s_cselect_b32 s22, s53, s20
	s_cselect_b32 s23, s7, s21
	s_cselect_b32 s28, s54, s55
	s_cselect_b32 s29, s9, s56
	s_add_u32 s26, s22, 0x80
	s_addc_u32 s27, s23, 0
	ds_read_b128 v[174:177], v137
	ds_read_b128 v[178:181], v137 offset:1024
	ds_read_b128 v[182:185], v137 offset:2048
	ds_read_b128 v[186:189], v137 offset:3072
	ds_read_b128 v[190:193], v137 offset:4096
	ds_read_b128 v[194:197], v137 offset:5120
	ds_read_b128 v[198:201], v137 offset:6144
	ds_read_b128 v[202:205], v137 offset:7168
	s_add_u32 s58, s24, 0x20080
	s_addc_u32 s59, s25, 0
	s_mov_b32 s60, m0
	s_mov_b32 m0, s50
	s_nop 0
	global_load_lds_dwordx4 v134, s[58:59]
	s_mov_b32 m0, s60
	s_add_u32 s24, s24, 0x30080
	s_addc_u32 s25, s25, 0
	s_mov_b32 s58, m0
	s_mov_b32 m0, s51
	s_nop 0
	global_load_lds_dwordx4 v134, s[24:25]
	s_mov_b32 m0, s58
	s_waitcnt vmcnt(8)
	s_waitcnt lgkmcnt(0)
	s_barrier
	s_setprio 1
	s_waitcnt lgkmcnt(4)
	v_mfma_scale_f32_16x16x128_f8f6f4 v[92:95], v[142:149], v[182:189], v[92:95], v138, v138 op_sel_hi:[0,0,0]
	v_mfma_scale_f32_16x16x128_f8f6f4 v[84:87], v[150:157], v[182:189], v[84:87], v138, v138 op_sel_hi:[0,0,0]
	s_waitcnt lgkmcnt(2)
	v_mfma_scale_f32_16x16x128_f8f6f4 v[64:67], v[142:149], v[190:197], v[64:67], v138, v138 op_sel_hi:[0,0,0]
	v_mfma_scale_f32_16x16x128_f8f6f4 v[52:55], v[150:157], v[190:197], v[52:55], v138, v138 op_sel_hi:[0,0,0]
	s_waitcnt lgkmcnt(0)
	v_mfma_scale_f32_16x16x128_f8f6f4 v[24:27], v[150:157], v[198:205], v[24:27], v138, v138 op_sel_hi:[0,0,0]
	v_mfma_scale_f32_16x16x128_f8f6f4 v[128:131], v[142:149], v[174:181], v[104:107], v138, v138 op_sel_hi:[0,0,0]
	v_mfma_scale_f32_16x16x128_f8f6f4 v[206:209], v[150:157], v[174:181], v[112:115], v138, v138 op_sel_hi:[0,0,0]
	v_mfma_scale_f32_16x16x128_f8f6f4 v[210:213], v[142:149], v[198:205], v[36:39], v138, v138 op_sel_hi:[0,0,0]
	s_setprio 0
	s_setprio 1
	v_mfma_scale_f32_16x16x128_f8f6f4 v[120:123], v[158:165], v[174:181], v[120:123], v138, v138 op_sel_hi:[0,0,0]
	v_mfma_scale_f32_16x16x128_f8f6f4 v[124:127], v[166:173], v[174:181], v[124:127], v138, v138 op_sel_hi:[0,0,0]
	v_mfma_scale_f32_16x16x128_f8f6f4 v[44:47], v[158:165], v[198:205], v[44:47], v138, v138 op_sel_hi:[0,0,0]
	v_mfma_scale_f32_16x16x128_f8f6f4 v[174:177], v[158:165], v[182:189], v[116:119], v138, v138 op_sel_hi:[0,0,0]
	v_mfma_scale_f32_16x16x128_f8f6f4 v[178:181], v[166:173], v[182:189], v[108:111], v138, v138 op_sel_hi:[0,0,0]
	v_mfma_scale_f32_16x16x128_f8f6f4 v[182:185], v[158:165], v[190:197], v[76:79], v138, v138 op_sel_hi:[0,0,0]
	v_mfma_scale_f32_16x16x128_f8f6f4 v[186:189], v[166:173], v[190:197], v[72:75], v138, v138 op_sel_hi:[0,0,0]
	v_mfma_scale_f32_16x16x128_f8f6f4 v[190:193], v[166:173], v[198:205], v[40:43], v138, v138 op_sel_hi:[0,0,0]
	s_setprio 0
	s_barrier
	ds_read_b128 v[36:39], v137 offset:16384
	s_nop 3
	ds_read_b128 v[40:43], v137 offset:17408
	ds_read_b128 v[72:75], v137 offset:18432
	ds_read_b128 v[76:79], v137 offset:19456
	ds_read_b128 v[104:107], v137 offset:20480
	ds_read_b128 v[108:111], v137 offset:21504
	ds_read_b128 v[112:115], v137 offset:22528
	ds_read_b128 v[116:119], v137 offset:23552
	s_mov_b32 s24, m0
	s_mov_b32 m0, s17
	s_nop 0
	global_load_lds_dwordx4 v133, s[28:29]
	s_mov_b32 m0, s24
	s_add_u32 s24, s28, 0x10000
	s_addc_u32 s25, s29, 0
	s_mov_b32 s58, m0
	s_mov_b32 m0, s19
	s_nop 0
	global_load_lds_dwordx4 v133, s[24:25]
	s_mov_b32 m0, s58
	s_add_u32 s24, s28, 0x20000
	s_addc_u32 s25, s29, 0
	s_mov_b32 s58, m0
	s_mov_b32 m0, s36
	s_nop 0
	global_load_lds_dwordx4 v133, s[24:25]
	s_mov_b32 m0, s58
	s_add_u32 s24, s28, 0x30000
	s_addc_u32 s25, s29, 0
	s_mov_b32 s58, m0
	s_mov_b32 m0, s37
	s_nop 0
	global_load_lds_dwordx4 v133, s[24:25]
	s_mov_b32 m0, s58
	s_waitcnt vmcnt(6)
	s_waitcnt lgkmcnt(0)
	s_barrier
	s_setprio 1
	s_waitcnt lgkmcnt(6)
	v_mfma_scale_f32_16x16x128_f8f6f4 v[88:91], v[142:149], v[36:43], v[88:91], v138, v138 op_sel_hi:[0,0,0]
	v_mfma_scale_f32_16x16x128_f8f6f4 v[80:83], v[150:157], v[36:43], v[80:83], v138, v138 op_sel_hi:[0,0,0]
	s_waitcnt lgkmcnt(4)
	v_mfma_scale_f32_16x16x128_f8f6f4 v[48:51], v[150:157], v[72:79], v[48:51], v138, v138 op_sel_hi:[0,0,0]
	v_mfma_scale_f32_16x16x128_f8f6f4 v[194:197], v[142:149], v[72:79], v[56:59], v138, v138 op_sel_hi:[0,0,0]
	s_waitcnt lgkmcnt(2)
	v_mfma_scale_f32_16x16x128_f8f6f4 v[198:201], v[142:149], v[104:111], v[28:31], v138, v138 op_sel_hi:[0,0,0]
	v_mfma_scale_f32_16x16x128_f8f6f4 v[202:205], v[150:157], v[104:111], v[16:19], v138, v138 op_sel_hi:[0,0,0]
	s_waitcnt lgkmcnt(0)
	v_mfma_scale_f32_16x16x128_f8f6f4 v[214:217], v[142:149], v[112:119], v[12:15], v138, v138 op_sel_hi:[0,0,0]
	v_mfma_scale_f32_16x16x128_f8f6f4 v[218:221], v[150:157], v[112:119], v[8:11], v138, v138 op_sel_hi:[0,0,0]
	s_setprio 0
	s_setprio 1
	v_mfma_scale_f32_16x16x128_f8f6f4 v[68:71], v[158:165], v[72:79], v[68:71], v138, v138 op_sel_hi:[0,0,0]
	v_mfma_scale_f32_16x16x128_f8f6f4 v[222:225], v[158:165], v[36:43], v[100:103], v138, v138 op_sel_hi:[0,0,0]
	v_mfma_scale_f32_16x16x128_f8f6f4 v[226:229], v[166:173], v[36:43], v[96:99], v138, v138 op_sel_hi:[0,0,0]
	v_mfma_scale_f32_16x16x128_f8f6f4 v[230:233], v[166:173], v[72:79], v[60:63], v138, v138 op_sel_hi:[0,0,0]
	v_mfma_scale_f32_16x16x128_f8f6f4 v[234:237], v[158:165], v[104:111], v[32:35], v138, v138 op_sel_hi:[0,0,0]
	v_mfma_scale_f32_16x16x128_f8f6f4 v[238:241], v[166:173], v[104:111], v[20:23], v138, v138 op_sel_hi:[0,0,0]
	v_mfma_scale_f32_16x16x128_f8f6f4 v[242:245], v[158:165], v[112:119], v[4:7], v138, v138 op_sel_hi:[0,0,0]
	v_mfma_scale_f32_16x16x128_f8f6f4 v[246:249], v[166:173], v[112:119], v[0:3], v138, v138 op_sel_hi:[0,0,0]
	s_setprio 0
	s_barrier
	s_nop 4
	ds_read_b128 v[0:3], v139
	ds_read_b128 v[4:7], v139 offset:1024
	ds_read_b128 v[96:99], v139 offset:2048
	ds_read_b128 v[100:103], v139 offset:3072
	ds_read_b128 v[142:145], v140
	ds_read_b128 v[146:149], v140 offset:1024
	ds_read_b128 v[150:153], v140 offset:2048
	ds_read_b128 v[154:157], v140 offset:3072
	ds_read_b128 v[8:11], v137 offset:32768
	ds_read_b128 v[12:15], v137 offset:33792
	ds_read_b128 v[16:19], v137 offset:34816
	ds_read_b128 v[20:23], v137 offset:35840
	ds_read_b128 v[28:31], v137 offset:36864
	ds_read_b128 v[32:35], v137 offset:37888
	ds_read_b128 v[56:59], v137 offset:38912
	ds_read_b128 v[60:63], v137 offset:39936
	s_mov_b32 s24, m0
	s_mov_b32 m0, s35
	s_nop 0
	global_load_lds_dwordx4 v134, s[22:23]
	s_mov_b32 m0, s24
	s_add_u32 s24, s22, 0x10000
	s_addc_u32 s25, s23, 0
	s_mov_b32 s58, m0
	s_mov_b32 m0, s38
	s_nop 0
	global_load_lds_dwordx4 v134, s[24:25]
	s_mov_b32 m0, s58
	s_add_u32 s24, s22, 0x20000
	s_addc_u32 s25, s23, 0
	s_mov_b32 s58, m0
	s_mov_b32 m0, s39
	s_nop 0
	global_load_lds_dwordx4 v134, s[24:25]
	s_mov_b32 m0, s58
	s_add_u32 s24, s22, 0x30000
	s_addc_u32 s25, s23, 0
	s_mov_b32 s58, m0
	s_mov_b32 m0, s40
	s_nop 0
	global_load_lds_dwordx4 v134, s[24:25]
	s_mov_b32 m0, s58
	s_waitcnt vmcnt(8)
	s_waitcnt lgkmcnt(0)
	s_barrier
	s_setprio 1
	s_waitcnt lgkmcnt(6)
	v_mfma_scale_f32_16x16x128_f8f6f4 v[104:107], v[0:7], v[8:15], v[128:131], v138, v138 op_sel_hi:[0,0,0]
	v_mfma_scale_f32_16x16x128_f8f6f4 v[112:115], v[96:103], v[8:15], v[206:209], v138, v138 op_sel_hi:[0,0,0]
	s_waitcnt lgkmcnt(4)
	v_mfma_scale_f32_16x16x128_f8f6f4 v[92:95], v[0:7], v[16:23], v[92:95], v138, v138 op_sel_hi:[0,0,0]
	v_mfma_scale_f32_16x16x128_f8f6f4 v[84:87], v[96:103], v[16:23], v[84:87], v138, v138 op_sel_hi:[0,0,0]
	s_waitcnt lgkmcnt(2)
	v_mfma_scale_f32_16x16x128_f8f6f4 v[64:67], v[0:7], v[28:35], v[64:67], v138, v138 op_sel_hi:[0,0,0]
	v_mfma_scale_f32_16x16x128_f8f6f4 v[52:55], v[96:103], v[28:35], v[52:55], v138, v138 op_sel_hi:[0,0,0]
	s_waitcnt lgkmcnt(0)
	v_mfma_scale_f32_16x16x128_f8f6f4 v[36:39], v[0:7], v[56:63], v[210:213], v138, v138 op_sel_hi:[0,0,0]
	v_mfma_scale_f32_16x16x128_f8f6f4 v[24:27], v[96:103], v[56:63], v[24:27], v138, v138 op_sel_hi:[0,0,0]
	s_setprio 0
	s_setprio 1
	v_mfma_scale_f32_16x16x128_f8f6f4 v[120:123], v[142:149], v[8:15], v[120:123], v138, v138 op_sel_hi:[0,0,0]
	v_mfma_scale_f32_16x16x128_f8f6f4 v[124:127], v[150:157], v[8:15], v[124:127], v138, v138 op_sel_hi:[0,0,0]
	v_mfma_scale_f32_16x16x128_f8f6f4 v[116:119], v[142:149], v[16:23], v[174:177], v138, v138 op_sel_hi:[0,0,0]
	v_mfma_scale_f32_16x16x128_f8f6f4 v[108:111], v[150:157], v[16:23], v[178:181], v138, v138 op_sel_hi:[0,0,0]
	v_mfma_scale_f32_16x16x128_f8f6f4 v[76:79], v[142:149], v[28:35], v[182:185], v138, v138 op_sel_hi:[0,0,0]
	v_mfma_scale_f32_16x16x128_f8f6f4 v[72:75], v[150:157], v[28:35], v[186:189], v138, v138 op_sel_hi:[0,0,0]
	v_mfma_scale_f32_16x16x128_f8f6f4 v[44:47], v[142:149], v[56:63], v[44:47], v138, v138 op_sel_hi:[0,0,0]
	v_mfma_scale_f32_16x16x128_f8f6f4 v[40:43], v[150:157], v[56:63], v[190:193], v138, v138 op_sel_hi:[0,0,0]
	s_setprio 0
	s_barrier
	s_add_u32 s24, s28, 0x80
	s_addc_u32 s25, s29, 0
	ds_read_b128 v[158:161], v137 offset:49152
	ds_read_b128 v[162:165], v137 offset:50176
	ds_read_b128 v[166:169], v137 offset:51200
	ds_read_b128 v[170:173], v137 offset:52224
	ds_read_b128 v[174:177], v137 offset:53248
	ds_read_b128 v[178:181], v137 offset:54272
	ds_read_b128 v[182:185], v137 offset:55296
	ds_read_b128 v[186:189], v137 offset:56320
	s_mov_b32 s58, m0
	s_mov_b32 m0, s44
	s_nop 0
	global_load_lds_dwordx4 v133, s[24:25]
	s_mov_b32 m0, s58
	s_add_u32 s24, s28, 0x10080
	s_addc_u32 s25, s29, 0
	s_mov_b32 s58, m0
	s_mov_b32 m0, s45
	s_nop 0
	global_load_lds_dwordx4 v133, s[24:25]
	s_mov_b32 m0, s58
	s_add_u32 s24, s28, 0x20080
	s_addc_u32 s25, s29, 0
	s_mov_b32 s58, m0
	s_mov_b32 m0, s48
	s_nop 0
	global_load_lds_dwordx4 v133, s[24:25]
	s_mov_b32 m0, s58
	s_add_u32 s24, s28, 0x30080
	s_addc_u32 s25, s29, 0
	s_mov_b32 s28, m0
	s_mov_b32 m0, s49
	s_nop 0
	global_load_lds_dwordx4 v133, s[24:25]
	s_mov_b32 m0, s28
	s_mov_b32 s24, m0
	s_mov_b32 m0, s46
	s_nop 0
	global_load_lds_dwordx4 v134, s[26:27]
	s_mov_b32 m0, s24
	s_add_u32 s22, s22, 0x10080
	s_addc_u32 s23, s23, 0
	s_mov_b32 s24, m0
	s_mov_b32 m0, s47
	s_nop 0
	global_load_lds_dwordx4 v134, s[22:23]
	s_mov_b32 m0, s24
	s_waitcnt vmcnt(8)
	s_waitcnt lgkmcnt(0)
	s_barrier
	s_setprio 1
	s_waitcnt lgkmcnt(6)
	v_mfma_scale_f32_16x16x128_f8f6f4 v[88:91], v[0:7], v[158:165], v[88:91], v138, v138 op_sel_hi:[0,0,0]
	v_mfma_scale_f32_16x16x128_f8f6f4 v[80:83], v[96:103], v[158:165], v[80:83], v138, v138 op_sel_hi:[0,0,0]
	s_waitcnt lgkmcnt(4)
	v_mfma_scale_f32_16x16x128_f8f6f4 v[56:59], v[0:7], v[166:173], v[194:197], v138, v138 op_sel_hi:[0,0,0]
	v_mfma_scale_f32_16x16x128_f8f6f4 v[48:51], v[96:103], v[166:173], v[48:51], v138, v138 op_sel_hi:[0,0,0]
	s_waitcnt lgkmcnt(2)
	v_mfma_scale_f32_16x16x128_f8f6f4 v[28:31], v[0:7], v[174:181], v[198:201], v138, v138 op_sel_hi:[0,0,0]
	v_mfma_scale_f32_16x16x128_f8f6f4 v[16:19], v[96:103], v[174:181], v[202:205], v138, v138 op_sel_hi:[0,0,0]
	s_waitcnt lgkmcnt(0)
	v_mfma_scale_f32_16x16x128_f8f6f4 v[12:15], v[0:7], v[182:189], v[214:217], v138, v138 op_sel_hi:[0,0,0]
	v_mfma_scale_f32_16x16x128_f8f6f4 v[8:11], v[96:103], v[182:189], v[218:221], v138, v138 op_sel_hi:[0,0,0]
	s_setprio 0
	s_setprio 1
	v_mfma_scale_f32_16x16x128_f8f6f4 v[100:103], v[142:149], v[158:165], v[222:225], v138, v138 op_sel_hi:[0,0,0]
	v_mfma_scale_f32_16x16x128_f8f6f4 v[96:99], v[150:157], v[158:165], v[226:229], v138, v138 op_sel_hi:[0,0,0]
	v_mfma_scale_f32_16x16x128_f8f6f4 v[68:71], v[142:149], v[166:173], v[68:71], v138, v138 op_sel_hi:[0,0,0]
	v_mfma_scale_f32_16x16x128_f8f6f4 v[60:63], v[150:157], v[166:173], v[230:233], v138, v138 op_sel_hi:[0,0,0]
	v_mfma_scale_f32_16x16x128_f8f6f4 v[32:35], v[142:149], v[174:181], v[234:237], v138, v138 op_sel_hi:[0,0,0]
	v_mfma_scale_f32_16x16x128_f8f6f4 v[20:23], v[150:157], v[174:181], v[238:241], v138, v138 op_sel_hi:[0,0,0]
	v_mfma_scale_f32_16x16x128_f8f6f4 v[4:7], v[142:149], v[182:189], v[242:245], v138, v138 op_sel_hi:[0,0,0]
	v_mfma_scale_f32_16x16x128_f8f6f4 v[0:3], v[150:157], v[182:189], v[246:249], v138, v138 op_sel_hi:[0,0,0]
	s_setprio 0
	s_barrier
	s_add_i32 s57, s57, 2
	s_add_u32 s55, s55, 0x100
	s_addc_u32 s56, s56, 0
	s_cmp_gt_u32 s57, 5
	s_mov_b64 s[24:25], s[20:21]
	s_cbranch_scc0 .LBB0_800
	s_and_b64 vcc, exec, s[4:5]
	s_cbranch_vccz .LBB0_803
	s_barrier

.LBB0_1042:
	s_ashr_i32 s7, s6, 31
	s_lshl_b64 s[10:11], s[6:7], 18
	v_readlane_b32 s14, v254, 49
	v_readlane_b32 s15, v254, 50
	s_add_u32 s10, s14, s10
	s_addc_u32 s11, s15, s11
	s_and_b64 s[14:15], s[12:13], exec
	ds_read_b128 v[0:3], v203
	ds_read_b128 v[4:7], v203 offset:1024
	ds_read_b128 v[8:11], v203 offset:2048
	ds_read_b128 v[12:15], v203 offset:3072
	ds_read_b128 v[16:19], v204
	ds_read_b128 v[20:23], v204 offset:1024
	ds_read_b128 v[24:27], v204 offset:2048
	ds_read_b128 v[28:31], v204 offset:3072
	s_cselect_b32 s7, s11, s23
	s_cselect_b32 s52, s10, s22
	s_ashr_i32 s9, s8, 31
	s_lshl_b64 s[14:15], s[8:9], 18
	s_add_u32 s14, s30, s14
	s_addc_u32 s15, s31, s15
	s_and_b64 s[24:25], s[12:13], exec
	s_cselect_b32 s9, s15, s21
	s_cselect_b32 s53, s14, s20
	s_add_u32 s24, s22, 0x100
	s_addc_u32 s25, s23, 0
	s_add_u32 s26, s22, 0x180
	s_addc_u32 s27, s23, 0
	s_add_u32 s28, s20, 0x100
	s_addc_u32 s29, s21, 0
	ds_read_b128 v[32:35], v205
	ds_read_b128 v[36:39], v205 offset:1024
	ds_read_b128 v[40:43], v205 offset:2048
	ds_read_b128 v[44:47], v205 offset:3072
	ds_read_b128 v[48:51], v205 offset:4096
	ds_read_b128 v[52:55], v205 offset:5120
	ds_read_b128 v[56:59], v205 offset:6144
	ds_read_b128 v[60:63], v205 offset:7168
	s_add_u32 s54, s22, 0x20080
	s_addc_u32 s55, s23, 0
	s_mov_b32 s56, m0
	s_mov_b32 m0, s50
	s_nop 0
	global_load_lds_dwordx4 v202, s[54:55]
	s_mov_b32 m0, s56
	s_add_u32 s54, s22, 0x30080
	s_addc_u32 s55, s23, 0
	s_mov_b32 s56, m0
	s_mov_b32 m0, s51
	s_nop 0
	global_load_lds_dwordx4 v202, s[54:55]
	s_mov_b32 m0, s56
	s_waitcnt vmcnt(8)
	s_waitcnt lgkmcnt(0)
	s_barrier
	s_setprio 1
	s_waitcnt vmcnt(4) lgkmcnt(6)
	v_mfma_scale_f32_16x16x128_f8f6f4 v[64:67], v[0:7], v[32:39], 0, v206, v206 op_sel_hi:[0,0,0]
	s_waitcnt vmcnt(3)
	v_mfma_scale_f32_16x16x128_f8f6f4 v[68:71], v[8:15], v[32:39], 0, v206, v206 op_sel_hi:[0,0,0]
	s_waitcnt vmcnt(2) lgkmcnt(4)
	v_mfma_scale_f32_16x16x128_f8f6f4 v[72:75], v[0:7], v[40:47], 0, v206, v206 op_sel_hi:[0,0,0]
	s_waitcnt vmcnt(0)
	v_mfma_scale_f32_16x16x128_f8f6f4 v[76:79], v[8:15], v[40:47], 0, v206, v206 op_sel_hi:[0,0,0]
	s_waitcnt lgkmcnt(2)
	v_mfma_scale_f32_16x16x128_f8f6f4 v[80:83], v[0:7], v[48:55], 0, v206, v206 op_sel_hi:[0,0,0]
	v_mfma_scale_f32_16x16x128_f8f6f4 v[84:87], v[8:15], v[48:55], 0, v206, v206 op_sel_hi:[0,0,0]
	s_waitcnt lgkmcnt(0)
	v_mfma_scale_f32_16x16x128_f8f6f4 v[88:91], v[0:7], v[56:63], 0, v206, v206 op_sel_hi:[0,0,0]
	v_mfma_scale_f32_16x16x128_f8f6f4 v[100:103], v[8:15], v[56:63], 0, v206, v206 op_sel_hi:[0,0,0]
	s_setprio 0
	s_setprio 1
	v_mfma_scale_f32_16x16x128_f8f6f4 v[108:111], v[16:23], v[32:39], 0, v206, v206 op_sel_hi:[0,0,0]
	v_mfma_scale_f32_16x16x128_f8f6f4 v[120:123], v[24:31], v[32:39], 0, v206, v206 op_sel_hi:[0,0,0]
	v_mfma_scale_f32_16x16x128_f8f6f4 v[136:139], v[16:23], v[40:47], 0, v206, v206 op_sel_hi:[0,0,0]
	v_mfma_scale_f32_16x16x128_f8f6f4 v[152:155], v[24:31], v[40:47], 0, v206, v206 op_sel_hi:[0,0,0]
	v_mfma_scale_f32_16x16x128_f8f6f4 v[156:159], v[16:23], v[48:55], 0, v206, v206 op_sel_hi:[0,0,0]
	v_mfma_scale_f32_16x16x128_f8f6f4 v[160:163], v[24:31], v[48:55], 0, v206, v206 op_sel_hi:[0,0,0]
	v_mfma_scale_f32_16x16x128_f8f6f4 v[164:167], v[16:23], v[56:63], 0, v206, v206 op_sel_hi:[0,0,0]
	v_mfma_scale_f32_16x16x128_f8f6f4 v[168:171], v[24:31], v[56:63], 0, v206, v206 op_sel_hi:[0,0,0]
	s_setprio 0
	s_barrier
	ds_read_b128 v[32:35], v205 offset:16384
	ds_read_b128 v[36:39], v205 offset:17408
	ds_read_b128 v[40:43], v205 offset:18432
	ds_read_b128 v[44:47], v205 offset:19456
	ds_read_b128 v[48:51], v205 offset:20480
	ds_read_b128 v[52:55], v205 offset:21504
	ds_read_b128 v[56:59], v205 offset:22528
	ds_read_b128 v[60:63], v205 offset:23552
	s_mov_b32 s54, m0
	s_mov_b32 m0, s17
	s_nop 0
	global_load_lds_dwordx4 v201, s[28:29]
	s_mov_b32 m0, s54
	s_add_u32 s28, s20, 0x10100
	s_addc_u32 s29, s21, 0
	s_mov_b32 s54, m0
	s_mov_b32 m0, s19
	s_nop 0
	global_load_lds_dwordx4 v201, s[28:29]
	s_mov_b32 m0, s54
	s_add_u32 s28, s20, 0x20100
	s_addc_u32 s29, s21, 0
	s_mov_b32 s54, m0
	s_mov_b32 m0, s34
	s_nop 0
	global_load_lds_dwordx4 v201, s[28:29]
	s_mov_b32 m0, s54
	s_add_u32 s28, s20, 0x30100
	s_addc_u32 s29, s21, 0
	s_mov_b32 s54, m0
	s_mov_b32 m0, s35
	s_nop 0
	global_load_lds_dwordx4 v201, s[28:29]
	s_mov_b32 m0, s54
	s_waitcnt vmcnt(6)
	s_waitcnt lgkmcnt(0)
	s_barrier
	s_setprio 1
	s_waitcnt lgkmcnt(6)
	v_mfma_scale_f32_16x16x128_f8f6f4 v[176:179], v[0:7], v[32:39], 0, v206, v206 op_sel_hi:[0,0,0]
	v_mfma_scale_f32_16x16x128_f8f6f4 v[180:183], v[8:15], v[32:39], 0, v206, v206 op_sel_hi:[0,0,0]
	s_waitcnt lgkmcnt(4)
	v_mfma_scale_f32_16x16x128_f8f6f4 v[184:187], v[0:7], v[40:47], 0, v206, v206 op_sel_hi:[0,0,0]
	v_mfma_scale_f32_16x16x128_f8f6f4 v[188:191], v[8:15], v[40:47], 0, v206, v206 op_sel_hi:[0,0,0]
	s_waitcnt lgkmcnt(2)
	v_mfma_scale_f32_16x16x128_f8f6f4 v[192:195], v[0:7], v[48:55], 0, v206, v206 op_sel_hi:[0,0,0]
	v_mfma_scale_f32_16x16x128_f8f6f4 v[196:199], v[8:15], v[48:55], 0, v206, v206 op_sel_hi:[0,0,0]
	s_waitcnt lgkmcnt(0)
	v_mfma_scale_f32_16x16x128_f8f6f4 v[210:213], v[0:7], v[56:63], 0, v206, v206 op_sel_hi:[0,0,0]
	v_mfma_scale_f32_16x16x128_f8f6f4 v[214:217], v[8:15], v[56:63], 0, v206, v206 op_sel_hi:[0,0,0]
	s_setprio 0
	s_setprio 1
	v_mfma_scale_f32_16x16x128_f8f6f4 v[218:221], v[16:23], v[32:39], 0, v206, v206 op_sel_hi:[0,0,0]
	v_mfma_scale_f32_16x16x128_f8f6f4 v[222:225], v[24:31], v[32:39], 0, v206, v206 op_sel_hi:[0,0,0]
	v_mfma_scale_f32_16x16x128_f8f6f4 v[226:229], v[16:23], v[40:47], 0, v206, v206 op_sel_hi:[0,0,0]
	v_mfma_scale_f32_16x16x128_f8f6f4 v[230:233], v[24:31], v[40:47], 0, v206, v206 op_sel_hi:[0,0,0]
	v_mfma_scale_f32_16x16x128_f8f6f4 v[234:237], v[16:23], v[48:55], 0, v206, v206 op_sel_hi:[0,0,0]
	v_mfma_scale_f32_16x16x128_f8f6f4 v[238:241], v[24:31], v[48:55], 0, v206, v206 op_sel_hi:[0,0,0]
	v_mfma_scale_f32_16x16x128_f8f6f4 v[242:245], v[16:23], v[56:63], 0, v206, v206 op_sel_hi:[0,0,0]
	v_mfma_scale_f32_16x16x128_f8f6f4 v[246:249], v[24:31], v[56:63], 0, v206, v206 op_sel_hi:[0,0,0]
	s_setprio 0
	s_barrier
	ds_read_b128 v[0:3], v207
	ds_read_b128 v[4:7], v207 offset:1024
	ds_read_b128 v[16:19], v207 offset:2048
	ds_read_b128 v[20:23], v207 offset:3072
	ds_read_b128 v[112:115], v208
	ds_read_b128 v[116:119], v208 offset:1024
	ds_read_b128 v[144:147], v208 offset:2048
	ds_read_b128 v[148:151], v208 offset:3072
	ds_read_b128 v[8:11], v205 offset:32768
	ds_read_b128 v[12:15], v205 offset:33792
	ds_read_b128 v[24:27], v205 offset:34816
	ds_read_b128 v[28:31], v205 offset:35840
	ds_read_b128 v[32:35], v205 offset:36864
	ds_read_b128 v[36:39], v205 offset:37888
	ds_read_b128 v[40:43], v205 offset:38912
	ds_read_b128 v[44:47], v205 offset:39936
	s_mov_b32 s28, m0
	s_mov_b32 m0, s33
	s_nop 0
	global_load_lds_dwordx4 v202, s[24:25]
	s_mov_b32 m0, s28
	s_add_u32 s28, s22, 0x10100
	s_addc_u32 s29, s23, 0
	s_mov_b32 s54, m0
	s_mov_b32 m0, s36
	s_nop 0
	global_load_lds_dwordx4 v202, s[28:29]
	s_mov_b32 m0, s54
	s_add_u32 s28, s22, 0x20100
	s_addc_u32 s29, s23, 0
	s_mov_b32 s54, m0
	s_mov_b32 m0, s37
	s_nop 0
	global_load_lds_dwordx4 v202, s[28:29]
	s_mov_b32 m0, s54
	s_add_u32 s28, s22, 0x30100
	s_addc_u32 s29, s23, 0
	s_mov_b32 s54, m0
	s_mov_b32 m0, s38
	s_nop 0
	global_load_lds_dwordx4 v202, s[28:29]
	s_mov_b32 m0, s54
	s_waitcnt vmcnt(8)
	s_waitcnt lgkmcnt(0)
	s_barrier
	s_setprio 1
	s_waitcnt lgkmcnt(6)
	v_mfma_scale_f32_16x16x128_f8f6f4 v[128:131], v[0:7], v[8:15], v[64:67], v206, v206 op_sel_hi:[0,0,0]
	v_mfma_scale_f32_16x16x128_f8f6f4 v[124:127], v[16:23], v[8:15], v[68:71], v206, v206 op_sel_hi:[0,0,0]
	s_waitcnt lgkmcnt(4)
	v_mfma_scale_f32_16x16x128_f8f6f4 v[104:107], v[0:7], v[24:31], v[72:75], v206, v206 op_sel_hi:[0,0,0]
	v_mfma_scale_f32_16x16x128_f8f6f4 v[96:99], v[16:23], v[24:31], v[76:79], v206, v206 op_sel_hi:[0,0,0]
	s_waitcnt lgkmcnt(2)
	v_mfma_scale_f32_16x16x128_f8f6f4 v[92:95], v[0:7], v[32:39], v[80:83], v206, v206 op_sel_hi:[0,0,0]
	v_mfma_scale_f32_16x16x128_f8f6f4 v[84:87], v[16:23], v[32:39], v[84:87], v206, v206 op_sel_hi:[0,0,0]
	s_waitcnt lgkmcnt(0)
	v_mfma_scale_f32_16x16x128_f8f6f4 v[68:71], v[0:7], v[40:47], v[88:91], v206, v206 op_sel_hi:[0,0,0]
	v_mfma_scale_f32_16x16x128_f8f6f4 v[56:59], v[16:23], v[40:47], v[100:103], v206, v206 op_sel_hi:[0,0,0]
	s_setprio 0
	s_setprio 1
	v_mfma_scale_f32_16x16x128_f8f6f4 v[140:143], v[112:119], v[8:15], v[108:111], v206, v206 op_sel_hi:[0,0,0]
	v_mfma_scale_f32_16x16x128_f8f6f4 v[132:135], v[144:151], v[8:15], v[120:123], v206, v206 op_sel_hi:[0,0,0]
	v_mfma_scale_f32_16x16x128_f8f6f4 v[108:111], v[112:119], v[24:31], v[136:139], v206, v206 op_sel_hi:[0,0,0]
	v_mfma_scale_f32_16x16x128_f8f6f4 v[100:103], v[144:151], v[24:31], v[152:155], v206, v206 op_sel_hi:[0,0,0]
	v_mfma_scale_f32_16x16x128_f8f6f4 v[88:91], v[112:119], v[32:39], v[156:159], v206, v206 op_sel_hi:[0,0,0]
	v_mfma_scale_f32_16x16x128_f8f6f4 v[80:83], v[144:151], v[32:39], v[160:163], v206, v206 op_sel_hi:[0,0,0]
	v_mfma_scale_f32_16x16x128_f8f6f4 v[52:55], v[112:119], v[40:47], v[164:167], v206, v206 op_sel_hi:[0,0,0]
	v_mfma_scale_f32_16x16x128_f8f6f4 v[48:51], v[144:151], v[40:47], v[168:171], v206, v206 op_sel_hi:[0,0,0]
	s_setprio 0
	s_barrier
	s_add_u32 s28, s20, 0x180
	s_addc_u32 s29, s21, 0
	ds_read_b128 v[32:35], v205 offset:49152
	ds_read_b128 v[36:39], v205 offset:50176
	ds_read_b128 v[152:155], v205 offset:51200
	ds_read_b128 v[156:159], v205 offset:52224
	ds_read_b128 v[160:163], v205 offset:53248
	ds_read_b128 v[164:167], v205 offset:54272
	ds_read_b128 v[168:171], v205 offset:55296
	ds_read_b128 v[172:175], v205 offset:56320
	s_mov_b32 s54, m0
	s_mov_b32 m0, s44
	s_nop 0
	global_load_lds_dwordx4 v201, s[28:29]
	s_mov_b32 m0, s54
	s_add_u32 s28, s20, 0x10180
	s_addc_u32 s29, s21, 0
	s_mov_b32 s54, m0
	s_mov_b32 m0, s45
	s_nop 0
	global_load_lds_dwordx4 v201, s[28:29]
	s_mov_b32 m0, s54
	s_add_u32 s28, s20, 0x20180
	s_addc_u32 s29, s21, 0
	s_mov_b32 s54, m0
	s_mov_b32 m0, s48
	s_nop 0
	global_load_lds_dwordx4 v201, s[28:29]
	s_mov_b32 m0, s54
	s_add_u32 s28, s20, 0x30180
	s_addc_u32 s29, s21, 0
	s_mov_b32 s54, m0
	s_mov_b32 m0, s49
	s_nop 0
	global_load_lds_dwordx4 v201, s[28:29]
	s_mov_b32 m0, s54
	s_mov_b32 s28, m0
	s_mov_b32 m0, s46
	s_nop 0
	global_load_lds_dwordx4 v202, s[26:27]
	s_mov_b32 m0, s28
	s_add_u32 s22, s22, 0x10180
	s_addc_u32 s23, s23, 0
	s_mov_b32 s26, m0
	s_mov_b32 m0, s47
	s_nop 0
	global_load_lds_dwordx4 v202, s[22:23]
	s_mov_b32 m0, s26
	s_waitcnt vmcnt(8)
	s_waitcnt lgkmcnt(0)
	s_barrier
	s_setprio 1
	s_waitcnt lgkmcnt(6)
	v_mfma_scale_f32_16x16x128_f8f6f4 v[76:79], v[0:7], v[32:39], v[176:179], v206, v206 op_sel_hi:[0,0,0]
	v_mfma_scale_f32_16x16x128_f8f6f4 v[64:67], v[16:23], v[32:39], v[180:183], v206, v206 op_sel_hi:[0,0,0]
	s_waitcnt lgkmcnt(4)
	v_mfma_scale_f32_16x16x128_f8f6f4 v[44:47], v[0:7], v[152:159], v[184:187], v206, v206 op_sel_hi:[0,0,0]
	v_mfma_scale_f32_16x16x128_f8f6f4 v[40:43], v[16:23], v[152:159], v[188:191], v206, v206 op_sel_hi:[0,0,0]
	s_waitcnt lgkmcnt(2)
	v_mfma_scale_f32_16x16x128_f8f6f4 v[28:31], v[0:7], v[160:167], v[192:195], v206, v206 op_sel_hi:[0,0,0]
	v_mfma_scale_f32_16x16x128_f8f6f4 v[24:27], v[16:23], v[160:167], v[196:199], v206, v206 op_sel_hi:[0,0,0]
	s_waitcnt lgkmcnt(0)
	v_mfma_scale_f32_16x16x128_f8f6f4 v[12:15], v[0:7], v[168:175], v[210:213], v206, v206 op_sel_hi:[0,0,0]
	v_mfma_scale_f32_16x16x128_f8f6f4 v[8:11], v[16:23], v[168:175], v[214:217], v206, v206 op_sel_hi:[0,0,0]
	s_setprio 0
	s_setprio 1
	v_mfma_scale_f32_16x16x128_f8f6f4 v[72:75], v[112:119], v[32:39], v[218:221], v206, v206 op_sel_hi:[0,0,0]
	v_mfma_scale_f32_16x16x128_f8f6f4 v[60:63], v[144:151], v[32:39], v[222:225], v206, v206 op_sel_hi:[0,0,0]
	v_mfma_scale_f32_16x16x128_f8f6f4 v[36:39], v[112:119], v[152:159], v[226:229], v206, v206 op_sel_hi:[0,0,0]
	v_mfma_scale_f32_16x16x128_f8f6f4 v[32:35], v[144:151], v[152:159], v[230:233], v206, v206 op_sel_hi:[0,0,0]
	v_mfma_scale_f32_16x16x128_f8f6f4 v[20:23], v[112:119], v[160:167], v[234:237], v206, v206 op_sel_hi:[0,0,0]
	v_mfma_scale_f32_16x16x128_f8f6f4 v[16:19], v[144:151], v[160:167], v[238:241], v206, v206 op_sel_hi:[0,0,0]
	v_mfma_scale_f32_16x16x128_f8f6f4 v[4:7], v[112:119], v[168:175], v[242:245], v206, v206 op_sel_hi:[0,0,0]
	v_mfma_scale_f32_16x16x128_f8f6f4 v[0:3], v[144:151], v[168:175], v[246:249], v206, v206 op_sel_hi:[0,0,0]
	s_setprio 0
	s_barrier
	s_add_u32 s54, s20, 0x200
	s_addc_u32 s55, s21, 0
	s_mov_b32 s56, 0

.LBB0_1223:
	s_add_u32 s34, s34, 0x100
	s_addc_u32 s35, s35, 0
	s_and_b64 s[36:37], s[38:39], exec
	s_cselect_b32 s42, s16, s34
	s_cselect_b32 s43, s17, s35
	s_add_u32 s36, s42, 0x80
	s_addc_u32 s37, s43, 0
	s_waitcnt vmcnt(8)
	s_and_b64 s[38:39], s[38:39], exec
	s_waitcnt lgkmcnt(0)
	s_cselect_b32 s38, s26, s15
	s_cselect_b32 s39, s27, s23
	s_add_u32 s40, s38, 0x80
	s_addc_u32 s41, s39, 0
	s_barrier
	s_setprio 1
	s_waitcnt lgkmcnt(6)
	v_mfma_scale_f32_16x16x128_f8f6f4 v[188:191], v[16:23], v[56:63], v[188:191], v205, v205 op_sel_hi:[0,0,0]
	v_mfma_scale_f32_16x16x128_f8f6f4 v[180:183], v[24:31], v[56:63], v[180:183], v205, v205 op_sel_hi:[0,0,0]
	s_waitcnt lgkmcnt(4)
	v_mfma_scale_f32_16x16x128_f8f6f4 v[172:175], v[16:23], v[48:55], v[172:175], v205, v205 op_sel_hi:[0,0,0]
	v_mfma_scale_f32_16x16x128_f8f6f4 v[164:167], v[24:31], v[48:55], v[164:167], v205, v205 op_sel_hi:[0,0,0]
	s_waitcnt lgkmcnt(2)
	v_mfma_scale_f32_16x16x128_f8f6f4 v[156:159], v[16:23], v[40:47], v[156:159], v205, v205 op_sel_hi:[0,0,0]
	v_mfma_scale_f32_16x16x128_f8f6f4 v[148:151], v[24:31], v[40:47], v[148:151], v205, v205 op_sel_hi:[0,0,0]
	s_waitcnt lgkmcnt(0)
	v_mfma_scale_f32_16x16x128_f8f6f4 v[140:143], v[16:23], v[32:39], v[140:143], v205, v205 op_sel_hi:[0,0,0]
	v_mfma_scale_f32_16x16x128_f8f6f4 v[132:135], v[24:31], v[32:39], v[132:135], v205, v205 op_sel_hi:[0,0,0]
	s_setprio 0
	s_setprio 1
	v_mfma_scale_f32_16x16x128_f8f6f4 v[184:187], v[0:7], v[56:63], v[184:187], v205, v205 op_sel_hi:[0,0,0]
	v_mfma_scale_f32_16x16x128_f8f6f4 v[176:179], v[8:15], v[56:63], v[176:179], v205, v205 op_sel_hi:[0,0,0]
	v_mfma_scale_f32_16x16x128_f8f6f4 v[168:171], v[0:7], v[48:55], v[168:171], v205, v205 op_sel_hi:[0,0,0]
	v_mfma_scale_f32_16x16x128_f8f6f4 v[160:163], v[8:15], v[48:55], v[160:163], v205, v205 op_sel_hi:[0,0,0]
	v_mfma_scale_f32_16x16x128_f8f6f4 v[152:155], v[0:7], v[40:47], v[152:155], v205, v205 op_sel_hi:[0,0,0]
	v_mfma_scale_f32_16x16x128_f8f6f4 v[144:147], v[8:15], v[40:47], v[144:147], v205, v205 op_sel_hi:[0,0,0]
	v_mfma_scale_f32_16x16x128_f8f6f4 v[136:139], v[0:7], v[32:39], v[136:139], v205, v205 op_sel_hi:[0,0,0]
	v_mfma_scale_f32_16x16x128_f8f6f4 v[128:131], v[8:15], v[32:39], v[128:131], v205, v205 op_sel_hi:[0,0,0]
	s_setprio 0
	s_barrier
	s_add_u32 s72, s38, 0x10000
	ds_read_b128 v[32:35], v210 offset:16384
	ds_read_b128 v[36:39], v210 offset:17408
	ds_read_b128 v[40:43], v210 offset:18432
	ds_read_b128 v[44:47], v210 offset:19456
	ds_read_b128 v[48:51], v210 offset:20480
	ds_read_b128 v[52:55], v210 offset:21504
	ds_read_b128 v[56:59], v210 offset:22528
	ds_read_b128 v[60:63], v210 offset:23552
	s_mov_b32 s71, m0
	s_mov_b32 m0, s29
	s_nop 0
	global_load_lds_dwordx4 v199, s[38:39]
	s_mov_b32 m0, s71
	s_addc_u32 s73, s39, 0
	s_mov_b32 s71, m0
	s_mov_b32 m0, s49
	s_nop 0
	global_load_lds_dwordx4 v199, s[72:73]
	s_mov_b32 m0, s71
	s_add_u32 s72, s38, 0x20000
	s_addc_u32 s73, s39, 0
	s_mov_b32 s71, m0
	s_mov_b32 m0, s50
	s_nop 0
	global_load_lds_dwordx4 v199, s[72:73]
	s_mov_b32 m0, s71
	s_add_u32 s72, s38, 0x30000
	s_addc_u32 s73, s39, 0
	s_mov_b32 s71, m0
	s_mov_b32 m0, s51
	s_nop 0
	global_load_lds_dwordx4 v199, s[72:73]
	s_mov_b32 m0, s71
	s_nop 0
	s_waitcnt vmcnt(6)
	s_waitcnt lgkmcnt(0)
	s_barrier
	s_setprio 1
	s_waitcnt lgkmcnt(6)
	v_mfma_scale_f32_16x16x128_f8f6f4 v[124:127], v[16:23], v[32:39], v[124:127], v205, v205 op_sel_hi:[0,0,0]
	v_mfma_scale_f32_16x16x128_f8f6f4 v[116:119], v[24:31], v[32:39], v[116:119], v205, v205 op_sel_hi:[0,0,0]
	s_waitcnt lgkmcnt(4)
	v_mfma_scale_f32_16x16x128_f8f6f4 v[108:111], v[16:23], v[40:47], v[108:111], v205, v205 op_sel_hi:[0,0,0]
	v_mfma_scale_f32_16x16x128_f8f6f4 v[100:103], v[24:31], v[40:47], v[100:103], v205, v205 op_sel_hi:[0,0,0]
	s_waitcnt lgkmcnt(2)
	v_mfma_scale_f32_16x16x128_f8f6f4 v[92:95], v[16:23], v[48:55], v[92:95], v205, v205 op_sel_hi:[0,0,0]
	v_mfma_scale_f32_16x16x128_f8f6f4 v[84:87], v[24:31], v[48:55], v[84:87], v205, v205 op_sel_hi:[0,0,0]
	s_waitcnt lgkmcnt(0)
	v_mfma_scale_f32_16x16x128_f8f6f4 v[72:75], v[16:23], v[56:63], v[72:75], v205, v205 op_sel_hi:[0,0,0]
	v_mfma_scale_f32_16x16x128_f8f6f4 v[64:67], v[24:31], v[56:63], v[64:67], v205, v205 op_sel_hi:[0,0,0]
	s_setprio 0
	s_setprio 1
	v_mfma_scale_f32_16x16x128_f8f6f4 v[120:123], v[0:7], v[32:39], v[120:123], v205, v205 op_sel_hi:[0,0,0]
	v_mfma_scale_f32_16x16x128_f8f6f4 v[112:115], v[8:15], v[32:39], v[112:115], v205, v205 op_sel_hi:[0,0,0]
	v_mfma_scale_f32_16x16x128_f8f6f4 v[104:107], v[0:7], v[40:47], v[104:107], v205, v205 op_sel_hi:[0,0,0]
	v_mfma_scale_f32_16x16x128_f8f6f4 v[96:99], v[8:15], v[40:47], v[96:99], v205, v205 op_sel_hi:[0,0,0]
	v_mfma_scale_f32_16x16x128_f8f6f4 v[88:91], v[0:7], v[48:55], v[88:91], v205, v205 op_sel_hi:[0,0,0]
	v_mfma_scale_f32_16x16x128_f8f6f4 v[80:83], v[8:15], v[48:55], v[80:83], v205, v205 op_sel_hi:[0,0,0]
	v_mfma_scale_f32_16x16x128_f8f6f4 v[76:79], v[0:7], v[56:63], v[76:79], v205, v205 op_sel_hi:[0,0,0]
	v_mfma_scale_f32_16x16x128_f8f6f4 v[68:71], v[8:15], v[56:63], v[68:71], v205, v205 op_sel_hi:[0,0,0]
	s_setprio 0
	s_barrier
	v_add_u32_e32 v12, 0x18000, v209
	v_add_u32_e32 v28, 0x1c000, v209
	ds_read_b128 v[0:3], v12
	ds_read_b128 v[4:7], v12 offset:1024
	ds_read_b128 v[8:11], v12 offset:2048
	ds_read_b128 v[12:15], v12 offset:3072
	ds_read_b128 v[16:19], v28
	ds_read_b128 v[20:23], v28 offset:1024
	ds_read_b128 v[24:27], v28 offset:2048
	ds_read_b128 v[28:31], v28 offset:3072
	ds_read_b128 v[32:35], v210 offset:32768
	ds_read_b128 v[36:39], v210 offset:33792
	ds_read_b128 v[40:43], v210 offset:34816
	ds_read_b128 v[44:47], v210 offset:35840
	ds_read_b128 v[48:51], v210 offset:36864
	ds_read_b128 v[52:55], v210 offset:37888
	ds_read_b128 v[56:59], v210 offset:38912
	ds_read_b128 v[60:63], v210 offset:39936
	s_mov_b32 s71, m0
	s_mov_b32 m0, s48
	s_nop 0
	global_load_lds_dwordx4 v200, s[42:43]
	s_mov_b32 m0, s71
	s_nop 0
	s_mov_b32 s71, m0
	s_mov_b32 m0, s52
	s_nop 0
	global_load_lds_dwordx4 v201, s[42:43]
	s_mov_b32 m0, s71
	s_mov_b32 s71, m0
	s_mov_b32 m0, s53
	s_nop 0
	global_load_lds_dwordx4 v202, s[42:43]
	s_mov_b32 m0, s71
	s_nop 0
	s_mov_b32 s71, m0
	s_mov_b32 m0, s54
	s_nop 0
	global_load_lds_dwordx4 v203, s[42:43]
	s_mov_b32 m0, s71
	s_waitcnt vmcnt(8)
	s_waitcnt lgkmcnt(0)
	s_barrier
	s_setprio 1
	s_waitcnt lgkmcnt(6)
	v_mfma_scale_f32_16x16x128_f8f6f4 v[188:191], v[0:7], v[32:39], v[188:191], v205, v205 op_sel_hi:[0,0,0]
	v_mfma_scale_f32_16x16x128_f8f6f4 v[180:183], v[8:15], v[32:39], v[180:183], v205, v205 op_sel_hi:[0,0,0]
	s_waitcnt lgkmcnt(4)
	v_mfma_scale_f32_16x16x128_f8f6f4 v[172:175], v[0:7], v[40:47], v[172:175], v205, v205 op_sel_hi:[0,0,0]
	v_mfma_scale_f32_16x16x128_f8f6f4 v[164:167], v[8:15], v[40:47], v[164:167], v205, v205 op_sel_hi:[0,0,0]
	s_waitcnt lgkmcnt(2)
	v_mfma_scale_f32_16x16x128_f8f6f4 v[156:159], v[0:7], v[48:55], v[156:159], v205, v205 op_sel_hi:[0,0,0]
	v_mfma_scale_f32_16x16x128_f8f6f4 v[148:151], v[8:15], v[48:55], v[148:151], v205, v205 op_sel_hi:[0,0,0]
	s_waitcnt lgkmcnt(0)
	v_mfma_scale_f32_16x16x128_f8f6f4 v[140:143], v[0:7], v[56:63], v[140:143], v205, v205 op_sel_hi:[0,0,0]
	v_mfma_scale_f32_16x16x128_f8f6f4 v[132:135], v[8:15], v[56:63], v[132:135], v205, v205 op_sel_hi:[0,0,0]
	s_setprio 0
	s_setprio 1
	v_mfma_scale_f32_16x16x128_f8f6f4 v[184:187], v[16:23], v[32:39], v[184:187], v205, v205 op_sel_hi:[0,0,0]
	v_mfma_scale_f32_16x16x128_f8f6f4 v[176:179], v[24:31], v[32:39], v[176:179], v205, v205 op_sel_hi:[0,0,0]
	v_mfma_scale_f32_16x16x128_f8f6f4 v[168:171], v[16:23], v[40:47], v[168:171], v205, v205 op_sel_hi:[0,0,0]
	v_mfma_scale_f32_16x16x128_f8f6f4 v[160:163], v[24:31], v[40:47], v[160:163], v205, v205 op_sel_hi:[0,0,0]
	v_mfma_scale_f32_16x16x128_f8f6f4 v[152:155], v[16:23], v[48:55], v[152:155], v205, v205 op_sel_hi:[0,0,0]
	v_mfma_scale_f32_16x16x128_f8f6f4 v[144:147], v[24:31], v[48:55], v[144:147], v205, v205 op_sel_hi:[0,0,0]
	v_mfma_scale_f32_16x16x128_f8f6f4 v[136:139], v[16:23], v[56:63], v[136:139], v205, v205 op_sel_hi:[0,0,0]
	v_mfma_scale_f32_16x16x128_f8f6f4 v[128:131], v[24:31], v[56:63], v[128:131], v205, v205 op_sel_hi:[0,0,0]
	s_setprio 0
	s_barrier
	ds_read_b128 v[32:35], v210 offset:49152
	ds_read_b128 v[36:39], v210 offset:50176
	ds_read_b128 v[40:43], v210 offset:51200
	ds_read_b128 v[44:47], v210 offset:52224
	ds_read_b128 v[48:51], v210 offset:53248
	ds_read_b128 v[52:55], v210 offset:54272
	ds_read_b128 v[56:59], v210 offset:55296
	ds_read_b128 v[60:63], v210 offset:56320
	s_mov_b32 s42, m0
	s_mov_b32 m0, s57
	s_nop 0
	global_load_lds_dwordx4 v199, s[40:41]
	s_mov_b32 m0, s42
	s_add_u32 s40, s38, 0x10080
	s_addc_u32 s41, s39, 0
	s_mov_b32 s42, m0
	s_mov_b32 m0, s58
	s_nop 0
	global_load_lds_dwordx4 v199, s[40:41]
	s_mov_b32 m0, s42
	s_add_u32 s40, s38, 0x20080
	s_addc_u32 s41, s39, 0
	s_mov_b32 s42, m0
	s_mov_b32 m0, s61
	s_nop 0
	global_load_lds_dwordx4 v199, s[40:41]
	s_mov_b32 m0, s42
	s_add_u32 s38, s38, 0x30080
	s_addc_u32 s39, s39, 0
	s_mov_b32 s40, m0
	s_mov_b32 m0, s62
	s_nop 0
	global_load_lds_dwordx4 v199, s[38:39]
	s_mov_b32 m0, s40
	s_mov_b32 s38, m0
	s_mov_b32 m0, s59
	s_nop 0
	global_load_lds_dwordx4 v200, s[36:37]
	s_mov_b32 m0, s38
	s_nop 0
	s_mov_b32 s38, m0
	s_mov_b32 m0, s60
	s_nop 0
	global_load_lds_dwordx4 v201, s[36:37]
	s_mov_b32 m0, s38
	s_waitcnt vmcnt(8)
	s_waitcnt lgkmcnt(0)
	s_barrier
	s_setprio 1
	s_waitcnt lgkmcnt(6)
	v_mfma_scale_f32_16x16x128_f8f6f4 v[124:127], v[0:7], v[32:39], v[124:127], v205, v205 op_sel_hi:[0,0,0]
	v_mfma_scale_f32_16x16x128_f8f6f4 v[116:119], v[8:15], v[32:39], v[116:119], v205, v205 op_sel_hi:[0,0,0]
	s_waitcnt lgkmcnt(4)
	v_mfma_scale_f32_16x16x128_f8f6f4 v[108:111], v[0:7], v[40:47], v[108:111], v205, v205 op_sel_hi:[0,0,0]
	v_mfma_scale_f32_16x16x128_f8f6f4 v[100:103], v[8:15], v[40:47], v[100:103], v205, v205 op_sel_hi:[0,0,0]
	s_waitcnt lgkmcnt(2)
	v_mfma_scale_f32_16x16x128_f8f6f4 v[92:95], v[0:7], v[48:55], v[92:95], v205, v205 op_sel_hi:[0,0,0]
	v_mfma_scale_f32_16x16x128_f8f6f4 v[84:87], v[8:15], v[48:55], v[84:87], v205, v205 op_sel_hi:[0,0,0]
	s_waitcnt lgkmcnt(0)
	v_mfma_scale_f32_16x16x128_f8f6f4 v[72:75], v[0:7], v[56:63], v[72:75], v205, v205 op_sel_hi:[0,0,0]
	v_mfma_scale_f32_16x16x128_f8f6f4 v[64:67], v[8:15], v[56:63], v[64:67], v205, v205 op_sel_hi:[0,0,0]
	s_setprio 0
	s_setprio 1
	v_mfma_scale_f32_16x16x128_f8f6f4 v[120:123], v[16:23], v[32:39], v[120:123], v205, v205 op_sel_hi:[0,0,0]
	v_mfma_scale_f32_16x16x128_f8f6f4 v[112:115], v[24:31], v[32:39], v[112:115], v205, v205 op_sel_hi:[0,0,0]
	v_mfma_scale_f32_16x16x128_f8f6f4 v[104:107], v[16:23], v[40:47], v[104:107], v205, v205 op_sel_hi:[0,0,0]
	v_mfma_scale_f32_16x16x128_f8f6f4 v[96:99], v[24:31], v[40:47], v[96:99], v205, v205 op_sel_hi:[0,0,0]
	v_mfma_scale_f32_16x16x128_f8f6f4 v[88:91], v[16:23], v[48:55], v[88:91], v205, v205 op_sel_hi:[0,0,0]
	v_mfma_scale_f32_16x16x128_f8f6f4 v[80:83], v[24:31], v[48:55], v[80:83], v205, v205 op_sel_hi:[0,0,0]
	v_mfma_scale_f32_16x16x128_f8f6f4 v[76:79], v[16:23], v[56:63], v[76:79], v205, v205 op_sel_hi:[0,0,0]
	v_mfma_scale_f32_16x16x128_f8f6f4 v[68:71], v[24:31], v[56:63], v[68:71], v205, v205 op_sel_hi:[0,0,0]
	s_setprio 0
	s_barrier
	s_add_i32 s25, s25, 2
	s_add_u32 s15, s15, 0x100
	s_addc_u32 s23, s23, 0
	s_cmp_gt_u32 s25, 5
	s_cbranch_scc1 .LBB0_1226

.LBB0_1338:
	ds_read_b128 v[146:149], v139
	ds_read_b128 v[150:153], v139 offset:1024
	ds_read_b128 v[154:157], v139 offset:2048
	ds_read_b128 v[158:161], v139 offset:3072
	ds_read_b128 v[162:165], v140
	ds_read_b128 v[166:169], v140 offset:1024
	ds_read_b128 v[170:173], v140 offset:2048
	ds_read_b128 v[174:177], v140 offset:3072
	s_add_u32 s24, s22, 0x100
	s_addc_u32 s25, s23, 0
	s_cmp_eq_u32 s13, 4
	s_cselect_b32 s26, s16, s24
	s_cselect_b32 s27, s17, s25
	s_cselect_b32 s30, s18, s1
	s_cselect_b32 s31, s19, s11
	s_add_u32 s28, s26, 0x80
	s_addc_u32 s29, s27, 0
	ds_read_b128 v[178:181], v141
	ds_read_b128 v[182:185], v141 offset:1024
	ds_read_b128 v[186:189], v141 offset:2048
	ds_read_b128 v[190:193], v141 offset:3072
	ds_read_b128 v[194:197], v141 offset:4096
	ds_read_b128 v[198:201], v141 offset:5120
	ds_read_b128 v[202:205], v141 offset:6144
	ds_read_b128 v[206:209], v141 offset:7168
	s_add_u32 s62, s22, 0x20080
	s_addc_u32 s63, s23, 0
	s_mov_b32 s15, m0
	s_mov_b32 m0, s55
	s_nop 0
	global_load_lds_dwordx4 v137, s[62:63]
	s_mov_b32 m0, s15
	s_add_u32 s22, s22, 0x30080
	s_addc_u32 s23, s23, 0
	s_mov_b32 s15, m0
	s_mov_b32 m0, s56
	s_nop 0
	global_load_lds_dwordx4 v137, s[22:23]
	s_mov_b32 m0, s15
	s_waitcnt vmcnt(8)
	s_waitcnt lgkmcnt(0)
	s_barrier
	s_setprio 1
	s_waitcnt lgkmcnt(6)
	v_mfma_scale_f32_16x16x128_f8f6f4 v[124:127], v[146:153], v[178:185], v[124:127], v142, v142 op_sel_hi:[0,0,0]
	v_mfma_scale_f32_16x16x128_f8f6f4 v[120:123], v[154:161], v[178:185], v[120:123], v142, v142 op_sel_hi:[0,0,0]
	s_waitcnt lgkmcnt(4)
	v_mfma_scale_f32_16x16x128_f8f6f4 v[116:119], v[146:153], v[186:193], v[116:119], v142, v142 op_sel_hi:[0,0,0]
	v_mfma_scale_f32_16x16x128_f8f6f4 v[112:115], v[154:161], v[186:193], v[112:115], v142, v142 op_sel_hi:[0,0,0]
	s_waitcnt lgkmcnt(2)
	v_mfma_scale_f32_16x16x128_f8f6f4 v[128:131], v[146:153], v[194:201], v[92:95], v142, v142 op_sel_hi:[0,0,0]
	v_mfma_scale_f32_16x16x128_f8f6f4 v[210:213], v[154:161], v[194:201], v[88:91], v142, v142 op_sel_hi:[0,0,0]
	s_waitcnt lgkmcnt(0)
	v_mfma_scale_f32_16x16x128_f8f6f4 v[214:217], v[146:153], v[202:209], v[84:87], v142, v142 op_sel_hi:[0,0,0]
	v_mfma_scale_f32_16x16x128_f8f6f4 v[218:221], v[154:161], v[202:209], v[80:83], v142, v142 op_sel_hi:[0,0,0]
	s_setprio 0
	s_setprio 1
	v_mfma_scale_f32_16x16x128_f8f6f4 v[108:111], v[162:169], v[178:185], v[108:111], v142, v142 op_sel_hi:[0,0,0]
	v_mfma_scale_f32_16x16x128_f8f6f4 v[104:107], v[170:177], v[178:185], v[104:107], v142, v142 op_sel_hi:[0,0,0]
	v_mfma_scale_f32_16x16x128_f8f6f4 v[100:103], v[162:169], v[186:193], v[100:103], v142, v142 op_sel_hi:[0,0,0]
	v_mfma_scale_f32_16x16x128_f8f6f4 v[96:99], v[170:177], v[186:193], v[96:99], v142, v142 op_sel_hi:[0,0,0]
	v_mfma_scale_f32_16x16x128_f8f6f4 v[178:181], v[162:169], v[194:201], v[76:79], v142, v142 op_sel_hi:[0,0,0]
	v_mfma_scale_f32_16x16x128_f8f6f4 v[182:185], v[170:177], v[194:201], v[72:75], v142, v142 op_sel_hi:[0,0,0]
	v_mfma_scale_f32_16x16x128_f8f6f4 v[186:189], v[162:169], v[202:209], v[68:71], v142, v142 op_sel_hi:[0,0,0]
	v_mfma_scale_f32_16x16x128_f8f6f4 v[190:193], v[170:177], v[202:209], v[64:67], v142, v142 op_sel_hi:[0,0,0]
	s_setprio 0
	s_barrier
	s_add_u32 s22, s30, 0x10000
	s_nop 3
	ds_read_b128 v[64:67], v141 offset:16384
	ds_read_b128 v[68:71], v141 offset:17408
	ds_read_b128 v[72:75], v141 offset:18432
	ds_read_b128 v[76:79], v141 offset:19456
	ds_read_b128 v[80:83], v141 offset:20480
	ds_read_b128 v[84:87], v141 offset:21504
	ds_read_b128 v[88:91], v141 offset:22528
	ds_read_b128 v[92:95], v141 offset:23552
	s_mov_b32 s15, m0
	s_mov_b32 m0, s38
	s_nop 0
	global_load_lds_dwordx4 v136, s[30:31]
	s_mov_b32 m0, s15
	s_addc_u32 s23, s31, 0
	s_mov_b32 s15, m0
	s_mov_b32 m0, s39
	s_nop 0
	global_load_lds_dwordx4 v136, s[22:23]
	s_mov_b32 m0, s15
	s_add_u32 s22, s30, 0x20000
	s_addc_u32 s23, s31, 0
	s_mov_b32 s15, m0
	s_mov_b32 m0, s40
	s_nop 0
	global_load_lds_dwordx4 v136, s[22:23]
	s_mov_b32 m0, s15
	s_add_u32 s22, s30, 0x30000
	s_addc_u32 s23, s31, 0
	s_mov_b32 s15, m0
	s_mov_b32 m0, s41
	s_nop 0
	global_load_lds_dwordx4 v136, s[22:23]
	s_mov_b32 m0, s15
	s_waitcnt vmcnt(6)
	s_waitcnt lgkmcnt(0)
	s_barrier
	s_setprio 1
	s_waitcnt lgkmcnt(6)
	v_mfma_scale_f32_16x16x128_f8f6f4 v[60:63], v[146:153], v[64:71], v[60:63], v142, v142 op_sel_hi:[0,0,0]
	v_mfma_scale_f32_16x16x128_f8f6f4 v[56:59], v[154:161], v[64:71], v[56:59], v142, v142 op_sel_hi:[0,0,0]
	s_waitcnt lgkmcnt(4)
	v_mfma_scale_f32_16x16x128_f8f6f4 v[52:55], v[146:153], v[72:79], v[52:55], v142, v142 op_sel_hi:[0,0,0]
	v_mfma_scale_f32_16x16x128_f8f6f4 v[48:51], v[154:161], v[72:79], v[48:51], v142, v142 op_sel_hi:[0,0,0]
	s_waitcnt lgkmcnt(2)
	v_mfma_scale_f32_16x16x128_f8f6f4 v[194:197], v[146:153], v[80:87], v[28:31], v142, v142 op_sel_hi:[0,0,0]
	v_mfma_scale_f32_16x16x128_f8f6f4 v[198:201], v[154:161], v[80:87], v[24:27], v142, v142 op_sel_hi:[0,0,0]
	s_waitcnt lgkmcnt(0)
	v_mfma_scale_f32_16x16x128_f8f6f4 v[202:205], v[146:153], v[88:95], v[12:15], v142, v142 op_sel_hi:[0,0,0]
	v_mfma_scale_f32_16x16x128_f8f6f4 v[206:209], v[154:161], v[88:95], v[8:11], v142, v142 op_sel_hi:[0,0,0]
	s_setprio 0
	s_setprio 1
	v_mfma_scale_f32_16x16x128_f8f6f4 v[222:225], v[162:169], v[64:71], v[44:47], v142, v142 op_sel_hi:[0,0,0]
	v_mfma_scale_f32_16x16x128_f8f6f4 v[226:229], v[170:177], v[64:71], v[40:43], v142, v142 op_sel_hi:[0,0,0]
	v_mfma_scale_f32_16x16x128_f8f6f4 v[230:233], v[162:169], v[72:79], v[36:39], v142, v142 op_sel_hi:[0,0,0]
	v_mfma_scale_f32_16x16x128_f8f6f4 v[234:237], v[170:177], v[72:79], v[32:35], v142, v142 op_sel_hi:[0,0,0]
	v_mfma_scale_f32_16x16x128_f8f6f4 v[238:241], v[162:169], v[80:87], v[20:23], v142, v142 op_sel_hi:[0,0,0]
	v_mfma_scale_f32_16x16x128_f8f6f4 v[242:245], v[170:177], v[80:87], v[16:19], v142, v142 op_sel_hi:[0,0,0]
	v_mfma_scale_f32_16x16x128_f8f6f4 v[246:249], v[162:169], v[88:95], v[4:7], v142, v142 op_sel_hi:[0,0,0]
	v_mfma_scale_f32_16x16x128_f8f6f4 v[250:253], v[170:177], v[88:95], v[0:3], v142, v142 op_sel_hi:[0,0,0]
	s_setprio 0
	s_barrier
	s_nop 4
	ds_read_b128 v[0:3], v143
	ds_read_b128 v[4:7], v143 offset:1024
	ds_read_b128 v[16:19], v143 offset:2048
	ds_read_b128 v[20:23], v143 offset:3072
	ds_read_b128 v[146:149], v144
	ds_read_b128 v[150:153], v144 offset:1024
	ds_read_b128 v[154:157], v144 offset:2048
	ds_read_b128 v[158:161], v144 offset:3072
	ds_read_b128 v[8:11], v141 offset:32768
	ds_read_b128 v[12:15], v141 offset:33792
	ds_read_b128 v[24:27], v141 offset:34816
	ds_read_b128 v[28:31], v141 offset:35840
	ds_read_b128 v[32:35], v141 offset:36864
	ds_read_b128 v[36:39], v141 offset:37888
	ds_read_b128 v[40:43], v141 offset:38912
	ds_read_b128 v[44:47], v141 offset:39936
	s_add_u32 s22, s26, 0x10000
	s_mov_b32 s15, m0
	s_mov_b32 m0, s37
	s_nop 0
	global_load_lds_dwordx4 v137, s[26:27]
	s_mov_b32 m0, s15
	s_addc_u32 s23, s27, 0
	s_mov_b32 s15, m0
	s_mov_b32 m0, s42
	s_nop 0
	global_load_lds_dwordx4 v137, s[22:23]
	s_mov_b32 m0, s15
	s_add_u32 s22, s26, 0x20000
	s_addc_u32 s23, s27, 0
	s_mov_b32 s15, m0
	s_mov_b32 m0, s43
	s_nop 0
	global_load_lds_dwordx4 v137, s[22:23]
	s_mov_b32 m0, s15
	s_add_u32 s22, s26, 0x30000
	s_addc_u32 s23, s27, 0
	s_mov_b32 s15, m0
	s_mov_b32 m0, s44
	s_nop 0
	global_load_lds_dwordx4 v137, s[22:23]
	s_mov_b32 m0, s15
	s_waitcnt vmcnt(8)
	s_waitcnt lgkmcnt(0)
	s_barrier
	s_setprio 1
	s_waitcnt lgkmcnt(6)
	v_mfma_scale_f32_16x16x128_f8f6f4 v[124:127], v[0:7], v[8:15], v[124:127], v142, v142 op_sel_hi:[0,0,0]
	v_mfma_scale_f32_16x16x128_f8f6f4 v[120:123], v[16:23], v[8:15], v[120:123], v142, v142 op_sel_hi:[0,0,0]
	s_waitcnt lgkmcnt(4)
	v_mfma_scale_f32_16x16x128_f8f6f4 v[116:119], v[0:7], v[24:31], v[116:119], v142, v142 op_sel_hi:[0,0,0]
	v_mfma_scale_f32_16x16x128_f8f6f4 v[112:115], v[16:23], v[24:31], v[112:115], v142, v142 op_sel_hi:[0,0,0]
	s_waitcnt lgkmcnt(2)
	v_mfma_scale_f32_16x16x128_f8f6f4 v[92:95], v[0:7], v[32:39], v[128:131], v142, v142 op_sel_hi:[0,0,0]
	v_mfma_scale_f32_16x16x128_f8f6f4 v[88:91], v[16:23], v[32:39], v[210:213], v142, v142 op_sel_hi:[0,0,0]
	s_waitcnt lgkmcnt(0)
	v_mfma_scale_f32_16x16x128_f8f6f4 v[84:87], v[0:7], v[40:47], v[214:217], v142, v142 op_sel_hi:[0,0,0]
	v_mfma_scale_f32_16x16x128_f8f6f4 v[80:83], v[16:23], v[40:47], v[218:221], v142, v142 op_sel_hi:[0,0,0]
	s_setprio 0
	s_setprio 1
	v_mfma_scale_f32_16x16x128_f8f6f4 v[108:111], v[146:153], v[8:15], v[108:111], v142, v142 op_sel_hi:[0,0,0]
	v_mfma_scale_f32_16x16x128_f8f6f4 v[104:107], v[154:161], v[8:15], v[104:107], v142, v142 op_sel_hi:[0,0,0]
	v_mfma_scale_f32_16x16x128_f8f6f4 v[100:103], v[146:153], v[24:31], v[100:103], v142, v142 op_sel_hi:[0,0,0]
	v_mfma_scale_f32_16x16x128_f8f6f4 v[96:99], v[154:161], v[24:31], v[96:99], v142, v142 op_sel_hi:[0,0,0]
	v_mfma_scale_f32_16x16x128_f8f6f4 v[76:79], v[146:153], v[32:39], v[178:181], v142, v142 op_sel_hi:[0,0,0]
	v_mfma_scale_f32_16x16x128_f8f6f4 v[72:75], v[154:161], v[32:39], v[182:185], v142, v142 op_sel_hi:[0,0,0]
	v_mfma_scale_f32_16x16x128_f8f6f4 v[68:71], v[146:153], v[40:47], v[186:189], v142, v142 op_sel_hi:[0,0,0]
	v_mfma_scale_f32_16x16x128_f8f6f4 v[64:67], v[154:161], v[40:47], v[190:193], v142, v142 op_sel_hi:[0,0,0]
	s_setprio 0
	s_barrier
	s_add_u32 s22, s30, 0x80
	s_addc_u32 s23, s31, 0
	ds_read_b128 v[32:35], v141 offset:49152
	ds_read_b128 v[36:39], v141 offset:50176
	ds_read_b128 v[162:165], v141 offset:51200
	ds_read_b128 v[166:169], v141 offset:52224
	ds_read_b128 v[170:173], v141 offset:53248
	ds_read_b128 v[174:177], v141 offset:54272
	ds_read_b128 v[178:181], v141 offset:55296
	ds_read_b128 v[182:185], v141 offset:56320
	s_mov_b32 s15, m0
	s_mov_b32 m0, s47
	s_nop 0
	global_load_lds_dwordx4 v136, s[22:23]
	s_mov_b32 m0, s15
	s_add_u32 s22, s30, 0x10080
	s_addc_u32 s23, s31, 0
	s_mov_b32 s15, m0
	s_mov_b32 m0, s49
	s_nop 0
	global_load_lds_dwordx4 v136, s[22:23]
	s_mov_b32 m0, s15
	s_add_u32 s22, s30, 0x20080
	s_addc_u32 s23, s31, 0
	s_mov_b32 s15, m0
	s_mov_b32 m0, s52
	s_nop 0
	global_load_lds_dwordx4 v136, s[22:23]
	s_mov_b32 m0, s15
	s_add_u32 s22, s30, 0x30080
	s_addc_u32 s23, s31, 0
	s_mov_b32 s15, m0
	s_mov_b32 m0, s53
	s_nop 0
	global_load_lds_dwordx4 v136, s[22:23]
	s_mov_b32 m0, s15
	s_add_u32 s22, s26, 0x10080
	s_mov_b32 s15, m0
	s_mov_b32 m0, s50
	s_nop 0
	global_load_lds_dwordx4 v137, s[28:29]
	s_mov_b32 m0, s15
	s_addc_u32 s23, s27, 0
	s_mov_b32 s15, m0
	s_mov_b32 m0, s51
	s_nop 0
	global_load_lds_dwordx4 v137, s[22:23]
	s_mov_b32 m0, s15
	s_waitcnt vmcnt(8)
	s_waitcnt lgkmcnt(0)
	s_barrier
	s_setprio 1
	s_waitcnt lgkmcnt(6)
	v_mfma_scale_f32_16x16x128_f8f6f4 v[60:63], v[0:7], v[32:39], v[60:63], v142, v142 op_sel_hi:[0,0,0]
	v_mfma_scale_f32_16x16x128_f8f6f4 v[56:59], v[16:23], v[32:39], v[56:59], v142, v142 op_sel_hi:[0,0,0]
	s_waitcnt lgkmcnt(4)
	v_mfma_scale_f32_16x16x128_f8f6f4 v[52:55], v[0:7], v[162:169], v[52:55], v142, v142 op_sel_hi:[0,0,0]
	v_mfma_scale_f32_16x16x128_f8f6f4 v[48:51], v[16:23], v[162:169], v[48:51], v142, v142 op_sel_hi:[0,0,0]
	s_waitcnt lgkmcnt(2)
	v_mfma_scale_f32_16x16x128_f8f6f4 v[28:31], v[0:7], v[170:177], v[194:197], v142, v142 op_sel_hi:[0,0,0]
	v_mfma_scale_f32_16x16x128_f8f6f4 v[24:27], v[16:23], v[170:177], v[198:201], v142, v142 op_sel_hi:[0,0,0]
	s_waitcnt lgkmcnt(0)
	v_mfma_scale_f32_16x16x128_f8f6f4 v[12:15], v[0:7], v[178:185], v[202:205], v142, v142 op_sel_hi:[0,0,0]
	v_mfma_scale_f32_16x16x128_f8f6f4 v[8:11], v[16:23], v[178:185], v[206:209], v142, v142 op_sel_hi:[0,0,0]
	s_setprio 0
	s_setprio 1
	v_mfma_scale_f32_16x16x128_f8f6f4 v[44:47], v[146:153], v[32:39], v[222:225], v142, v142 op_sel_hi:[0,0,0]
	v_mfma_scale_f32_16x16x128_f8f6f4 v[40:43], v[154:161], v[32:39], v[226:229], v142, v142 op_sel_hi:[0,0,0]
	v_mfma_scale_f32_16x16x128_f8f6f4 v[36:39], v[146:153], v[162:169], v[230:233], v142, v142 op_sel_hi:[0,0,0]
	v_mfma_scale_f32_16x16x128_f8f6f4 v[32:35], v[154:161], v[162:169], v[234:237], v142, v142 op_sel_hi:[0,0,0]
	v_mfma_scale_f32_16x16x128_f8f6f4 v[20:23], v[146:153], v[170:177], v[238:241], v142, v142 op_sel_hi:[0,0,0]
	v_mfma_scale_f32_16x16x128_f8f6f4 v[16:19], v[154:161], v[170:177], v[242:245], v142, v142 op_sel_hi:[0,0,0]
	v_mfma_scale_f32_16x16x128_f8f6f4 v[4:7], v[146:153], v[178:185], v[246:249], v142, v142 op_sel_hi:[0,0,0]
	v_mfma_scale_f32_16x16x128_f8f6f4 v[0:3], v[154:161], v[178:185], v[250:253], v142, v142 op_sel_hi:[0,0,0]
	s_setprio 0
	s_barrier
	s_add_i32 s13, s13, 2
	s_add_u32 s1, s1, 0x100
	s_addc_u32 s11, s11, 0
	s_cmp_gt_u32 s13, 5
	s_mov_b64 s[22:23], s[24:25]
	s_cbranch_scc0 .LBB0_1338
	s_and_b64 vcc, exec, s[8:9]
	s_cbranch_vccz .LBB0_1341
	s_barrier

.LBB0_1636:
	s_setprio 0
	s_cmp_lt_u32 s96, 64
	s_cbranch_scc1 .Ltc_skip_9
	v_writelane_b32 v200, s0, 0
	s_nop 1
	v_writelane_b32 v200, s1, 1
	s_nop 1
	v_writelane_b32 v200, s2, 2
	s_nop 1
	v_writelane_b32 v200, s3, 3
	s_nop 1
	v_writelane_b32 v200, s4, 4
	s_nop 1
	v_writelane_b32 v200, s5, 5
	s_nop 1
	v_writelane_b32 v200, s6, 6
	s_nop 1
	v_writelane_b32 v200, s7, 7
	s_nop 1
	v_writelane_b32 v200, s10, 8
	s_nop 1
	v_writelane_b32 v200, s11, 9
	s_nop 1
	v_writelane_b32 v200, s12, 10
	s_nop 1
	v_writelane_b32 v200, s13, 11
	s_nop 1
	v_writelane_b32 v200, s14, 12
	s_nop 1
	v_writelane_b32 v200, s15, 13
	s_nop 1
	v_writelane_b32 v200, s16, 14
	s_nop 1
	v_writelane_b32 v200, s17, 15
	s_nop 1
	v_writelane_b32 v200, s18, 16
	s_nop 1
	v_writelane_b32 v200, s19, 17
	s_nop 1
	v_writelane_b32 v200, s20, 18
	s_nop 1
	v_writelane_b32 v200, s21, 19
	s_nop 1
	v_writelane_b32 v200, s22, 20
	s_nop 1
	v_writelane_b32 v200, s23, 21
	s_nop 1
	v_writelane_b32 v200, s24, 22
	s_nop 1
	v_writelane_b32 v200, s25, 23
	s_nop 1
	v_writelane_b32 v200, s36, 24
	s_nop 1
	v_writelane_b32 v200, s37, 25
	s_nop 1
	v_writelane_b32 v200, s38, 26
	s_nop 1
	v_writelane_b32 v200, s39, 27
	s_nop 1
	v_writelane_b32 v200, s40, 28
	s_nop 1
	v_writelane_b32 v200, s41, 29
	s_nop 1
	v_writelane_b32 v200, s42, 30
	s_nop 1
	v_writelane_b32 v200, s43, 31
	s_nop 1
	v_writelane_b32 v200, s44, 32
	s_nop 1
	v_writelane_b32 v200, s45, 33
	s_nop 1
	v_writelane_b32 v200, s46, 34
	s_nop 1
	v_writelane_b32 v200, s47, 35
	s_nop 1
	v_writelane_b32 v200, s48, 36
	s_nop 1
	v_writelane_b32 v200, s49, 37
	s_nop 1
	v_writelane_b32 v200, s50, 38
	s_nop 1
	v_writelane_b32 v200, s51, 39
	s_nop 1
	s_mov_b32 s99, 9
	s_mov_b32 s98, 1
	s_mov_b32 s101, 192
	s_add_i32 s100, s96, 2752
	s_branch .Ltc_s1_back

.LBB0_2302:
	s_ashr_i32 s9, s8, 31
	s_lshl_b64 s[12:13], s[8:9], 18
	v_readlane_b32 s16, v254, 49
	v_readlane_b32 s17, v254, 50
	s_add_u32 s12, s16, s12
	s_addc_u32 s13, s17, s13
	s_and_b64 s[16:17], s[14:15], exec
	ds_read_b128 v[0:3], v203
	ds_read_b128 v[4:7], v203 offset:1024
	ds_read_b128 v[8:11], v203 offset:2048
	ds_read_b128 v[12:15], v203 offset:3072
	ds_read_b128 v[16:19], v204
	ds_read_b128 v[20:23], v204 offset:1024
	ds_read_b128 v[24:27], v204 offset:2048
	ds_read_b128 v[28:31], v204 offset:3072
	s_cselect_b32 s9, s13, s25
	s_cselect_b32 s54, s12, s24
	s_ashr_i32 s11, s10, 31
	s_lshl_b64 s[16:17], s[10:11], 18
	s_add_u32 s16, s33, s16
	s_addc_u32 s17, s34, s17
	s_and_b64 s[26:27], s[14:15], exec
	s_cselect_b32 s11, s17, s23
	s_cselect_b32 s55, s16, s22
	s_add_u32 s26, s24, 0x100
	s_addc_u32 s27, s25, 0
	s_add_u32 s28, s24, 0x180
	s_addc_u32 s29, s25, 0
	s_add_u32 s30, s22, 0x100
	s_addc_u32 s31, s23, 0
	ds_read_b128 v[32:35], v205
	ds_read_b128 v[36:39], v205 offset:1024
	ds_read_b128 v[40:43], v205 offset:2048
	ds_read_b128 v[44:47], v205 offset:3072
	ds_read_b128 v[48:51], v205 offset:4096
	ds_read_b128 v[52:55], v205 offset:5120
	ds_read_b128 v[56:59], v205 offset:6144
	ds_read_b128 v[60:63], v205 offset:7168
	s_add_u32 s56, s24, 0x20080
	s_addc_u32 s57, s25, 0
	s_mov_b32 s58, m0
	s_mov_b32 m0, s52
	s_nop 0
	global_load_lds_dwordx4 v202, s[56:57]
	s_mov_b32 m0, s58
	s_add_u32 s56, s24, 0x30080
	s_addc_u32 s57, s25, 0
	s_mov_b32 s58, m0
	s_mov_b32 m0, s53
	s_nop 0
	global_load_lds_dwordx4 v202, s[56:57]
	s_mov_b32 m0, s58
	s_waitcnt vmcnt(8)
	s_waitcnt lgkmcnt(0)
	s_barrier
	s_setprio 1
	s_waitcnt vmcnt(4) lgkmcnt(6)
	v_mfma_scale_f32_16x16x128_f8f6f4 v[64:67], v[0:7], v[32:39], 0, v206, v206 op_sel_hi:[0,0,0]
	s_waitcnt vmcnt(3)
	v_mfma_scale_f32_16x16x128_f8f6f4 v[68:71], v[8:15], v[32:39], 0, v206, v206 op_sel_hi:[0,0,0]
	s_waitcnt vmcnt(2) lgkmcnt(4)
	v_mfma_scale_f32_16x16x128_f8f6f4 v[72:75], v[0:7], v[40:47], 0, v206, v206 op_sel_hi:[0,0,0]
	s_waitcnt vmcnt(0)
	v_mfma_scale_f32_16x16x128_f8f6f4 v[76:79], v[8:15], v[40:47], 0, v206, v206 op_sel_hi:[0,0,0]
	s_waitcnt lgkmcnt(2)
	v_mfma_scale_f32_16x16x128_f8f6f4 v[80:83], v[0:7], v[48:55], 0, v206, v206 op_sel_hi:[0,0,0]
	v_mfma_scale_f32_16x16x128_f8f6f4 v[84:87], v[8:15], v[48:55], 0, v206, v206 op_sel_hi:[0,0,0]
	s_waitcnt lgkmcnt(0)
	v_mfma_scale_f32_16x16x128_f8f6f4 v[88:91], v[0:7], v[56:63], 0, v206, v206 op_sel_hi:[0,0,0]
	v_mfma_scale_f32_16x16x128_f8f6f4 v[100:103], v[8:15], v[56:63], 0, v206, v206 op_sel_hi:[0,0,0]
	s_setprio 0
	s_setprio 1
	v_mfma_scale_f32_16x16x128_f8f6f4 v[108:111], v[16:23], v[32:39], 0, v206, v206 op_sel_hi:[0,0,0]
	v_mfma_scale_f32_16x16x128_f8f6f4 v[120:123], v[24:31], v[32:39], 0, v206, v206 op_sel_hi:[0,0,0]
	v_mfma_scale_f32_16x16x128_f8f6f4 v[132:135], v[16:23], v[40:47], 0, v206, v206 op_sel_hi:[0,0,0]
	v_mfma_scale_f32_16x16x128_f8f6f4 v[152:155], v[24:31], v[40:47], 0, v206, v206 op_sel_hi:[0,0,0]
	v_mfma_scale_f32_16x16x128_f8f6f4 v[156:159], v[16:23], v[48:55], 0, v206, v206 op_sel_hi:[0,0,0]
	v_mfma_scale_f32_16x16x128_f8f6f4 v[160:163], v[24:31], v[48:55], 0, v206, v206 op_sel_hi:[0,0,0]
	v_mfma_scale_f32_16x16x128_f8f6f4 v[164:167], v[16:23], v[56:63], 0, v206, v206 op_sel_hi:[0,0,0]
	v_mfma_scale_f32_16x16x128_f8f6f4 v[168:171], v[24:31], v[56:63], 0, v206, v206 op_sel_hi:[0,0,0]
	s_setprio 0
	s_barrier
	ds_read_b128 v[32:35], v205 offset:16384
	ds_read_b128 v[36:39], v205 offset:17408
	ds_read_b128 v[40:43], v205 offset:18432
	ds_read_b128 v[44:47], v205 offset:19456
	ds_read_b128 v[48:51], v205 offset:20480
	ds_read_b128 v[52:55], v205 offset:21504
	ds_read_b128 v[56:59], v205 offset:22528
	ds_read_b128 v[60:63], v205 offset:23552
	s_mov_b32 s56, m0
	s_mov_b32 m0, s19
	s_nop 0
	global_load_lds_dwordx4 v201, s[30:31]
	s_mov_b32 m0, s56
	s_add_u32 s30, s22, 0x10100
	s_addc_u32 s31, s23, 0
	s_mov_b32 s56, m0
	s_mov_b32 m0, s21
	s_nop 0
	global_load_lds_dwordx4 v201, s[30:31]
	s_mov_b32 m0, s56
	s_add_u32 s30, s22, 0x20100
	s_addc_u32 s31, s23, 0
	s_mov_b32 s56, m0
	s_mov_b32 m0, s36
	s_nop 0
	global_load_lds_dwordx4 v201, s[30:31]
	s_mov_b32 m0, s56
	s_add_u32 s30, s22, 0x30100
	s_addc_u32 s31, s23, 0
	s_mov_b32 s56, m0
	s_mov_b32 m0, s37
	s_nop 0
	global_load_lds_dwordx4 v201, s[30:31]
	s_mov_b32 m0, s56
	s_waitcnt vmcnt(6)
	s_waitcnt lgkmcnt(0)
	s_barrier
	s_setprio 1
	s_waitcnt lgkmcnt(6)
	v_mfma_scale_f32_16x16x128_f8f6f4 v[176:179], v[0:7], v[32:39], 0, v206, v206 op_sel_hi:[0,0,0]
	v_mfma_scale_f32_16x16x128_f8f6f4 v[180:183], v[8:15], v[32:39], 0, v206, v206 op_sel_hi:[0,0,0]
	s_waitcnt lgkmcnt(4)
	v_mfma_scale_f32_16x16x128_f8f6f4 v[184:187], v[0:7], v[40:47], 0, v206, v206 op_sel_hi:[0,0,0]
	v_mfma_scale_f32_16x16x128_f8f6f4 v[188:191], v[8:15], v[40:47], 0, v206, v206 op_sel_hi:[0,0,0]
	s_waitcnt lgkmcnt(2)
	v_mfma_scale_f32_16x16x128_f8f6f4 v[192:195], v[0:7], v[48:55], 0, v206, v206 op_sel_hi:[0,0,0]
	v_mfma_scale_f32_16x16x128_f8f6f4 v[196:199], v[8:15], v[48:55], 0, v206, v206 op_sel_hi:[0,0,0]
	s_waitcnt lgkmcnt(0)
	v_mfma_scale_f32_16x16x128_f8f6f4 v[210:213], v[0:7], v[56:63], 0, v206, v206 op_sel_hi:[0,0,0]
	v_mfma_scale_f32_16x16x128_f8f6f4 v[214:217], v[8:15], v[56:63], 0, v206, v206 op_sel_hi:[0,0,0]
	s_setprio 0
	s_setprio 1
	v_mfma_scale_f32_16x16x128_f8f6f4 v[218:221], v[16:23], v[32:39], 0, v206, v206 op_sel_hi:[0,0,0]
	v_mfma_scale_f32_16x16x128_f8f6f4 v[222:225], v[24:31], v[32:39], 0, v206, v206 op_sel_hi:[0,0,0]
	v_mfma_scale_f32_16x16x128_f8f6f4 v[226:229], v[16:23], v[40:47], 0, v206, v206 op_sel_hi:[0,0,0]
	v_mfma_scale_f32_16x16x128_f8f6f4 v[230:233], v[24:31], v[40:47], 0, v206, v206 op_sel_hi:[0,0,0]
	v_mfma_scale_f32_16x16x128_f8f6f4 v[234:237], v[16:23], v[48:55], 0, v206, v206 op_sel_hi:[0,0,0]
	v_mfma_scale_f32_16x16x128_f8f6f4 v[238:241], v[24:31], v[48:55], 0, v206, v206 op_sel_hi:[0,0,0]
	v_mfma_scale_f32_16x16x128_f8f6f4 v[242:245], v[16:23], v[56:63], 0, v206, v206 op_sel_hi:[0,0,0]
	v_mfma_scale_f32_16x16x128_f8f6f4 v[246:249], v[24:31], v[56:63], 0, v206, v206 op_sel_hi:[0,0,0]
	s_setprio 0
	s_barrier
	ds_read_b128 v[0:3], v207
	ds_read_b128 v[4:7], v207 offset:1024
	ds_read_b128 v[16:19], v207 offset:2048
	ds_read_b128 v[20:23], v207 offset:3072
	ds_read_b128 v[112:115], v208
	ds_read_b128 v[116:119], v208 offset:1024
	ds_read_b128 v[144:147], v208 offset:2048
	ds_read_b128 v[148:151], v208 offset:3072
	ds_read_b128 v[8:11], v205 offset:32768
	ds_read_b128 v[12:15], v205 offset:33792
	ds_read_b128 v[24:27], v205 offset:34816
	ds_read_b128 v[28:31], v205 offset:35840
	ds_read_b128 v[32:35], v205 offset:36864
	ds_read_b128 v[36:39], v205 offset:37888
	ds_read_b128 v[40:43], v205 offset:38912
	ds_read_b128 v[44:47], v205 offset:39936
	s_mov_b32 s30, m0
	s_mov_b32 m0, s35
	s_nop 0
	global_load_lds_dwordx4 v202, s[26:27]
	s_mov_b32 m0, s30
	s_add_u32 s30, s24, 0x10100
	s_addc_u32 s31, s25, 0
	s_mov_b32 s56, m0
	s_mov_b32 m0, s38
	s_nop 0
	global_load_lds_dwordx4 v202, s[30:31]
	s_mov_b32 m0, s56
	s_add_u32 s30, s24, 0x20100
	s_addc_u32 s31, s25, 0
	s_mov_b32 s56, m0
	s_mov_b32 m0, s39
	s_nop 0
	global_load_lds_dwordx4 v202, s[30:31]
	s_mov_b32 m0, s56
	s_add_u32 s30, s24, 0x30100
	s_addc_u32 s31, s25, 0
	s_mov_b32 s56, m0
	s_mov_b32 m0, s40
	s_nop 0
	global_load_lds_dwordx4 v202, s[30:31]
	s_mov_b32 m0, s56
	s_waitcnt vmcnt(8)
	s_waitcnt lgkmcnt(0)
	s_barrier
	s_setprio 1
	s_waitcnt lgkmcnt(6)
	v_mfma_scale_f32_16x16x128_f8f6f4 v[128:131], v[0:7], v[8:15], v[64:67], v206, v206 op_sel_hi:[0,0,0]
	v_mfma_scale_f32_16x16x128_f8f6f4 v[124:127], v[16:23], v[8:15], v[68:71], v206, v206 op_sel_hi:[0,0,0]
	s_waitcnt lgkmcnt(4)
	v_mfma_scale_f32_16x16x128_f8f6f4 v[104:107], v[0:7], v[24:31], v[72:75], v206, v206 op_sel_hi:[0,0,0]
	v_mfma_scale_f32_16x16x128_f8f6f4 v[96:99], v[16:23], v[24:31], v[76:79], v206, v206 op_sel_hi:[0,0,0]
	s_waitcnt lgkmcnt(2)
	v_mfma_scale_f32_16x16x128_f8f6f4 v[92:95], v[0:7], v[32:39], v[80:83], v206, v206 op_sel_hi:[0,0,0]
	v_mfma_scale_f32_16x16x128_f8f6f4 v[84:87], v[16:23], v[32:39], v[84:87], v206, v206 op_sel_hi:[0,0,0]
	s_waitcnt lgkmcnt(0)
	v_mfma_scale_f32_16x16x128_f8f6f4 v[68:71], v[0:7], v[40:47], v[88:91], v206, v206 op_sel_hi:[0,0,0]
	v_mfma_scale_f32_16x16x128_f8f6f4 v[56:59], v[16:23], v[40:47], v[100:103], v206, v206 op_sel_hi:[0,0,0]
	s_setprio 0
	s_setprio 1
	v_mfma_scale_f32_16x16x128_f8f6f4 v[140:143], v[112:119], v[8:15], v[108:111], v206, v206 op_sel_hi:[0,0,0]
	v_mfma_scale_f32_16x16x128_f8f6f4 v[136:139], v[144:151], v[8:15], v[120:123], v206, v206 op_sel_hi:[0,0,0]
	v_mfma_scale_f32_16x16x128_f8f6f4 v[108:111], v[112:119], v[24:31], v[132:135], v206, v206 op_sel_hi:[0,0,0]
	v_mfma_scale_f32_16x16x128_f8f6f4 v[100:103], v[144:151], v[24:31], v[152:155], v206, v206 op_sel_hi:[0,0,0]
	v_mfma_scale_f32_16x16x128_f8f6f4 v[88:91], v[112:119], v[32:39], v[156:159], v206, v206 op_sel_hi:[0,0,0]
	v_mfma_scale_f32_16x16x128_f8f6f4 v[80:83], v[144:151], v[32:39], v[160:163], v206, v206 op_sel_hi:[0,0,0]
	v_mfma_scale_f32_16x16x128_f8f6f4 v[52:55], v[112:119], v[40:47], v[164:167], v206, v206 op_sel_hi:[0,0,0]
	v_mfma_scale_f32_16x16x128_f8f6f4 v[48:51], v[144:151], v[40:47], v[168:171], v206, v206 op_sel_hi:[0,0,0]
	s_setprio 0
	s_barrier
	s_add_u32 s30, s22, 0x180
	s_addc_u32 s31, s23, 0
	ds_read_b128 v[32:35], v205 offset:49152
	ds_read_b128 v[36:39], v205 offset:50176
	ds_read_b128 v[152:155], v205 offset:51200
	ds_read_b128 v[156:159], v205 offset:52224
	ds_read_b128 v[160:163], v205 offset:53248
	ds_read_b128 v[164:167], v205 offset:54272
	ds_read_b128 v[168:171], v205 offset:55296
	ds_read_b128 v[172:175], v205 offset:56320
	s_mov_b32 s56, m0
	s_mov_b32 m0, s46
	s_nop 0
	global_load_lds_dwordx4 v201, s[30:31]
	s_mov_b32 m0, s56
	s_add_u32 s30, s22, 0x10180
	s_addc_u32 s31, s23, 0
	s_mov_b32 s56, m0
	s_mov_b32 m0, s47
	s_nop 0
	global_load_lds_dwordx4 v201, s[30:31]
	s_mov_b32 m0, s56
	s_add_u32 s30, s22, 0x20180
	s_addc_u32 s31, s23, 0
	s_mov_b32 s56, m0
	s_mov_b32 m0, s50
	s_nop 0
	global_load_lds_dwordx4 v201, s[30:31]
	s_mov_b32 m0, s56
	s_add_u32 s30, s22, 0x30180
	s_addc_u32 s31, s23, 0
	s_mov_b32 s56, m0
	s_mov_b32 m0, s51
	s_nop 0
	global_load_lds_dwordx4 v201, s[30:31]
	s_mov_b32 m0, s56
	s_mov_b32 s30, m0
	s_mov_b32 m0, s48
	s_nop 0
	global_load_lds_dwordx4 v202, s[28:29]
	s_mov_b32 m0, s30
	s_add_u32 s24, s24, 0x10180
	s_addc_u32 s25, s25, 0
	s_mov_b32 s28, m0
	s_mov_b32 m0, s49
	s_nop 0
	global_load_lds_dwordx4 v202, s[24:25]
	s_mov_b32 m0, s28
	s_waitcnt vmcnt(8)
	s_waitcnt lgkmcnt(0)
	s_barrier
	s_setprio 1
	s_waitcnt lgkmcnt(6)
	v_mfma_scale_f32_16x16x128_f8f6f4 v[76:79], v[0:7], v[32:39], v[176:179], v206, v206 op_sel_hi:[0,0,0]
	v_mfma_scale_f32_16x16x128_f8f6f4 v[64:67], v[16:23], v[32:39], v[180:183], v206, v206 op_sel_hi:[0,0,0]
	s_waitcnt lgkmcnt(4)
	v_mfma_scale_f32_16x16x128_f8f6f4 v[44:47], v[0:7], v[152:159], v[184:187], v206, v206 op_sel_hi:[0,0,0]
	v_mfma_scale_f32_16x16x128_f8f6f4 v[40:43], v[16:23], v[152:159], v[188:191], v206, v206 op_sel_hi:[0,0,0]
	s_waitcnt lgkmcnt(2)
	v_mfma_scale_f32_16x16x128_f8f6f4 v[28:31], v[0:7], v[160:167], v[192:195], v206, v206 op_sel_hi:[0,0,0]
	v_mfma_scale_f32_16x16x128_f8f6f4 v[24:27], v[16:23], v[160:167], v[196:199], v206, v206 op_sel_hi:[0,0,0]
	s_waitcnt lgkmcnt(0)
	v_mfma_scale_f32_16x16x128_f8f6f4 v[12:15], v[0:7], v[168:175], v[210:213], v206, v206 op_sel_hi:[0,0,0]
	v_mfma_scale_f32_16x16x128_f8f6f4 v[8:11], v[16:23], v[168:175], v[214:217], v206, v206 op_sel_hi:[0,0,0]
	s_setprio 0
	s_setprio 1
	v_mfma_scale_f32_16x16x128_f8f6f4 v[72:75], v[112:119], v[32:39], v[218:221], v206, v206 op_sel_hi:[0,0,0]
	v_mfma_scale_f32_16x16x128_f8f6f4 v[60:63], v[144:151], v[32:39], v[222:225], v206, v206 op_sel_hi:[0,0,0]
	v_mfma_scale_f32_16x16x128_f8f6f4 v[36:39], v[112:119], v[152:159], v[226:229], v206, v206 op_sel_hi:[0,0,0]
	v_mfma_scale_f32_16x16x128_f8f6f4 v[32:35], v[144:151], v[152:159], v[230:233], v206, v206 op_sel_hi:[0,0,0]
	v_mfma_scale_f32_16x16x128_f8f6f4 v[20:23], v[112:119], v[160:167], v[234:237], v206, v206 op_sel_hi:[0,0,0]
	v_mfma_scale_f32_16x16x128_f8f6f4 v[16:19], v[144:151], v[160:167], v[238:241], v206, v206 op_sel_hi:[0,0,0]
	v_mfma_scale_f32_16x16x128_f8f6f4 v[4:7], v[112:119], v[168:175], v[242:245], v206, v206 op_sel_hi:[0,0,0]
	v_mfma_scale_f32_16x16x128_f8f6f4 v[0:3], v[144:151], v[168:175], v[246:249], v206, v206 op_sel_hi:[0,0,0]
	s_setprio 0
	s_barrier
	s_add_u32 s56, s22, 0x200
	s_addc_u32 s57, s23, 0
	s_mov_b32 s58, 0
.LBB0_2303:
	ds_read_b128 v[112:115], v203
	ds_read_b128 v[116:119], v203 offset:1024
	ds_read_b128 v[144:147], v203 offset:2048
	ds_read_b128 v[148:151], v203 offset:3072
	ds_read_b128 v[152:155], v204
	ds_read_b128 v[156:159], v204 offset:1024
	ds_read_b128 v[160:163], v204 offset:2048
	ds_read_b128 v[164:167], v204 offset:3072
	s_add_u32 s22, s26, 0x100
	s_addc_u32 s23, s27, 0
	s_cmp_eq_u32 s58, 4
	s_cselect_b32 s24, s54, s22
	s_cselect_b32 s25, s9, s23
	s_cselect_b32 s30, s55, s56
	s_cselect_b32 s31, s11, s57
	s_add_u32 s28, s24, 0x80
	s_addc_u32 s29, s25, 0
	ds_read_b128 v[168:171], v205
	ds_read_b128 v[172:175], v205 offset:1024
	ds_read_b128 v[176:179], v205 offset:2048
	ds_read_b128 v[180:183], v205 offset:3072
	ds_read_b128 v[184:187], v205 offset:4096
	ds_read_b128 v[188:191], v205 offset:5120
	ds_read_b128 v[192:195], v205 offset:6144
	ds_read_b128 v[196:199], v205 offset:7168
	s_add_u32 s60, s26, 0x20080
	s_addc_u32 s61, s27, 0
	s_mov_b32 s59, m0
	s_mov_b32 m0, s52
	s_nop 0
	global_load_lds_dwordx4 v202, s[60:61]
	s_mov_b32 m0, s59
	s_add_u32 s26, s26, 0x30080
	s_addc_u32 s27, s27, 0
	s_mov_b32 s59, m0
	s_mov_b32 m0, s53
	s_nop 0
	global_load_lds_dwordx4 v202, s[26:27]
	s_mov_b32 m0, s59
	s_waitcnt vmcnt(8)
	s_waitcnt lgkmcnt(0)
	s_barrier
	s_setprio 1
	s_waitcnt lgkmcnt(6)
	v_mfma_scale_f32_16x16x128_f8f6f4 v[124:127], v[144:151], v[168:175], v[124:127], v206, v206 op_sel_hi:[0,0,0]
	s_waitcnt lgkmcnt(4)
	v_mfma_scale_f32_16x16x128_f8f6f4 v[104:107], v[112:119], v[176:183], v[104:107], v206, v206 op_sel_hi:[0,0,0]
	s_waitcnt lgkmcnt(0)
	v_mfma_scale_f32_16x16x128_f8f6f4 v[68:71], v[112:119], v[192:199], v[68:71], v206, v206 op_sel_hi:[0,0,0]
	v_mfma_scale_f32_16x16x128_f8f6f4 v[56:59], v[144:151], v[192:199], v[56:59], v206, v206 op_sel_hi:[0,0,0]
	v_mfma_scale_f32_16x16x128_f8f6f4 v[120:123], v[112:119], v[168:175], v[128:131], v206, v206 op_sel_hi:[0,0,0]
	v_mfma_scale_f32_16x16x128_f8f6f4 v[132:135], v[144:151], v[176:183], v[96:99], v206, v206 op_sel_hi:[0,0,0]
	v_mfma_scale_f32_16x16x128_f8f6f4 v[210:213], v[112:119], v[184:191], v[92:95], v206, v206 op_sel_hi:[0,0,0]
	v_mfma_scale_f32_16x16x128_f8f6f4 v[214:217], v[144:151], v[184:191], v[84:87], v206, v206 op_sel_hi:[0,0,0]
	s_setprio 0
	s_setprio 1
	v_mfma_scale_f32_16x16x128_f8f6f4 v[140:143], v[152:159], v[168:175], v[140:143], v206, v206 op_sel_hi:[0,0,0]
	v_mfma_scale_f32_16x16x128_f8f6f4 v[136:139], v[160:167], v[168:175], v[136:139], v206, v206 op_sel_hi:[0,0,0]
	v_mfma_scale_f32_16x16x128_f8f6f4 v[108:111], v[152:159], v[176:183], v[108:111], v206, v206 op_sel_hi:[0,0,0]
	v_mfma_scale_f32_16x16x128_f8f6f4 v[168:171], v[160:167], v[176:183], v[100:103], v206, v206 op_sel_hi:[0,0,0]
	v_mfma_scale_f32_16x16x128_f8f6f4 v[172:175], v[152:159], v[184:191], v[88:91], v206, v206 op_sel_hi:[0,0,0]
	v_mfma_scale_f32_16x16x128_f8f6f4 v[176:179], v[160:167], v[184:191], v[80:83], v206, v206 op_sel_hi:[0,0,0]
	v_mfma_scale_f32_16x16x128_f8f6f4 v[180:183], v[152:159], v[192:199], v[52:55], v206, v206 op_sel_hi:[0,0,0]
	v_mfma_scale_f32_16x16x128_f8f6f4 v[184:187], v[160:167], v[192:199], v[48:51], v206, v206 op_sel_hi:[0,0,0]
	s_setprio 0
	s_barrier
	s_nop 4
	ds_read_b128 v[48:51], v205 offset:16384
	ds_read_b128 v[52:55], v205 offset:17408
	ds_read_b128 v[80:83], v205 offset:18432
	ds_read_b128 v[84:87], v205 offset:19456
	ds_read_b128 v[88:91], v205 offset:20480
	ds_read_b128 v[92:95], v205 offset:21504
	ds_read_b128 v[96:99], v205 offset:22528
	ds_read_b128 v[100:103], v205 offset:23552
	s_mov_b32 s26, m0
	s_mov_b32 m0, s19
	s_nop 0
	global_load_lds_dwordx4 v201, s[30:31]
	s_mov_b32 m0, s26
	s_add_u32 s26, s30, 0x10000
	s_addc_u32 s27, s31, 0
	s_mov_b32 s59, m0
	s_mov_b32 m0, s21
	s_nop 0
	global_load_lds_dwordx4 v201, s[26:27]
	s_mov_b32 m0, s59
	s_add_u32 s26, s30, 0x20000
	s_addc_u32 s27, s31, 0
	s_mov_b32 s59, m0
	s_mov_b32 m0, s36
	s_nop 0
	global_load_lds_dwordx4 v201, s[26:27]
	s_mov_b32 m0, s59
	s_add_u32 s26, s30, 0x30000
	s_addc_u32 s27, s31, 0
	s_mov_b32 s59, m0
	s_mov_b32 m0, s37
	s_nop 0
	global_load_lds_dwordx4 v201, s[26:27]
	s_mov_b32 m0, s59
	s_waitcnt vmcnt(6)
	s_waitcnt lgkmcnt(0)
	s_barrier
	s_setprio 1
	s_waitcnt lgkmcnt(6)
	v_mfma_scale_f32_16x16x128_f8f6f4 v[76:79], v[112:119], v[48:55], v[76:79], v206, v206 op_sel_hi:[0,0,0]
	v_mfma_scale_f32_16x16x128_f8f6f4 v[64:67], v[144:151], v[48:55], v[64:67], v206, v206 op_sel_hi:[0,0,0]
	s_waitcnt lgkmcnt(4)
	v_mfma_scale_f32_16x16x128_f8f6f4 v[188:191], v[112:119], v[80:87], v[44:47], v206, v206 op_sel_hi:[0,0,0]
	v_mfma_scale_f32_16x16x128_f8f6f4 v[192:195], v[144:151], v[80:87], v[40:43], v206, v206 op_sel_hi:[0,0,0]
	s_waitcnt lgkmcnt(2)
	v_mfma_scale_f32_16x16x128_f8f6f4 v[196:199], v[112:119], v[88:95], v[28:31], v206, v206 op_sel_hi:[0,0,0]
	v_mfma_scale_f32_16x16x128_f8f6f4 v[218:221], v[144:151], v[88:95], v[24:27], v206, v206 op_sel_hi:[0,0,0]
	s_waitcnt lgkmcnt(0)
	v_mfma_scale_f32_16x16x128_f8f6f4 v[222:225], v[112:119], v[96:103], v[12:15], v206, v206 op_sel_hi:[0,0,0]
	v_mfma_scale_f32_16x16x128_f8f6f4 v[226:229], v[144:151], v[96:103], v[8:11], v206, v206 op_sel_hi:[0,0,0]
	s_setprio 0
	s_setprio 1
	v_mfma_scale_f32_16x16x128_f8f6f4 v[72:75], v[152:159], v[48:55], v[72:75], v206, v206 op_sel_hi:[0,0,0]
	v_mfma_scale_f32_16x16x128_f8f6f4 v[60:63], v[160:167], v[48:55], v[60:63], v206, v206 op_sel_hi:[0,0,0]
	v_mfma_scale_f32_16x16x128_f8f6f4 v[230:233], v[152:159], v[80:87], v[36:39], v206, v206 op_sel_hi:[0,0,0]
	v_mfma_scale_f32_16x16x128_f8f6f4 v[234:237], v[160:167], v[80:87], v[32:35], v206, v206 op_sel_hi:[0,0,0]
	v_mfma_scale_f32_16x16x128_f8f6f4 v[238:241], v[152:159], v[88:95], v[20:23], v206, v206 op_sel_hi:[0,0,0]
	v_mfma_scale_f32_16x16x128_f8f6f4 v[242:245], v[160:167], v[88:95], v[16:19], v206, v206 op_sel_hi:[0,0,0]
	v_mfma_scale_f32_16x16x128_f8f6f4 v[246:249], v[152:159], v[96:103], v[4:7], v206, v206 op_sel_hi:[0,0,0]
	v_mfma_scale_f32_16x16x128_f8f6f4 v[250:253], v[160:167], v[96:103], v[0:3], v206, v206 op_sel_hi:[0,0,0]
	s_setprio 0
	s_barrier
	s_nop 4
	ds_read_b128 v[0:3], v207
	ds_read_b128 v[4:7], v207 offset:1024
	ds_read_b128 v[16:19], v207 offset:2048
	ds_read_b128 v[20:23], v207 offset:3072
	ds_read_b128 v[112:115], v208
	ds_read_b128 v[116:119], v208 offset:1024
	ds_read_b128 v[144:147], v208 offset:2048
	ds_read_b128 v[148:151], v208 offset:3072
	ds_read_b128 v[8:11], v205 offset:32768
	ds_read_b128 v[12:15], v205 offset:33792
	ds_read_b128 v[24:27], v205 offset:34816
	ds_read_b128 v[28:31], v205 offset:35840
	ds_read_b128 v[32:35], v205 offset:36864
	ds_read_b128 v[36:39], v205 offset:37888
	ds_read_b128 v[40:43], v205 offset:38912
	ds_read_b128 v[44:47], v205 offset:39936
	s_mov_b32 s26, m0
	s_mov_b32 m0, s35
	s_nop 0
	global_load_lds_dwordx4 v202, s[24:25]
	s_mov_b32 m0, s26
	s_add_u32 s26, s24, 0x10000
	s_addc_u32 s27, s25, 0
	s_mov_b32 s59, m0
	s_mov_b32 m0, s38
	s_nop 0
	global_load_lds_dwordx4 v202, s[26:27]
	s_mov_b32 m0, s59
	s_add_u32 s26, s24, 0x20000
	s_addc_u32 s27, s25, 0
	s_mov_b32 s59, m0
	s_mov_b32 m0, s39
	s_nop 0
	global_load_lds_dwordx4 v202, s[26:27]
	s_mov_b32 m0, s59
	s_add_u32 s26, s24, 0x30000
	s_addc_u32 s27, s25, 0
	s_mov_b32 s59, m0
	s_mov_b32 m0, s40
	s_nop 0
	global_load_lds_dwordx4 v202, s[26:27]
	s_mov_b32 m0, s59
	s_waitcnt vmcnt(8)
	s_waitcnt lgkmcnt(0)
	s_barrier
	s_setprio 1
	s_waitcnt lgkmcnt(6)
	v_mfma_scale_f32_16x16x128_f8f6f4 v[128:131], v[0:7], v[8:15], v[120:123], v206, v206 op_sel_hi:[0,0,0]
	v_mfma_scale_f32_16x16x128_f8f6f4 v[124:127], v[16:23], v[8:15], v[124:127], v206, v206 op_sel_hi:[0,0,0]
	s_waitcnt lgkmcnt(4)
	v_mfma_scale_f32_16x16x128_f8f6f4 v[104:107], v[0:7], v[24:31], v[104:107], v206, v206 op_sel_hi:[0,0,0]
	v_mfma_scale_f32_16x16x128_f8f6f4 v[96:99], v[16:23], v[24:31], v[132:135], v206, v206 op_sel_hi:[0,0,0]
	s_waitcnt lgkmcnt(2)
	v_mfma_scale_f32_16x16x128_f8f6f4 v[92:95], v[0:7], v[32:39], v[210:213], v206, v206 op_sel_hi:[0,0,0]
	v_mfma_scale_f32_16x16x128_f8f6f4 v[84:87], v[16:23], v[32:39], v[214:217], v206, v206 op_sel_hi:[0,0,0]
	s_waitcnt lgkmcnt(0)
	v_mfma_scale_f32_16x16x128_f8f6f4 v[68:71], v[0:7], v[40:47], v[68:71], v206, v206 op_sel_hi:[0,0,0]
	v_mfma_scale_f32_16x16x128_f8f6f4 v[56:59], v[16:23], v[40:47], v[56:59], v206, v206 op_sel_hi:[0,0,0]
	s_setprio 0
	s_setprio 1
	v_mfma_scale_f32_16x16x128_f8f6f4 v[140:143], v[112:119], v[8:15], v[140:143], v206, v206 op_sel_hi:[0,0,0]
	v_mfma_scale_f32_16x16x128_f8f6f4 v[136:139], v[144:151], v[8:15], v[136:139], v206, v206 op_sel_hi:[0,0,0]
	v_mfma_scale_f32_16x16x128_f8f6f4 v[108:111], v[112:119], v[24:31], v[108:111], v206, v206 op_sel_hi:[0,0,0]
	v_mfma_scale_f32_16x16x128_f8f6f4 v[100:103], v[144:151], v[24:31], v[168:171], v206, v206 op_sel_hi:[0,0,0]
	v_mfma_scale_f32_16x16x128_f8f6f4 v[88:91], v[112:119], v[32:39], v[172:175], v206, v206 op_sel_hi:[0,0,0]
	v_mfma_scale_f32_16x16x128_f8f6f4 v[80:83], v[144:151], v[32:39], v[176:179], v206, v206 op_sel_hi:[0,0,0]
	v_mfma_scale_f32_16x16x128_f8f6f4 v[52:55], v[112:119], v[40:47], v[180:183], v206, v206 op_sel_hi:[0,0,0]
	v_mfma_scale_f32_16x16x128_f8f6f4 v[48:51], v[144:151], v[40:47], v[184:187], v206, v206 op_sel_hi:[0,0,0]
	s_setprio 0
	s_barrier
	s_add_u32 s26, s30, 0x80
	s_addc_u32 s27, s31, 0
	ds_read_b128 v[32:35], v205 offset:49152
	ds_read_b128 v[36:39], v205 offset:50176
	ds_read_b128 v[152:155], v205 offset:51200
	ds_read_b128 v[156:159], v205 offset:52224
	ds_read_b128 v[160:163], v205 offset:53248
	ds_read_b128 v[164:167], v205 offset:54272
	ds_read_b128 v[168:171], v205 offset:55296
	ds_read_b128 v[172:175], v205 offset:56320
	s_mov_b32 s59, m0
	s_mov_b32 m0, s46
	s_nop 0
	global_load_lds_dwordx4 v201, s[26:27]
	s_mov_b32 m0, s59
	s_add_u32 s26, s30, 0x10080
	s_addc_u32 s27, s31, 0
	s_mov_b32 s59, m0
	s_mov_b32 m0, s47
	s_nop 0
	global_load_lds_dwordx4 v201, s[26:27]
	s_mov_b32 m0, s59
	s_add_u32 s26, s30, 0x20080
	s_addc_u32 s27, s31, 0
	s_mov_b32 s59, m0
	s_mov_b32 m0, s50
	s_nop 0
	global_load_lds_dwordx4 v201, s[26:27]
	s_mov_b32 m0, s59
	s_add_u32 s26, s30, 0x30080
	s_addc_u32 s27, s31, 0
	s_mov_b32 s30, m0
	s_mov_b32 m0, s51
	s_nop 0
	global_load_lds_dwordx4 v201, s[26:27]
	s_mov_b32 m0, s30
	s_mov_b32 s26, m0
	s_mov_b32 m0, s48
	s_nop 0
	global_load_lds_dwordx4 v202, s[28:29]
	s_mov_b32 m0, s26
	s_add_u32 s24, s24, 0x10080
	s_addc_u32 s25, s25, 0
	s_mov_b32 s26, m0
	s_mov_b32 m0, s49
	s_nop 0
	global_load_lds_dwordx4 v202, s[24:25]
	s_mov_b32 m0, s26
	s_waitcnt vmcnt(8)
	s_waitcnt lgkmcnt(0)
	s_barrier
	s_setprio 1
	s_waitcnt lgkmcnt(6)
	v_mfma_scale_f32_16x16x128_f8f6f4 v[76:79], v[0:7], v[32:39], v[76:79], v206, v206 op_sel_hi:[0,0,0]
	v_mfma_scale_f32_16x16x128_f8f6f4 v[64:67], v[16:23], v[32:39], v[64:67], v206, v206 op_sel_hi:[0,0,0]
	s_waitcnt lgkmcnt(4)
	v_mfma_scale_f32_16x16x128_f8f6f4 v[44:47], v[0:7], v[152:159], v[188:191], v206, v206 op_sel_hi:[0,0,0]
	v_mfma_scale_f32_16x16x128_f8f6f4 v[40:43], v[16:23], v[152:159], v[192:195], v206, v206 op_sel_hi:[0,0,0]
	s_waitcnt lgkmcnt(2)
	v_mfma_scale_f32_16x16x128_f8f6f4 v[28:31], v[0:7], v[160:167], v[196:199], v206, v206 op_sel_hi:[0,0,0]
	v_mfma_scale_f32_16x16x128_f8f6f4 v[24:27], v[16:23], v[160:167], v[218:221], v206, v206 op_sel_hi:[0,0,0]
	s_waitcnt lgkmcnt(0)
	v_mfma_scale_f32_16x16x128_f8f6f4 v[12:15], v[0:7], v[168:175], v[222:225], v206, v206 op_sel_hi:[0,0,0]
	v_mfma_scale_f32_16x16x128_f8f6f4 v[8:11], v[16:23], v[168:175], v[226:229], v206, v206 op_sel_hi:[0,0,0]
	s_setprio 0
	s_setprio 1
	v_mfma_scale_f32_16x16x128_f8f6f4 v[72:75], v[112:119], v[32:39], v[72:75], v206, v206 op_sel_hi:[0,0,0]
	v_mfma_scale_f32_16x16x128_f8f6f4 v[60:63], v[144:151], v[32:39], v[60:63], v206, v206 op_sel_hi:[0,0,0]
	v_mfma_scale_f32_16x16x128_f8f6f4 v[36:39], v[112:119], v[152:159], v[230:233], v206, v206 op_sel_hi:[0,0,0]
	v_mfma_scale_f32_16x16x128_f8f6f4 v[32:35], v[144:151], v[152:159], v[234:237], v206, v206 op_sel_hi:[0,0,0]
	v_mfma_scale_f32_16x16x128_f8f6f4 v[20:23], v[112:119], v[160:167], v[238:241], v206, v206 op_sel_hi:[0,0,0]
	v_mfma_scale_f32_16x16x128_f8f6f4 v[16:19], v[144:151], v[160:167], v[242:245], v206, v206 op_sel_hi:[0,0,0]
	v_mfma_scale_f32_16x16x128_f8f6f4 v[4:7], v[112:119], v[168:175], v[246:249], v206, v206 op_sel_hi:[0,0,0]
	v_mfma_scale_f32_16x16x128_f8f6f4 v[0:3], v[144:151], v[168:175], v[250:253], v206, v206 op_sel_hi:[0,0,0]
	s_setprio 0
	s_barrier
	s_add_i32 s58, s58, 2
	s_add_u32 s56, s56, 0x100
	s_addc_u32 s57, s57, 0
	s_cmp_gt_u32 s58, 5
	s_mov_b64 s[26:27], s[22:23]
	s_cbranch_scc0 .LBB0_2303
	s_and_b64 vcc, exec, s[4:5]
	s_cbranch_vccz .LBB0_2306
	s_barrier
